# nt streaming hint extended to other read-once / write-once streams: P6 row loads, P4 chunk and state-snapshot loads, P0b weight loads, P10 residual-row loads, SSD-scan snapshot stores
# speedup vs baseline: 1.0260x; 1.0114x over previous
.LBB0_82:
	s_mul_hi_i32 s6, s35, 0xb81702e1
	s_add_i32 s6, s6, s35
	s_lshr_b32 s7, s6, 31
	s_ashr_i32 s6, s6, 6
	s_add_i32 s6, s6, s7
	s_mul_i32 s7, s6, 0xffffe9c0
	v_add_u32_e32 v75, s7, v74
	v_add_u32_e32 v68, 32, v75
	v_cmp_gt_i32_e32 vcc, s3, v68
	s_and_saveexec_b64 s[24:25], vcc
	s_cbranch_execz .LBB0_81
	v_ashrrev_i32_e32 v69, 31, v68
	v_lshlrev_b64 v[54:55], 2, v[68:69]
	v_lshl_add_u32 v70, s6, 9, v67
	v_lshl_add_u64 v[50:51], s[22:23], 0, v[54:55]
	v_mad_i64_i32 v[6:7], s[8:9], v70, s4, v[50:51]
	v_or_b32_e32 v2, 1, v70
	v_mad_i64_i32 v[8:9], s[8:9], v2, s4, v[50:51]
	global_load_dwordx4 v[10:13], v[6:7], off nt
	global_load_dwordx4 v[2:5], v[8:9], off nt
	v_or_b32_e32 v6, 2, v70
	v_mad_i64_i32 v[6:7], s[8:9], v6, s4, v[50:51]
	v_or_b32_e32 v8, 3, v70
	v_mad_i64_i32 v[8:9], s[8:9], v8, s4, v[50:51]
	global_load_dwordx4 v[34:37], v[6:7], off nt
	global_load_dwordx4 v[18:21], v[8:9], off nt
	v_or_b32_e32 v6, 4, v70
	v_mad_i64_i32 v[14:15], s[8:9], v6, s4, v[50:51]
	v_or_b32_e32 v6, 5, v70
	v_mad_i64_i32 v[16:17], s[8:9], v6, s4, v[50:51]
	global_load_dwordx4 v[22:25], v[14:15], off nt
	global_load_dwordx4 v[6:9], v[16:17], off nt
	v_or_b32_e32 v14, 6, v70
	v_mad_i64_i32 v[14:15], s[8:9], v14, s4, v[50:51]
	v_or_b32_e32 v16, 7, v70
	v_mad_i64_i32 v[16:17], s[8:9], v16, s4, v[50:51]
	global_load_dwordx4 v[42:45], v[14:15], off nt
	global_load_dwordx4 v[26:29], v[16:17], off nt
	v_or_b32_e32 v14, 8, v70
	v_mad_i64_i32 v[38:39], s[8:9], v14, s4, v[50:51]
	v_or_b32_e32 v14, 9, v70
	v_mad_i64_i32 v[40:41], s[8:9], v14, s4, v[50:51]
	global_load_dwordx4 v[30:33], v[38:39], off nt
	global_load_dwordx4 v[14:17], v[40:41], off nt
	v_or_b32_e32 v38, 10, v70
	v_mad_i64_i32 v[52:53], s[8:9], v38, s4, v[50:51]
	v_or_b32_e32 v38, 11, v70
	v_mad_i64_i32 v[56:57], s[8:9], v38, s4, v[50:51]
	global_load_dwordx4 v[46:49], v[52:53], off nt
	global_load_dwordx4 v[38:41], v[56:57], off nt
	v_or_b32_e32 v52, 12, v70
	v_mad_i64_i32 v[56:57], s[8:9], v52, s4, v[50:51]
	v_or_b32_e32 v52, 13, v70
	v_mad_i64_i32 v[62:63], s[8:9], v52, s4, v[50:51]
	v_or_b32_e32 v52, 14, v70
	v_mad_i64_i32 v[72:73], s[8:9], v52, s4, v[50:51]
	v_or_b32_e32 v52, 15, v70
	v_mad_i64_i32 v[80:81], s[8:9], v52, s4, v[50:51]
	global_load_dwordx4 v[58:61], v[56:57], off nt
	global_load_dwordx4 v[50:53], v[62:63], off nt
	v_lshl_add_u64 v[82:83], s[18:19], 0, v[54:55]
	global_load_dwordx4 v[62:65], v[72:73], off nt
	global_load_dwordx4 v[54:57], v[80:81], off nt
	global_load_dword v79, v[82:83], off sc1
	global_load_dword v78, v[82:83], off offset:4 sc1
	global_load_dword v77, v[82:83], off offset:8 sc1
	global_load_dword v69, v[82:83], off offset:12 sc1
	s_mulk_i32 s6, 0x59
	s_sub_i32 s8, s35, s6
	v_lshl_or_b32 v76, s8, 6, v1
	v_cmp_lt_i32_e64 s[6:7], s5, v68
	v_mov_b32_e32 v72, v76
	s_and_saveexec_b64 s[8:9], s[6:7]
	s_cbranch_execz .LBB0_87
	v_cmp_gt_u32_e32 vcc, s30, v68
	v_mov_b32_e32 v72, v75
	s_and_saveexec_b64 s[10:11], vcc
	v_add_u32_e32 v72, 0xc00, v76
	s_or_b64 exec, exec, s[10:11]

.LBB0_361:
	v_mov_b32_e32 v130, s28
	ds_bpermute_b32 v134, v130, v131
	v_lshl_add_u64 v[132:133], v[172:173], 0, s[62:63]
	s_waitcnt lgkmcnt(0)
	v_sub_f32_e32 v130, v134, v131
	v_mul_f32_e32 v130, 0x3fb8aa3b, v130
	v_exp_f32_e32 v135, v130
	v_lshlrev_b64 v[130:131], 14, v[132:133]
	v_lshl_add_u64 v[130:131], v[174:175], 0, v[130:131]
	v_add_co_u32_e32 v136, vcc, s33, v130
	v_mul_f32_e32 v132, v170, v135
	ds_write_b32 v179, v132
	v_cvt_pk_bf16_f32 v132, v114, v115
	v_cvt_pk_bf16_f32 v133, v116, v117
	global_store_dwordx2 v[130:131], v[132:133], off nt
	v_cvt_pk_bf16_f32 v132, v118, v119
	v_cvt_pk_bf16_f32 v133, v120, v121
	global_store_dwordx2 v[130:131], v[132:133], off offset:512 nt
	v_cvt_pk_bf16_f32 v132, v122, v123
	v_cvt_pk_bf16_f32 v133, v124, v125
	global_store_dwordx2 v[130:131], v[132:133], off offset:1024 nt
	v_cvt_pk_bf16_f32 v132, v126, v127
	v_addc_co_u32_e32 v137, vcc, 0, v131, vcc
	v_cvt_pk_bf16_f32 v133, v128, v129
	global_store_dwordx2 v[130:131], v[132:133], off offset:1536 nt
	v_add_co_u32_e32 v132, vcc, s52, v130
	v_mul_f32_e32 v138, 0x3fb8aa3b, v134
	v_cvt_pk_bf16_f32 v134, v98, v99
	v_cvt_pk_bf16_f32 v135, v100, v101
	s_nop 0
	v_addc_co_u32_e32 v133, vcc, 0, v131, vcc
	global_store_dwordx2 v[132:133], v[134:135], off offset:-4096 nt
	v_cvt_pk_bf16_f32 v134, v102, v103
	v_cvt_pk_bf16_f32 v135, v104, v105
	global_store_dwordx2 v[136:137], v[134:135], off offset:512 nt
	v_cvt_pk_bf16_f32 v134, v106, v107
	v_cvt_pk_bf16_f32 v135, v108, v109
	global_store_dwordx2 v[136:137], v[134:135], off offset:1024 nt
	v_cvt_pk_bf16_f32 v134, v110, v111
	v_cvt_pk_bf16_f32 v135, v112, v113
	global_store_dwordx2 v[136:137], v[134:135], off offset:1536 nt
	v_cvt_pk_bf16_f32 v134, v82, v83
	v_cvt_pk_bf16_f32 v135, v84, v85
	global_store_dwordx2 v[130:131], v[134:135], off offset:2048 nt
	v_cvt_pk_bf16_f32 v134, v86, v87
	v_cvt_pk_bf16_f32 v135, v88, v89
	global_store_dwordx2 v[130:131], v[134:135], off offset:2560 nt
	v_cvt_pk_bf16_f32 v134, v90, v91
	v_cvt_pk_bf16_f32 v135, v92, v93
	global_store_dwordx2 v[130:131], v[134:135], off offset:3072 nt
	v_cvt_pk_bf16_f32 v134, v94, v95
	v_cvt_pk_bf16_f32 v135, v96, v97
	global_store_dwordx2 v[130:131], v[134:135], off offset:3584 nt
	v_cvt_pk_bf16_f32 v134, v66, v67
	v_cvt_pk_bf16_f32 v135, v68, v69
	global_store_dwordx2 v[136:137], v[134:135], off offset:2048 nt
	v_cvt_pk_bf16_f32 v134, v70, v71
	v_cvt_pk_bf16_f32 v135, v72, v73
	global_store_dwordx2 v[136:137], v[134:135], off offset:2560 nt
	v_cvt_pk_bf16_f32 v134, v74, v75
	v_cvt_pk_bf16_f32 v135, v76, v77
	global_store_dwordx2 v[136:137], v[134:135], off offset:3072 nt
	v_cvt_pk_bf16_f32 v134, v78, v79
	v_cvt_pk_bf16_f32 v135, v80, v81
	v_add_co_u32_e32 v130, vcc, s5, v130
	global_store_dwordx2 v[136:137], v[134:135], off offset:3584 nt
	v_cvt_pk_bf16_f32 v134, v50, v51
	v_cvt_pk_bf16_f32 v135, v52, v53
	s_nop 0
	v_addc_co_u32_e32 v131, vcc, 0, v131, vcc
	global_store_dwordx2 v[130:131], v[134:135], off nt
	v_cvt_pk_bf16_f32 v134, v54, v55
	v_cvt_pk_bf16_f32 v135, v56, v57
	global_store_dwordx2 v[130:131], v[134:135], off offset:512 nt
	v_cvt_pk_bf16_f32 v134, v58, v59
	v_cvt_pk_bf16_f32 v135, v60, v61
	global_store_dwordx2 v[130:131], v[134:135], off offset:1024 nt
	v_cvt_pk_bf16_f32 v134, v62, v63
	v_cvt_pk_bf16_f32 v135, v64, v65
	global_store_dwordx2 v[130:131], v[134:135], off offset:1536 nt
	v_cvt_pk_bf16_f32 v134, v34, v35
	v_cvt_pk_bf16_f32 v135, v36, v37
	global_store_dwordx2 v[132:133], v[134:135], off nt
	v_cvt_pk_bf16_f32 v134, v38, v39
	v_cvt_pk_bf16_f32 v135, v40, v41
	global_store_dwordx2 v[132:133], v[134:135], off offset:512 nt
	v_cvt_pk_bf16_f32 v134, v42, v43
	v_cvt_pk_bf16_f32 v135, v44, v45
	global_store_dwordx2 v[132:133], v[134:135], off offset:1024 nt
	v_cvt_pk_bf16_f32 v134, v46, v47
	v_cvt_pk_bf16_f32 v135, v48, v49
	global_store_dwordx2 v[132:133], v[134:135], off offset:1536 nt
	v_cvt_pk_bf16_f32 v134, v18, v19
	v_cvt_pk_bf16_f32 v135, v20, v21
	global_store_dwordx2 v[130:131], v[134:135], off offset:2048 nt
	v_cvt_pk_bf16_f32 v134, v22, v23
	v_cvt_pk_bf16_f32 v135, v24, v25
	global_store_dwordx2 v[130:131], v[134:135], off offset:2560 nt
	v_cvt_pk_bf16_f32 v134, v26, v27
	v_cvt_pk_bf16_f32 v135, v28, v29
	global_store_dwordx2 v[130:131], v[134:135], off offset:3072 nt
	v_cvt_pk_bf16_f32 v134, v30, v31
	v_cvt_pk_bf16_f32 v135, v32, v33
	global_store_dwordx2 v[130:131], v[134:135], off offset:3584 nt
	v_cvt_pk_bf16_f32 v130, v2, v3
	v_cvt_pk_bf16_f32 v131, v4, v5
	global_store_dwordx2 v[132:133], v[130:131], off offset:2048 nt
	v_cvt_pk_bf16_f32 v130, v6, v7
	v_cvt_pk_bf16_f32 v131, v8, v9
	global_store_dwordx2 v[132:133], v[130:131], off offset:2560 nt
	v_cvt_pk_bf16_f32 v130, v10, v11
	v_cvt_pk_bf16_f32 v131, v12, v13
	global_store_dwordx2 v[132:133], v[130:131], off offset:3072 nt
	v_exp_f32_e32 v130, v138
	v_cvt_pk_bf16_f32 v134, v14, v15
	v_cvt_pk_bf16_f32 v135, v16, v17
	global_store_dwordx2 v[132:133], v[134:135], off offset:3584 nt
	v_pk_mul_f32 v[128:129], v[128:129], v[130:131] op_sel_hi:[1,0]
	v_pk_mul_f32 v[126:127], v[126:127], v[130:131] op_sel_hi:[1,0]
	v_pk_mul_f32 v[124:125], v[124:125], v[130:131] op_sel_hi:[1,0]
	v_pk_mul_f32 v[122:123], v[122:123], v[130:131] op_sel_hi:[1,0]
	v_pk_mul_f32 v[120:121], v[120:121], v[130:131] op_sel_hi:[1,0]
	v_pk_mul_f32 v[118:119], v[118:119], v[130:131] op_sel_hi:[1,0]
	v_pk_mul_f32 v[116:117], v[116:117], v[130:131] op_sel_hi:[1,0]
	v_pk_mul_f32 v[114:115], v[114:115], v[130:131] op_sel_hi:[1,0]
	v_pk_mul_f32 v[112:113], v[112:113], v[130:131] op_sel_hi:[1,0]
	v_pk_mul_f32 v[110:111], v[110:111], v[130:131] op_sel_hi:[1,0]
	v_pk_mul_f32 v[108:109], v[108:109], v[130:131] op_sel_hi:[1,0]
	v_pk_mul_f32 v[106:107], v[106:107], v[130:131] op_sel_hi:[1,0]
	v_pk_mul_f32 v[104:105], v[104:105], v[130:131] op_sel_hi:[1,0]
	v_pk_mul_f32 v[102:103], v[102:103], v[130:131] op_sel_hi:[1,0]
	v_pk_mul_f32 v[100:101], v[100:101], v[130:131] op_sel_hi:[1,0]
	v_pk_mul_f32 v[98:99], v[98:99], v[130:131] op_sel_hi:[1,0]
	v_pk_mul_f32 v[96:97], v[96:97], v[130:131] op_sel_hi:[1,0]
	v_pk_mul_f32 v[94:95], v[94:95], v[130:131] op_sel_hi:[1,0]
	v_pk_mul_f32 v[92:93], v[92:93], v[130:131] op_sel_hi:[1,0]
	v_pk_mul_f32 v[90:91], v[90:91], v[130:131] op_sel_hi:[1,0]
	v_pk_mul_f32 v[88:89], v[88:89], v[130:131] op_sel_hi:[1,0]
	v_pk_mul_f32 v[86:87], v[86:87], v[130:131] op_sel_hi:[1,0]
	v_pk_mul_f32 v[84:85], v[84:85], v[130:131] op_sel_hi:[1,0]
	v_pk_mul_f32 v[82:83], v[82:83], v[130:131] op_sel_hi:[1,0]
	v_pk_mul_f32 v[80:81], v[80:81], v[130:131] op_sel_hi:[1,0]
	v_pk_mul_f32 v[78:79], v[78:79], v[130:131] op_sel_hi:[1,0]
	v_pk_mul_f32 v[76:77], v[76:77], v[130:131] op_sel_hi:[1,0]
	v_pk_mul_f32 v[74:75], v[74:75], v[130:131] op_sel_hi:[1,0]
	v_pk_mul_f32 v[72:73], v[72:73], v[130:131] op_sel_hi:[1,0]
	v_pk_mul_f32 v[70:71], v[70:71], v[130:131] op_sel_hi:[1,0]
	v_pk_mul_f32 v[68:69], v[68:69], v[130:131] op_sel_hi:[1,0]
	v_pk_mul_f32 v[66:67], v[66:67], v[130:131] op_sel_hi:[1,0]
	v_pk_mul_f32 v[64:65], v[64:65], v[130:131] op_sel_hi:[1,0]
	v_pk_mul_f32 v[62:63], v[62:63], v[130:131] op_sel_hi:[1,0]
	v_pk_mul_f32 v[60:61], v[60:61], v[130:131] op_sel_hi:[1,0]
	v_pk_mul_f32 v[58:59], v[58:59], v[130:131] op_sel_hi:[1,0]
	v_pk_mul_f32 v[56:57], v[56:57], v[130:131] op_sel_hi:[1,0]
	v_pk_mul_f32 v[54:55], v[54:55], v[130:131] op_sel_hi:[1,0]
	v_pk_mul_f32 v[52:53], v[52:53], v[130:131] op_sel_hi:[1,0]
	v_pk_mul_f32 v[50:51], v[50:51], v[130:131] op_sel_hi:[1,0]
	v_pk_mul_f32 v[48:49], v[48:49], v[130:131] op_sel_hi:[1,0]
	v_pk_mul_f32 v[46:47], v[46:47], v[130:131] op_sel_hi:[1,0]
	v_pk_mul_f32 v[44:45], v[44:45], v[130:131] op_sel_hi:[1,0]
	v_pk_mul_f32 v[42:43], v[42:43], v[130:131] op_sel_hi:[1,0]
	v_pk_mul_f32 v[40:41], v[40:41], v[130:131] op_sel_hi:[1,0]
	v_pk_mul_f32 v[38:39], v[38:39], v[130:131] op_sel_hi:[1,0]
	v_pk_mul_f32 v[36:37], v[36:37], v[130:131] op_sel_hi:[1,0]
	v_pk_mul_f32 v[34:35], v[34:35], v[130:131] op_sel_hi:[1,0]
	v_pk_mul_f32 v[32:33], v[32:33], v[130:131] op_sel_hi:[1,0]
	v_pk_mul_f32 v[30:31], v[30:31], v[130:131] op_sel_hi:[1,0]
	v_pk_mul_f32 v[28:29], v[28:29], v[130:131] op_sel_hi:[1,0]
	v_pk_mul_f32 v[26:27], v[26:27], v[130:131] op_sel_hi:[1,0]
	v_pk_mul_f32 v[24:25], v[24:25], v[130:131] op_sel_hi:[1,0]
	v_pk_mul_f32 v[22:23], v[22:23], v[130:131] op_sel_hi:[1,0]
	v_pk_mul_f32 v[20:21], v[20:21], v[130:131] op_sel_hi:[1,0]
	v_pk_mul_f32 v[18:19], v[18:19], v[130:131] op_sel_hi:[1,0]
	v_pk_mul_f32 v[16:17], v[16:17], v[130:131] op_sel_hi:[1,0]
	v_pk_mul_f32 v[14:15], v[14:15], v[130:131] op_sel_hi:[1,0]
	v_pk_mul_f32 v[12:13], v[12:13], v[130:131] op_sel_hi:[1,0]
	v_pk_mul_f32 v[10:11], v[10:11], v[130:131] op_sel_hi:[1,0]
	v_pk_mul_f32 v[8:9], v[8:9], v[130:131] op_sel_hi:[1,0]
	v_pk_mul_f32 v[6:7], v[6:7], v[130:131] op_sel_hi:[1,0]
	v_pk_mul_f32 v[4:5], v[4:5], v[130:131] op_sel_hi:[1,0]
	v_pk_mul_f32 v[2:3], v[2:3], v[130:131] op_sel_hi:[1,0]
	s_waitcnt lgkmcnt(0)
	s_barrier
	ds_read_b128 v[130:133], v214
	ds_read_b128 v[134:137], v214 offset:16
	ds_read_b64_tr_b16 v[154:155], v192 offset:0
	ds_read_b64_tr_b16 v[156:157], v192 offset:0x800
	ds_read_b64_tr_b16 v[158:159], v192 offset:0x200
	ds_read_b64_tr_b16 v[160:161], v192 offset:0xa00
	ds_read_b64_tr_b16 v[138:139], v190
	ds_read_b64_tr_b16 v[140:141], v190 offset:2048
	ds_read_b64_tr_b16 v[142:143], v193
	ds_read_b64_tr_b16 v[144:145], v193 offset:2048
	ds_read_b64_tr_b16 v[146:147], v194
	ds_read_b64_tr_b16 v[148:149], v194 offset:2048
	ds_read_b64_tr_b16 v[150:151], v195
	ds_read_b64_tr_b16 v[152:153], v195 offset:2048
	s_waitcnt lgkmcnt(0)
	s_nop 0
	v_lshlrev_b32_e32 v162, 16, v154
	v_and_b32_e32 v154, 0xffff0000, v154
	s_waitcnt lgkmcnt(1)
	v_mul_f32_e32 v162, v130, v162
	v_mul_f32_e32 v154, v131, v154
	v_cvt_pk_bf16_f32 v154, v162, v154
	v_lshlrev_b32_e32 v162, 16, v155
	v_and_b32_e32 v155, 0xffff0000, v155
	v_mul_f32_e32 v162, v132, v162
	v_mul_f32_e32 v155, v133, v155
	v_cvt_pk_bf16_f32 v155, v162, v155
	v_lshlrev_b32_e32 v162, 16, v156
	v_and_b32_e32 v156, 0xffff0000, v156
	s_waitcnt lgkmcnt(0)
	v_mul_f32_e32 v162, v134, v162
	v_mul_f32_e32 v156, v135, v156
	v_cvt_pk_bf16_f32 v156, v162, v156
	v_lshlrev_b32_e32 v162, 16, v157
	v_and_b32_e32 v157, 0xffff0000, v157
	v_mul_f32_e32 v162, v136, v162
	v_mul_f32_e32 v157, v137, v157
	v_cvt_pk_bf16_f32 v157, v162, v157
	v_lshlrev_b32_e32 v162, 16, v158
	v_and_b32_e32 v158, 0xffff0000, v158
	v_mul_f32_e32 v130, v130, v162
	v_mul_f32_e32 v131, v131, v158
	v_cvt_pk_bf16_f32 v130, v130, v131
	v_lshlrev_b32_e32 v131, 16, v159
	v_mul_f32_e32 v131, v132, v131
	v_and_b32_e32 v132, 0xffff0000, v159
	v_mul_f32_e32 v132, v133, v132
	v_cvt_pk_bf16_f32 v131, v131, v132
	v_lshlrev_b32_e32 v132, 16, v160
	v_and_b32_e32 v133, 0xffff0000, v160
	v_mul_f32_e32 v132, v134, v132
	v_mul_f32_e32 v133, v135, v133
	v_cvt_pk_bf16_f32 v132, v132, v133
	v_lshlrev_b32_e32 v133, 16, v161
	v_and_b32_e32 v134, 0xffff0000, v161
	v_mul_f32_e32 v133, v136, v133
	v_mul_f32_e32 v134, v137, v134
	v_mfma_f32_32x32x16_bf16 v[114:129], v[138:141], v[154:157], v[114:129]
	v_cvt_pk_bf16_f32 v133, v133, v134
	s_nop 0
	v_mfma_f32_32x32x16_bf16 v[98:113], v[138:141], v[130:133], v[98:113]
	ds_read_b128 v[134:137], v214 offset:64
	ds_read_b128 v[138:141], v214 offset:80
	ds_read_b64_tr_b16 v[162:163], v197 offset:0
	ds_read_b64_tr_b16 v[164:165], v197 offset:0x800
	ds_read_b64_tr_b16 v[166:167], v197 offset:0x200
	ds_read_b64_tr_b16 v[168:169], v197 offset:0xa00
	v_mfma_f32_32x32x16_bf16 v[82:97], v[142:145], v[154:157], v[82:97]
	v_mfma_f32_32x32x16_bf16 v[66:81], v[142:145], v[130:133], v[66:81]
	ds_read_b64_tr_b16 v[142:143], v198
	ds_read_b64_tr_b16 v[144:145], v198 offset:2048
	v_mfma_f32_32x32x16_bf16 v[50:65], v[146:149], v[154:157], v[50:65]
	v_mfma_f32_32x32x16_bf16 v[34:49], v[146:149], v[130:133], v[34:49]
	ds_read_b64_tr_b16 v[146:147], v199
	ds_read_b64_tr_b16 v[148:149], v199 offset:2048
	v_mfma_f32_32x32x16_bf16 v[18:33], v[150:153], v[154:157], v[18:33]
	ds_read_b64_tr_b16 v[154:155], v200
	ds_read_b64_tr_b16 v[156:157], v200 offset:2048
	ds_read_b64_tr_b16 v[158:159], v201
	ds_read_b64_tr_b16 v[160:161], v201 offset:2048
	s_waitcnt lgkmcnt(0)
	v_mfma_f32_32x32x16_bf16 v[2:17], v[150:153], v[130:133], v[2:17]
	v_lshlrev_b32_e32 v130, 16, v162
	v_and_b32_e32 v131, 0xffff0000, v162
	s_waitcnt lgkmcnt(1)
	v_mul_f32_e32 v130, v134, v130
	v_mul_f32_e32 v131, v135, v131
	v_cvt_pk_bf16_f32 v130, v130, v131
	v_lshlrev_b32_e32 v131, 16, v163
	v_and_b32_e32 v132, 0xffff0000, v163
	v_mul_f32_e32 v131, v136, v131
	v_mul_f32_e32 v132, v137, v132
	v_cvt_pk_bf16_f32 v131, v131, v132
	v_lshlrev_b32_e32 v132, 16, v164
	v_and_b32_e32 v133, 0xffff0000, v164
	s_waitcnt lgkmcnt(0)
	v_mul_f32_e32 v132, v138, v132
	v_mul_f32_e32 v133, v139, v133
	v_cvt_pk_bf16_f32 v132, v132, v133
	v_lshlrev_b32_e32 v133, 16, v165
	v_and_b32_e32 v150, 0xffff0000, v165
	v_mul_f32_e32 v133, v140, v133
	v_mul_f32_e32 v150, v141, v150
	v_cvt_pk_bf16_f32 v133, v133, v150
	v_lshlrev_b32_e32 v150, 16, v166
	v_mul_f32_e32 v134, v134, v150
	v_and_b32_e32 v150, 0xffff0000, v166
	v_mul_f32_e32 v135, v135, v150
	v_cvt_pk_bf16_f32 v134, v134, v135
	v_lshlrev_b32_e32 v135, 16, v167
	v_mul_f32_e32 v135, v136, v135
	v_and_b32_e32 v136, 0xffff0000, v167
	v_mul_f32_e32 v136, v137, v136
	v_cvt_pk_bf16_f32 v135, v135, v136
	v_lshlrev_b32_e32 v136, 16, v168
	v_and_b32_e32 v137, 0xffff0000, v168
	v_mul_f32_e32 v136, v138, v136
	v_mul_f32_e32 v137, v139, v137
	v_cvt_pk_bf16_f32 v136, v136, v137
	v_lshlrev_b32_e32 v137, 16, v169
	v_and_b32_e32 v138, 0xffff0000, v169
	v_mul_f32_e32 v137, v140, v137
	v_mul_f32_e32 v138, v141, v138
	v_mfma_f32_32x32x16_bf16 v[114:129], v[142:145], v[130:133], v[114:129]
	v_cvt_pk_bf16_f32 v137, v137, v138
	s_nop 0
	v_mfma_f32_32x32x16_bf16 v[98:113], v[142:145], v[134:137], v[98:113]
	ds_read_b128 v[138:141], v214 offset:128
	ds_read_b128 v[142:145], v214 offset:144
	ds_read_b64_tr_b16 v[162:163], v202 offset:0
	ds_read_b64_tr_b16 v[164:165], v202 offset:0x800
	ds_read_b64_tr_b16 v[166:167], v202 offset:0x200
	ds_read_b64_tr_b16 v[168:169], v202 offset:0xa00
	v_mfma_f32_32x32x16_bf16 v[82:97], v[146:149], v[130:133], v[82:97]
	v_mfma_f32_32x32x16_bf16 v[66:81], v[146:149], v[134:137], v[66:81]
	ds_read_b64_tr_b16 v[146:147], v203
	ds_read_b64_tr_b16 v[148:149], v203 offset:2048
	v_mfma_f32_32x32x16_bf16 v[50:65], v[154:157], v[130:133], v[50:65]
	v_mfma_f32_32x32x16_bf16 v[18:33], v[158:161], v[130:133], v[18:33]
	ds_read_b64_tr_b16 v[130:131], v204
	ds_read_b64_tr_b16 v[132:133], v204 offset:2048
	ds_read_b64_tr_b16 v[150:151], v205
	ds_read_b64_tr_b16 v[152:153], v205 offset:2048
	v_mfma_f32_32x32x16_bf16 v[34:49], v[154:157], v[134:137], v[34:49]
	ds_read_b64_tr_b16 v[154:155], v206
	ds_read_b64_tr_b16 v[156:157], v206 offset:2048
	s_waitcnt lgkmcnt(0)
	v_mfma_f32_32x32x16_bf16 v[2:17], v[158:161], v[134:137], v[2:17]
	v_lshlrev_b32_e32 v134, 16, v162
	v_and_b32_e32 v135, 0xffff0000, v162
	s_waitcnt lgkmcnt(1)
	v_mul_f32_e32 v134, v138, v134
	v_mul_f32_e32 v135, v139, v135
	v_cvt_pk_bf16_f32 v134, v134, v135
	v_lshlrev_b32_e32 v135, 16, v163
	v_and_b32_e32 v136, 0xffff0000, v163
	v_mul_f32_e32 v135, v140, v135
	v_mul_f32_e32 v136, v141, v136
	v_cvt_pk_bf16_f32 v135, v135, v136
	v_lshlrev_b32_e32 v136, 16, v164
	v_and_b32_e32 v137, 0xffff0000, v164
	s_waitcnt lgkmcnt(0)
	v_mul_f32_e32 v136, v142, v136
	v_mul_f32_e32 v137, v143, v137
	v_cvt_pk_bf16_f32 v136, v136, v137
	v_lshlrev_b32_e32 v137, 16, v165
	v_and_b32_e32 v158, 0xffff0000, v165
	v_mul_f32_e32 v137, v144, v137
	v_mul_f32_e32 v158, v145, v158
	v_cvt_pk_bf16_f32 v137, v137, v158
	v_lshlrev_b32_e32 v158, 16, v166
	v_mul_f32_e32 v138, v138, v158
	v_and_b32_e32 v158, 0xffff0000, v166
	v_mul_f32_e32 v139, v139, v158
	v_cvt_pk_bf16_f32 v138, v138, v139
	v_lshlrev_b32_e32 v139, 16, v167
	v_mul_f32_e32 v139, v140, v139
	v_and_b32_e32 v140, 0xffff0000, v167
	v_mul_f32_e32 v140, v141, v140
	v_cvt_pk_bf16_f32 v139, v139, v140
	v_lshlrev_b32_e32 v140, 16, v168
	v_and_b32_e32 v141, 0xffff0000, v168
	v_mul_f32_e32 v140, v142, v140
	v_mul_f32_e32 v141, v143, v141
	v_cvt_pk_bf16_f32 v140, v140, v141
	v_lshlrev_b32_e32 v141, 16, v169
	v_and_b32_e32 v142, 0xffff0000, v169
	v_mul_f32_e32 v141, v144, v141
	v_mul_f32_e32 v142, v145, v142
	v_cvt_pk_bf16_f32 v141, v141, v142
	v_mfma_f32_32x32x16_bf16 v[82:97], v[130:133], v[134:137], v[82:97]
	v_mfma_f32_32x32x16_bf16 v[66:81], v[130:133], v[138:141], v[66:81]
	ds_read_b128 v[130:133], v214 offset:192
	ds_read_b128 v[142:145], v214 offset:208
	ds_read_b64_tr_b16 v[162:163], v207 offset:0
	ds_read_b64_tr_b16 v[164:165], v207 offset:0x800
	ds_read_b64_tr_b16 v[166:167], v207 offset:0x200
	ds_read_b64_tr_b16 v[168:169], v207 offset:0xa00
	v_mfma_f32_32x32x16_bf16 v[114:129], v[146:149], v[134:137], v[114:129]
	v_mfma_f32_32x32x16_bf16 v[98:113], v[146:149], v[138:141], v[98:113]
	ds_read_b64_tr_b16 v[146:147], v208
	ds_read_b64_tr_b16 v[148:149], v208 offset:2048
	v_mfma_f32_32x32x16_bf16 v[50:65], v[150:153], v[134:137], v[50:65]
	v_mfma_f32_32x32x16_bf16 v[18:33], v[154:157], v[134:137], v[18:33]
	ds_read_b64_tr_b16 v[134:135], v209
	ds_read_b64_tr_b16 v[136:137], v209 offset:2048
	v_mfma_f32_32x32x16_bf16 v[34:49], v[150:153], v[138:141], v[34:49]
	ds_read_b64_tr_b16 v[150:151], v210
	ds_read_b64_tr_b16 v[152:153], v210 offset:2048
	ds_read_b64_tr_b16 v[158:159], v211
	ds_read_b64_tr_b16 v[160:161], v211 offset:2048
	s_waitcnt lgkmcnt(0)
	v_mfma_f32_32x32x16_bf16 v[2:17], v[154:157], v[138:141], v[2:17]
	v_lshlrev_b32_e32 v138, 16, v162
	v_and_b32_e32 v139, 0xffff0000, v162
	s_waitcnt lgkmcnt(1)
	v_mul_f32_e32 v138, v130, v138
	v_mul_f32_e32 v139, v131, v139
	v_cvt_pk_bf16_f32 v138, v138, v139
	v_lshlrev_b32_e32 v139, 16, v163
	v_and_b32_e32 v140, 0xffff0000, v163
	v_mul_f32_e32 v139, v132, v139
	v_mul_f32_e32 v140, v133, v140
	v_cvt_pk_bf16_f32 v139, v139, v140
	v_lshlrev_b32_e32 v140, 16, v164
	v_and_b32_e32 v141, 0xffff0000, v164
	s_waitcnt lgkmcnt(0)
	v_mul_f32_e32 v140, v142, v140
	v_mul_f32_e32 v141, v143, v141
	v_cvt_pk_bf16_f32 v140, v140, v141
	v_lshlrev_b32_e32 v141, 16, v165
	v_and_b32_e32 v154, 0xffff0000, v165
	v_mul_f32_e32 v141, v144, v141
	v_mul_f32_e32 v154, v145, v154
	v_cvt_pk_bf16_f32 v141, v141, v154
	v_lshlrev_b32_e32 v154, 16, v166
	v_mul_f32_e32 v130, v130, v154
	v_and_b32_e32 v154, 0xffff0000, v166
	v_mul_f32_e32 v131, v131, v154
	v_cvt_pk_bf16_f32 v130, v130, v131
	v_lshlrev_b32_e32 v131, 16, v167
	v_mul_f32_e32 v131, v132, v131
	v_and_b32_e32 v132, 0xffff0000, v167
	v_mul_f32_e32 v132, v133, v132
	v_cvt_pk_bf16_f32 v131, v131, v132
	v_lshlrev_b32_e32 v132, 16, v168
	v_and_b32_e32 v133, 0xffff0000, v168
	v_mul_f32_e32 v132, v142, v132
	v_mul_f32_e32 v133, v143, v133
	v_cvt_pk_bf16_f32 v132, v132, v133
	v_lshlrev_b32_e32 v133, 16, v169
	v_mul_f32_e32 v133, v144, v133
	v_and_b32_e32 v142, 0xffff0000, v169
	v_mfma_f32_32x32x16_bf16 v[114:129], v[146:149], v[138:141], v[114:129]
	v_mul_f32_e32 v142, v145, v142
	v_cvt_pk_bf16_f32 v133, v133, v142
	s_add_i32 s72, s72, 1
	s_add_i32 s71, s71, -1
	s_cmp_lg_u32 s72, 32
	v_mfma_f32_32x32x16_bf16 v[98:113], v[146:149], v[130:133], v[98:113]
	v_mfma_f32_32x32x16_bf16 v[82:97], v[134:137], v[138:141], v[82:97]
	v_mfma_f32_32x32x16_bf16 v[66:81], v[134:137], v[130:133], v[66:81]
	v_mfma_f32_32x32x16_bf16 v[50:65], v[150:153], v[138:141], v[50:65]
	v_mfma_f32_32x32x16_bf16 v[34:49], v[150:153], v[130:133], v[34:49]
	v_mfma_f32_32x32x16_bf16 v[18:33], v[158:161], v[138:141], v[18:33]
	v_mfma_f32_32x32x16_bf16 v[2:17], v[158:161], v[130:133], v[2:17]
	s_cbranch_scc0 .LBB0_359

.LBB0_630:
	s_or_saveexec_b64 s[6:7], s[6:7]
	s_lshl_b32 s85, s10, 9
	s_xor_b64 exec, exec, s[6:7]
	v_lshl_add_u32 v2, v80, 3, s85
	s_or_b64 exec, exec, s[6:7]
	s_mul_i32 s6, s65, 0xc00
	s_mul_hi_u32 s7, s64, 0xc00
	s_add_i32 s7, s7, s6
	s_mul_i32 s6, s64, 0xc00
	s_add_u32 s68, s48, s6
	s_addc_u32 s69, s49, s7
	v_mov_b64_e32 v[8:9], s[68:69]
	v_mad_i64_i32 v[8:9], s[6:7], v79, s61, v[8:9]
	v_ashrrev_i32_e32 v3, 31, v2
	v_lshl_add_u64 v[2:3], v[2:3], 1, v[8:9]
	global_load_dwordx4 v[50:53], v[2:3], off nt
	v_add_u32_e32 v2, 0x200, v6
	v_mul_hi_i32 v3, v2, s33
	v_lshrrev_b32_e32 v7, 31, v3
	v_ashrrev_i32_e32 v3, 4, v3
	v_add_u32_e32 v77, v3, v7
	v_mul_lo_u32 v3, v77, s52
	v_sub_u32_e32 v78, v2, v3
	v_cmp_lt_i32_e64 s[24:25], 63, v78
	s_and_saveexec_b64 s[6:7], s[24:25]
	s_xor_b64 s[6:7], exec, s[6:7]
	s_cbranch_execz .LBB0_638
	v_cmp_lt_u32_e32 vcc, s53, v78
	v_lshlrev_b32_e32 v3, 3, v78
	s_and_saveexec_b64 s[8:9], vcc
	s_xor_b64 s[8:9], exec, s[8:9]
	v_add_u32_e32 v2, s84, v3
	s_andn2_saveexec_b64 s[8:9], s[8:9]
	v_add_u32_e32 v2, s1, v3
	s_or_b64 exec, exec, s[8:9]
.LBB0_638:
	s_andn2_saveexec_b64 s[6:7], s[6:7]
	v_lshl_add_u32 v2, v78, 3, s85
	s_or_b64 exec, exec, s[6:7]
	v_mov_b64_e32 v[8:9], s[68:69]
	v_mad_i64_i32 v[8:9], s[6:7], v77, s61, v[8:9]
	v_ashrrev_i32_e32 v3, 31, v2
	v_lshl_add_u64 v[2:3], v[2:3], 1, v[8:9]
	global_load_dwordx4 v[46:49], v[2:3], off nt
	v_add_u32_e32 v2, 0x400, v6
	v_mul_hi_i32 v3, v2, s33
	v_lshrrev_b32_e32 v7, 31, v3
	v_ashrrev_i32_e32 v3, 4, v3
	v_add_u32_e32 v75, v3, v7
	v_mul_lo_u32 v3, v75, s52
	v_sub_u32_e32 v76, v2, v3
	v_cmp_lt_i32_e64 s[22:23], 63, v76
	s_and_saveexec_b64 s[6:7], s[22:23]
	s_xor_b64 s[6:7], exec, s[6:7]
	s_cbranch_execz .LBB0_646
	v_cmp_lt_u32_e32 vcc, s53, v76
	v_lshlrev_b32_e32 v3, 3, v76
	s_and_saveexec_b64 s[8:9], vcc
	s_xor_b64 s[8:9], exec, s[8:9]
	v_add_u32_e32 v2, s84, v3
	s_andn2_saveexec_b64 s[8:9], s[8:9]
	v_add_u32_e32 v2, s1, v3
	s_or_b64 exec, exec, s[8:9]
.LBB0_646:
	s_andn2_saveexec_b64 s[6:7], s[6:7]
	v_lshl_add_u32 v2, v76, 3, s85
	s_or_b64 exec, exec, s[6:7]
	v_mov_b64_e32 v[8:9], s[68:69]
	v_mad_i64_i32 v[8:9], s[6:7], v75, s61, v[8:9]
	v_ashrrev_i32_e32 v3, 31, v2
	v_lshl_add_u64 v[2:3], v[2:3], 1, v[8:9]
	global_load_dwordx4 v[42:45], v[2:3], off nt
	v_add_u32_e32 v2, 0x600, v6
	v_mul_hi_i32 v3, v2, s33
	v_lshrrev_b32_e32 v7, 31, v3
	v_ashrrev_i32_e32 v3, 4, v3
	v_add_u32_e32 v73, v3, v7
	v_mul_lo_u32 v3, v73, s52
	v_sub_u32_e32 v74, v2, v3
	v_cmp_lt_i32_e64 s[20:21], 63, v74
	s_and_saveexec_b64 s[6:7], s[20:21]
	s_xor_b64 s[6:7], exec, s[6:7]
	s_cbranch_execz .LBB0_654
	v_cmp_lt_u32_e32 vcc, s53, v74
	v_lshlrev_b32_e32 v3, 3, v74
	s_and_saveexec_b64 s[8:9], vcc
	s_xor_b64 s[8:9], exec, s[8:9]
	v_add_u32_e32 v2, s84, v3
	s_andn2_saveexec_b64 s[8:9], s[8:9]
	v_add_u32_e32 v2, s1, v3
	s_or_b64 exec, exec, s[8:9]
.LBB0_654:
	s_andn2_saveexec_b64 s[6:7], s[6:7]
	v_lshl_add_u32 v2, v74, 3, s85
	s_or_b64 exec, exec, s[6:7]
	v_mov_b64_e32 v[8:9], s[68:69]
	v_mad_i64_i32 v[8:9], s[6:7], v73, s61, v[8:9]
	v_ashrrev_i32_e32 v3, 31, v2
	v_lshl_add_u64 v[2:3], v[2:3], 1, v[8:9]
	global_load_dwordx4 v[38:41], v[2:3], off nt
	v_add_u32_e32 v2, 0x800, v6
	v_mul_hi_i32 v3, v2, s33
	v_lshrrev_b32_e32 v7, 31, v3
	v_ashrrev_i32_e32 v3, 4, v3
	v_add_u32_e32 v71, v3, v7
	v_mul_lo_u32 v3, v71, s52
	v_sub_u32_e32 v72, v2, v3
	v_cmp_lt_i32_e64 s[18:19], 63, v72
	s_and_saveexec_b64 s[6:7], s[18:19]
	s_xor_b64 s[6:7], exec, s[6:7]
	s_cbranch_execz .LBB0_662
	v_cmp_lt_u32_e32 vcc, s53, v72
	v_lshlrev_b32_e32 v3, 3, v72
	s_and_saveexec_b64 s[8:9], vcc
	s_xor_b64 s[8:9], exec, s[8:9]
	v_add_u32_e32 v2, s84, v3
	s_andn2_saveexec_b64 s[8:9], s[8:9]
	v_add_u32_e32 v2, s1, v3
	s_or_b64 exec, exec, s[8:9]
.LBB0_662:
	s_andn2_saveexec_b64 s[6:7], s[6:7]
	v_lshl_add_u32 v2, v72, 3, s85
	s_or_b64 exec, exec, s[6:7]
	v_mov_b64_e32 v[8:9], s[68:69]
	v_mad_i64_i32 v[8:9], s[6:7], v71, s61, v[8:9]
	v_ashrrev_i32_e32 v3, 31, v2
	v_lshl_add_u64 v[2:3], v[2:3], 1, v[8:9]
	global_load_dwordx4 v[34:37], v[2:3], off nt
	v_add_u32_e32 v2, 0xa00, v6
	v_mul_hi_i32 v3, v2, s33
	v_lshrrev_b32_e32 v7, 31, v3
	v_ashrrev_i32_e32 v3, 4, v3
	v_add_u32_e32 v69, v3, v7
	v_mul_lo_u32 v3, v69, s52
	v_sub_u32_e32 v70, v2, v3
	v_cmp_lt_i32_e64 s[16:17], 63, v70
	s_and_saveexec_b64 s[6:7], s[16:17]
	s_xor_b64 s[6:7], exec, s[6:7]
	s_cbranch_execz .LBB0_670
	v_cmp_lt_u32_e32 vcc, s53, v70
	v_lshlrev_b32_e32 v3, 3, v70
	s_and_saveexec_b64 s[8:9], vcc
	s_xor_b64 s[8:9], exec, s[8:9]
	v_add_u32_e32 v2, s84, v3
	s_andn2_saveexec_b64 s[8:9], s[8:9]
	v_add_u32_e32 v2, s1, v3
	s_or_b64 exec, exec, s[8:9]
.LBB0_670:
	s_andn2_saveexec_b64 s[6:7], s[6:7]
	v_lshl_add_u32 v2, v70, 3, s85
	s_or_b64 exec, exec, s[6:7]
	v_mov_b64_e32 v[8:9], s[68:69]
	v_mad_i64_i32 v[8:9], s[6:7], v69, s61, v[8:9]
	v_ashrrev_i32_e32 v3, 31, v2
	v_lshl_add_u64 v[2:3], v[2:3], 1, v[8:9]
	global_load_dwordx4 v[30:33], v[2:3], off nt
	v_add_u32_e32 v2, 0xc00, v6
	v_mul_hi_i32 v3, v2, s33
	v_lshrrev_b32_e32 v7, 31, v3
	v_ashrrev_i32_e32 v3, 4, v3
	v_add_u32_e32 v67, v3, v7
	v_mul_lo_u32 v3, v67, s52
	v_sub_u32_e32 v68, v2, v3
	v_cmp_lt_i32_e64 s[14:15], 63, v68
	s_and_saveexec_b64 s[6:7], s[14:15]
	s_xor_b64 s[6:7], exec, s[6:7]
	s_cbranch_execz .LBB0_678
	v_cmp_lt_u32_e32 vcc, s53, v68
	v_lshlrev_b32_e32 v3, 3, v68
	s_and_saveexec_b64 s[8:9], vcc
	s_xor_b64 s[8:9], exec, s[8:9]
	v_add_u32_e32 v2, s84, v3
	s_andn2_saveexec_b64 s[8:9], s[8:9]
	v_add_u32_e32 v2, s1, v3
	s_or_b64 exec, exec, s[8:9]
.LBB0_678:
	s_andn2_saveexec_b64 s[6:7], s[6:7]
	v_lshl_add_u32 v2, v68, 3, s85
	s_or_b64 exec, exec, s[6:7]
	v_mov_b64_e32 v[8:9], s[68:69]
	v_mad_i64_i32 v[8:9], s[6:7], v67, s61, v[8:9]
	v_ashrrev_i32_e32 v3, 31, v2
	v_lshl_add_u64 v[2:3], v[2:3], 1, v[8:9]
	global_load_dwordx4 v[26:29], v[2:3], off nt
	v_add_u32_e32 v2, 0xe00, v6
	v_mul_hi_i32 v3, v2, s33
	v_lshrrev_b32_e32 v7, 31, v3
	v_ashrrev_i32_e32 v3, 4, v3
	v_add_u32_e32 v65, v3, v7
	v_mul_lo_u32 v3, v65, s52
	v_sub_u32_e32 v66, v2, v3
	v_cmp_lt_i32_e64 s[12:13], 63, v66
	s_and_saveexec_b64 s[6:7], s[12:13]
	s_xor_b64 s[6:7], exec, s[6:7]
	s_cbranch_execz .LBB0_686
	v_cmp_lt_u32_e32 vcc, s53, v66
	v_lshlrev_b32_e32 v3, 3, v66
	s_and_saveexec_b64 s[8:9], vcc
	s_xor_b64 s[8:9], exec, s[8:9]
	v_add_u32_e32 v2, s84, v3
	s_andn2_saveexec_b64 s[8:9], s[8:9]
	v_add_u32_e32 v2, s1, v3
	s_or_b64 exec, exec, s[8:9]
.LBB0_686:
	s_andn2_saveexec_b64 s[6:7], s[6:7]
	v_lshl_add_u32 v2, v66, 3, s85
	s_or_b64 exec, exec, s[6:7]
	v_mov_b64_e32 v[8:9], s[68:69]
	v_mad_i64_i32 v[8:9], s[6:7], v65, s61, v[8:9]
	v_ashrrev_i32_e32 v3, 31, v2
	v_lshl_add_u64 v[2:3], v[2:3], 1, v[8:9]
	global_load_dwordx4 v[22:25], v[2:3], off nt
	v_add_u32_e32 v2, 0x1000, v6
	v_mul_hi_i32 v3, v2, s33
	v_lshrrev_b32_e32 v7, 31, v3
	v_ashrrev_i32_e32 v3, 4, v3
	v_add_u32_e32 v63, v3, v7
	v_mul_lo_u32 v3, v63, s52
	v_sub_u32_e32 v64, v2, v3
	v_cmp_lt_i32_e64 s[10:11], 63, v64
	s_and_saveexec_b64 s[6:7], s[10:11]
	s_xor_b64 s[6:7], exec, s[6:7]
	s_cbranch_execz .LBB0_694
	v_cmp_lt_u32_e32 vcc, s53, v64
	v_lshlrev_b32_e32 v3, 3, v64
	s_and_saveexec_b64 s[8:9], vcc
	s_xor_b64 s[8:9], exec, s[8:9]
	v_add_u32_e32 v2, s84, v3
	s_andn2_saveexec_b64 s[8:9], s[8:9]
	v_add_u32_e32 v2, s1, v3
	s_or_b64 exec, exec, s[8:9]
.LBB0_694:
	s_andn2_saveexec_b64 s[6:7], s[6:7]
	v_lshl_add_u32 v2, v64, 3, s85
	s_or_b64 exec, exec, s[6:7]
	v_mov_b64_e32 v[8:9], s[68:69]
	v_mad_i64_i32 v[8:9], s[6:7], v63, s61, v[8:9]
	v_ashrrev_i32_e32 v3, 31, v2
	v_lshl_add_u64 v[2:3], v[2:3], 1, v[8:9]
	global_load_dwordx4 v[18:21], v[2:3], off nt
	v_add_u32_e32 v2, 0x1200, v6
	v_mul_hi_i32 v3, v2, s33
	v_lshrrev_b32_e32 v7, 31, v3
	v_ashrrev_i32_e32 v3, 4, v3
	v_add_u32_e32 v61, v3, v7
	v_mul_lo_u32 v3, v61, s52
	v_sub_u32_e32 v62, v2, v3
	v_cmp_lt_i32_e64 s[8:9], 63, v62
	s_and_saveexec_b64 s[6:7], s[8:9]
	s_xor_b64 s[6:7], exec, s[6:7]
	s_cbranch_execz .LBB0_702
	v_cmp_lt_u32_e32 vcc, s53, v62
	v_lshlrev_b32_e32 v3, 3, v62
	s_and_saveexec_b64 s[28:29], vcc
	s_xor_b64 s[28:29], exec, s[28:29]
	v_add_u32_e32 v2, s84, v3
	s_andn2_saveexec_b64 s[28:29], s[28:29]
	v_add_u32_e32 v2, s1, v3
	s_or_b64 exec, exec, s[28:29]
.LBB0_702:
	s_andn2_saveexec_b64 s[6:7], s[6:7]
	v_lshl_add_u32 v2, v62, 3, s85
	s_or_b64 exec, exec, s[6:7]
	v_mov_b64_e32 v[8:9], s[68:69]
	v_mad_i64_i32 v[8:9], s[6:7], v61, s61, v[8:9]
	v_ashrrev_i32_e32 v3, 31, v2
	v_lshl_add_u64 v[2:3], v[2:3], 1, v[8:9]
	global_load_dwordx4 v[14:17], v[2:3], off nt
	v_add_u32_e32 v2, 0x1400, v6
	v_mul_hi_i32 v3, v2, s33
	v_lshrrev_b32_e32 v7, 31, v3
	v_ashrrev_i32_e32 v3, 4, v3
	v_add_u32_e32 v59, v3, v7
	v_mul_lo_u32 v3, v59, s52
	v_sub_u32_e32 v60, v2, v3
	v_cmp_lt_i32_e64 s[6:7], 63, v60
	s_and_saveexec_b64 s[28:29], s[6:7]
	s_xor_b64 s[28:29], exec, s[28:29]
	s_cbranch_execz .LBB0_710
	v_cmp_lt_u32_e32 vcc, s53, v60
	v_lshlrev_b32_e32 v3, 3, v60
	s_and_saveexec_b64 s[54:55], vcc
	s_xor_b64 s[54:55], exec, s[54:55]
	v_add_u32_e32 v2, s84, v3
	s_andn2_saveexec_b64 s[70:71], s[54:55]
	v_add_u32_e32 v2, s1, v3
	s_or_b64 exec, exec, s[70:71]
.LBB0_710:
	s_andn2_saveexec_b64 s[28:29], s[28:29]
	v_lshl_add_u32 v2, v60, 3, s85
	s_or_b64 exec, exec, s[28:29]
	v_mov_b64_e32 v[8:9], s[68:69]
	v_mad_i64_i32 v[8:9], s[28:29], v59, s61, v[8:9]
	v_ashrrev_i32_e32 v3, 31, v2
	v_lshl_add_u64 v[2:3], v[2:3], 1, v[8:9]
	global_load_dwordx4 v[10:13], v[2:3], off nt
	v_add_u32_e32 v2, 0x1600, v6
	v_mul_hi_i32 v3, v2, s33
	v_lshrrev_b32_e32 v6, 31, v3
	v_ashrrev_i32_e32 v3, 4, v3
	v_add_u32_e32 v57, v3, v6
	v_mul_lo_u32 v3, v57, s52
	v_sub_u32_e32 v58, v2, v3
	v_cmp_lt_i32_e32 vcc, 63, v58
	s_and_saveexec_b64 s[28:29], vcc
	s_xor_b64 s[70:71], exec, s[28:29]
	s_cbranch_execz .LBB0_718
	v_cmp_lt_u32_e64 s[28:29], s53, v58
	v_lshlrev_b32_e32 v3, 3, v58
	s_and_saveexec_b64 s[54:55], s[28:29]
	s_xor_b64 s[28:29], exec, s[54:55]
	v_add_u32_e32 v2, s84, v3
	s_andn2_saveexec_b64 s[28:29], s[28:29]
	v_add_u32_e32 v2, s1, v3
	s_or_b64 exec, exec, s[28:29]
.LBB0_718:
	s_andn2_saveexec_b64 s[28:29], s[70:71]
	v_lshl_add_u32 v2, v58, 3, s85
	s_or_b64 exec, exec, s[28:29]
	v_mov_b64_e32 v[6:7], s[68:69]
	v_mad_i64_i32 v[6:7], s[28:29], v57, s61, v[6:7]
	v_ashrrev_i32_e32 v3, 31, v2
	v_lshl_add_u64 v[2:3], v[2:3], 1, v[6:7]
	global_load_dwordx4 v[6:9], v[2:3], off nt
	v_lshlrev_b32_e32 v2, 4, v80
	s_and_saveexec_b64 s[28:29], s[26:27]
	s_xor_b64 s[28:29], exec, s[28:29]
	s_cbranch_execz .LBB0_726
	v_lshlrev_b32_e32 v3, 8, v79
	v_lshlrev_b32_e32 v79, 4, v79
	v_cmp_lt_u32_e64 s[26:27], s53, v80
	v_and_b32_e32 v79, 0xf0, v79
	s_and_saveexec_b64 s[54:55], s[26:27]
	s_xor_b64 s[26:27], exec, s[54:55]
	s_cbranch_execz .LBB0_723
	v_add_u32_e32 v2, 0xfffffb00, v2
	v_xor_b32_e32 v2, v2, v79
	v_add3_u32 v2, 0, v3, v2
	s_waitcnt vmcnt(11)
	ds_write_b128 v2, v[50:53] offset:16384

.LBB0_816:
	s_or_b64 exec, exec, s[6:7]
	v_lshlrev_b64 v[2:3], 2, v[148:149]
	s_waitcnt vmcnt(0)
	v_lshl_add_u64 v[6:7], s[36:37], 0, v[2:3]
	global_load_dword v8, v[6:7], off
	v_lshl_add_u64 v[6:7], s[38:39], 0, v[2:3]
	global_load_dword v6, v[6:7], off
	v_lshlrev_b32_e32 v7, 2, v55
	v_add_u32_e32 v9, 0xfc, v7
	v_add_u32_e32 v14, 4, v7
	v_and_b32_e32 v9, 0xfc, v9
	v_and_b32_e32 v14, 0xfc, v14
	v_add_u32_e32 v10, 0xf8, v7
	v_cmp_eq_u32_e32 vcc, 0, v55
	v_add_u32_e32 v17, 8, v7
	v_and_b32_e32 v10, 0xfc, v10
	v_and_b32_e32 v17, 0xfc, v17
	v_add_u32_e32 v11, 0xf0, v7
	v_and_b32_e32 v11, 0xfc, v11
	v_add_u32_e32 v12, 0xe0, v7
	v_and_b32_e32 v12, 0xfc, v12
	v_add_u32_e32 v13, 0xc0, v7
	v_and_b32_e32 v213, 0xffffffc0, v56
	v_lshl_add_u32 v37, v213, 4, s72
	s_lshl_b32 s0, s0, 5
	s_sub_i32 s10, s83, s0
	s_cmp_lg_u32 s10, 0
	s_cselect_b64 s[12:13], -1, 0
	s_ashr_i32 s11, s10, 31
	s_lshl_b64 s[0:1], s[66:67], 23
	s_lshl_b64 s[6:7], s[10:11], 14
	s_add_u32 s0, s34, s0
	s_addc_u32 s1, s35, s1
	v_lshlrev_b32_e32 v18, 4, v56
	s_cmp_eq_u32 s10, 0
	v_and_b32_e32 v146, 0x3f0, v18
	s_waitcnt vmcnt(1)
	v_mul_f32_e32 v8, 0x3fb8aa3b, v8
	v_exp_f32_e32 v8, v8
	s_waitcnt vmcnt(0)
	v_mul_f32_e32 v6, 0x3fb8aa3b, v6
	v_exp_f32_e32 v6, v6
	v_mul_f32_e64 v15, v4, -v8
	ds_bpermute_b32 v9, v9, v15
	v_mul_f32_e64 v16, v5, -v6
	ds_bpermute_b32 v14, v14, v16
	s_waitcnt lgkmcnt(1)
	v_fma_f32 v8, v4, -v8, v9
	v_cndmask_b32_e32 v8, v8, v15, vcc
	s_waitcnt lgkmcnt(0)
	v_fma_f32 v6, v5, -v6, v14
	v_cmp_eq_u32_e32 vcc, 63, v55
	ds_bpermute_b32 v9, v10, v8
	v_add_u32_e32 v14, 16, v7
	v_cndmask_b32_e32 v6, v6, v16, vcc
	ds_bpermute_b32 v10, v17, v6
	v_cmp_gt_u32_e32 vcc, 2, v55
	s_waitcnt lgkmcnt(1)
	v_add_f32_e32 v9, v8, v9
	v_and_b32_e32 v14, 0xfc, v14
	v_cndmask_b32_e32 v8, v9, v8, vcc
	s_waitcnt lgkmcnt(0)
	v_add_f32_e32 v10, v6, v10
	v_cmp_gt_u32_e32 vcc, 62, v55
	ds_bpermute_b32 v9, v11, v8
	v_add_u32_e32 v11, 32, v7
	v_cndmask_b32_e32 v6, v6, v10, vcc
	ds_bpermute_b32 v10, v14, v6
	v_cmp_gt_u32_e32 vcc, 4, v55
	s_waitcnt lgkmcnt(1)
	v_add_f32_e32 v9, v8, v9
	v_and_b32_e32 v11, 0xfc, v11
	v_cndmask_b32_e32 v8, v9, v8, vcc
	s_waitcnt lgkmcnt(0)
	v_add_f32_e32 v10, v6, v10
	v_cmp_gt_u32_e32 vcc, 60, v55
	ds_bpermute_b32 v9, v12, v8
	v_and_b32_e32 v12, 0xfc, v13
	v_cndmask_b32_e32 v6, v6, v10, vcc
	ds_bpermute_b32 v10, v11, v6
	v_cmp_gt_u32_e32 vcc, 8, v55
	s_waitcnt lgkmcnt(1)
	v_add_f32_e32 v9, v8, v9
	v_add_u32_e32 v11, 64, v7
	v_cndmask_b32_e32 v8, v9, v8, vcc
	s_waitcnt lgkmcnt(0)
	v_add_f32_e32 v10, v6, v10
	v_cmp_gt_u32_e32 vcc, 56, v55
	v_and_b32_e32 v11, 0xfc, v11
	ds_bpermute_b32 v9, v12, v8
	v_cndmask_b32_e32 v6, v6, v10, vcc
	ds_bpermute_b32 v10, v11, v6
	v_cmp_gt_u32_e32 vcc, 16, v55
	v_xor_b32_e32 v7, 0x80, v7
	s_waitcnt lgkmcnt(1)
	v_add_f32_e32 v9, v8, v9
	v_cndmask_b32_e32 v8, v9, v8, vcc
	s_waitcnt lgkmcnt(0)
	v_add_f32_e32 v10, v6, v10
	v_cmp_gt_u32_e32 vcc, 48, v55
	v_lshl_add_u32 v12, v55, 4, v37
	s_nop 0
	v_cndmask_b32_e32 v9, v6, v10, vcc
	ds_bpermute_b32 v10, v7, v8
	ds_bpermute_b32 v11, v7, v9
	v_lshl_add_u64 v[6:7], s[40:41], 0, v[2:3]
	v_cmp_gt_u32_e32 vcc, 32, v55
	s_waitcnt lgkmcnt(1)
	v_add_f32_e32 v2, v8, v10
	s_waitcnt lgkmcnt(0)
	v_add_f32_e32 v3, v9, v11
	v_cndmask_b32_e32 v2, v2, v8, vcc
	v_cndmask_b32_e32 v3, v9, v3, vcc
	v_mul_f32_e32 v2, 0x3fb8aa3b, v2
	v_mul_f32_e32 v3, 0x3fb8aa3b, v3
	ds_write_b128 v12, v[2:5]
	s_waitcnt lgkmcnt(0)
	s_barrier
	global_load_dword v124, v[6:7], off
	v_lshlrev_b64 v[2:3], 19, v[148:149]
	v_lshl_add_u64 v[2:3], s[0:1], 0, v[2:3]
	v_lshl_add_u64 v[150:151], v[2:3], 0, s[6:7]
	s_cbranch_scc1 .LBB0_818
	v_lshl_add_u64 v[2:3], v[150:151], 0, v[146:147]
	global_load_dwordx4 v[110:113], v[2:3], off nt
	global_load_dwordx4 v[106:109], v[2:3], off offset:1024 nt
	global_load_dwordx4 v[102:105], v[2:3], off offset:2048 nt
	global_load_dwordx4 v[98:101], v[2:3], off offset:3072 nt
	v_add_co_u32_e32 v2, vcc, 0x1000, v2
	s_nop 1
	v_addc_co_u32_e32 v3, vcc, 0, v3, vcc
	global_load_dwordx4 v[94:97], v[2:3], off nt
	global_load_dwordx4 v[90:93], v[2:3], off offset:1024 nt
	global_load_dwordx4 v[86:89], v[2:3], off offset:2048 nt
	global_load_dwordx4 v[82:85], v[2:3], off offset:3072 nt
.LBB0_818:
	v_lshrrev_b32_e32 v194, 5, v55
	v_and_b32_e32 v195, 31, v56
	v_lshlrev_b32_e32 v214, 4, v194
	v_lshl_add_u32 v57, v195, 8, 0
	v_bitop3_b32 v36, v214, v18, s63 bitop3:0x78
	v_add_u32_e32 v215, v57, v36
	ds_read_b128 v[2:5], v215
	ds_read_b128 v[20:23], v215 offset:16384
	ds_read_b128 v[24:27], v215 offset:8192
	v_and_b32_e32 v65, 0xf0, v18
	s_waitcnt lgkmcnt(1)
	v_mfma_f32_32x32x16_bf16 v[2:17], v[2:5], v[20:23], 0
	v_bitop3_b32 v58, v214, v65, 32 bitop3:0x36
	v_add_u32_e32 v217, v57, v58
	ds_read_b128 v[38:41], v217
	ds_read_b128 v[42:45], v217 offset:16384
	v_bitop3_b32 v60, v214, v65, 64 bitop3:0x36
	v_add_u32_e32 v218, v57, v60
	ds_read_b128 v[46:49], v217 offset:8192
	ds_read_b128 v[50:53], v218
	v_bitop3_b32 v61, v214, v65, s52 bitop3:0x36
	s_waitcnt lgkmcnt(4)
	v_mfma_f32_32x32x16_bf16 v[18:33], v[24:27], v[20:23], 0
	v_add_u32_e32 v219, v57, v61
	v_bitop3_b32 v62, v214, v65, s75 bitop3:0x36
	v_add_u32_e32 v220, v57, v62
	v_lshl_add_u32 v59, v195, 4, v37
	v_bitop3_b32 v63, v214, v65, s77 bitop3:0x36
	v_add_u32_e32 v221, v57, v63
	v_lshlrev_b32_e32 v66, 3, v55
	s_waitcnt lgkmcnt(2)
	v_mfma_f32_32x32x16_bf16 v[2:17], v[38:41], v[42:45], v[2:17]
	v_bitop3_b32 v64, v214, v65, s74 bitop3:0x36
	v_add_u32_e32 v222, v57, v64
	v_and_b32_e32 v67, 24, v66
	s_cmp_lg_u32 s76, -1
	v_bitop3_b32 v65, v214, v65, s73 bitop3:0x36
	s_cselect_b32 s0, s76, 0
	v_add_u32_e32 v223, v57, v65
	s_waitcnt lgkmcnt(1)
	v_mfma_f32_32x32x16_bf16 v[18:33], v[46:49], v[42:45], v[18:33]
	ds_read_b128 v[38:41], v218 offset:16384
	ds_read_b128 v[42:45], v218 offset:8192
	v_lshl_add_u32 v216, v194, 6, v37
	v_lshlrev_b32_e32 v211, 2, v194
	v_cmp_gt_u32_e32 vcc, v211, v195
	v_cmp_lt_u32_e64 s[6:7], v211, v195
	v_cmp_eq_u32_e64 s[8:9], v211, v195
	v_or_b32_e32 v209, 1, v211
	s_waitcnt lgkmcnt(1)
	v_mfma_f32_32x32x16_bf16 v[2:17], v[50:53], v[38:41], v[2:17]
	s_waitcnt vmcnt(0)
	v_cndmask_b32_e64 v126, 0, v124, s[8:9]
	v_cmp_lt_u32_e64 s[8:9], v209, v195
	v_or_b32_e32 v210, 2, v211
	v_or_b32_e32 v208, 3, v211
	v_or_b32_e32 v200, 8, v211
	v_or_b32_e32 v204, 9, v211
	v_or_b32_e32 v206, 10, v211
	s_waitcnt lgkmcnt(0)
	v_mfma_f32_32x32x16_bf16 v[18:33], v[42:45], v[38:41], v[18:33]
	ds_read_b128 v[38:41], v219
	ds_read_b128 v[42:45], v219 offset:16384
	ds_read_b128 v[46:49], v219 offset:8192
	ds_read_b128 v[50:53], v220
	ds_read_b64 v[34:35], v59
	v_or_b32_e32 v207, 11, v211
	v_or_b32_e32 v197, 16, v211
	v_or_b32_e32 v201, 17, v211
	v_or_b32_e32 v202, 18, v211
	s_waitcnt lgkmcnt(3)
	v_mfma_f32_32x32x16_bf16 v[2:17], v[38:41], v[42:45], v[2:17]
	ds_read_b128 v[38:41], v220 offset:16384
	v_or_b32_e32 v205, 19, v211
	v_or_b32_e32 v196, 24, v211
	v_or_b32_e32 v198, 25, v211
	v_or_b32_e32 v199, 26, v211
	v_or_b32_e32 v203, 27, v211
	v_or_b32_e32 v190, 33, v211
	s_waitcnt lgkmcnt(3)
	v_mfma_f32_32x32x16_bf16 v[18:33], v[46:49], v[42:45], v[18:33]
	v_lshlrev_b32_e32 v42, 7, v56
	v_and_b32_e32 v56, 0xffffc000, v42
	ds_read_b128 v[42:45], v220 offset:8192
	v_lshlrev_b32_e32 v46, 4, v55
	v_and_b32_e32 v68, 0xc0, v46
	ds_read_b128 v[46:49], v221
	v_or_b32_e32 v191, 34, v211
	s_waitcnt lgkmcnt(2)
	v_mfma_f32_32x32x16_bf16 v[2:17], v[50:53], v[38:41], v[2:17]
	v_or_b32_e32 v193, 35, v211
	v_or_b32_e32 v184, 40, v211
	v_or_b32_e32 v187, 41, v211
	v_or_b32_e32 v189, 42, v211
	v_or_b32_e32 v192, 43, v211
	v_or_b32_e32 v180, 48, v211
	v_or_b32_e32 v183, 49, v211
	s_waitcnt lgkmcnt(1)
	v_mfma_f32_32x32x16_bf16 v[18:33], v[42:45], v[38:41], v[18:33]
	v_lshlrev_b32_e32 v38, 1, v55
	v_and_b32_e32 v55, 32, v38
	ds_read_b128 v[38:41], v221 offset:16384
	ds_read_b128 v[42:45], v221 offset:8192
	ds_read_b128 v[50:53], v222
	v_or_b32_e32 v185, 50, v211
	v_or_b32_e32 v188, 51, v211
	v_or_b32_e32 v149, 56, v211
	s_waitcnt lgkmcnt(2)
	v_mfma_f32_32x32x16_bf16 v[2:17], v[46:49], v[38:41], v[2:17]
	v_lshlrev_b32_e32 v47, 10, v54
	v_and_b32_e32 v46, 0x100, v66
	v_and_b32_e32 v47, 0x400, v47
	v_or3_b32 v48, v67, v68, v55
	v_or3_b32 v46, v48, v46, v47
	v_add3_u32 v125, s0, v56, v46
	v_or_b32_e32 v181, 57, v211
	s_waitcnt lgkmcnt(1)
	v_mfma_f32_32x32x16_bf16 v[18:33], v[42:45], v[38:41], v[18:33]
	ds_read_b128 v[38:41], v222 offset:16384
	ds_read_b128 v[42:45], v222 offset:8192
	ds_read_b128 v[46:49], v223 offset:16384
	ds_read_b128 v[54:57], v216
	v_or_b32_e32 v182, 58, v211
	v_or_b32_e32 v186, 59, v211
	s_waitcnt lgkmcnt(0)
	v_sub_f32_e32 v37, v34, v54
	v_mfma_f32_32x32x16_bf16 v[2:17], v[50:53], v[38:41], v[2:17]
	v_exp_f32_e32 v37, v37
	ds_read_b128 v[50:53], v223
	ds_read_b128 v[66:69], v223 offset:8192
	ds_read_b128 v[70:73], v216 offset:16
	ds_read_b128 v[74:77], v216 offset:32
	ds_read_b128 v[78:81], v216 offset:48
	v_fma_f32 v37, v56, v37, 0
	v_mfma_f32_32x32x16_bf16 v[18:33], v[42:45], v[38:41], v[18:33]
	v_sub_f32_e32 v38, v35, v55
	v_exp_f32_e32 v38, v38
	v_cndmask_b32_e64 v40, v37, 0, vcc
	v_fmac_f32_e32 v40, v57, v38
	ds_read2_b32 v[38:39], v216 offset0:129 offset1:131
	s_waitcnt lgkmcnt(5)
	v_mfma_f32_32x32x16_bf16 v[2:17], v[50:53], v[46:49], v[2:17]
	v_cndmask_b32_e64 v37, v40, v37, s[6:7]
	s_waitcnt lgkmcnt(0)
	v_sub_f32_e32 v38, v35, v38
	v_exp_f32_e32 v38, v38
	s_nop 7
	v_fma_f32 v37, v2, v37, v126
	v_mfma_f32_32x32x16_bf16 v[18:33], v[66:69], v[46:49], v[18:33]
	v_mul_f32_e32 v2, v39, v38
	v_sub_f32_e32 v38, v35, v71
	v_exp_f32_e32 v38, v38
	s_nop 8
	v_fma_f32 v2, v18, v2, 0
	v_sub_f32_e32 v18, v34, v70
	v_exp_f32_e32 v18, v18
	s_nop 0
	v_fma_f32 v18, v72, v18, 0
	v_cndmask_b32_e64 v40, 0, v18, s[6:7]
	v_fmac_f32_e32 v40, v73, v38
	ds_read2_b32 v[38:39], v216 offset0:133 offset1:135
	v_cndmask_b32_e64 v18, v40, v18, s[8:9]
	v_cmp_eq_u32_e64 s[8:9], v209, v195
	s_nop 1
	v_cndmask_b32_e64 v50, 0, v124, s[8:9]
	v_fmac_f32_e32 v50, v3, v18
	s_waitcnt lgkmcnt(0)
	v_sub_f32_e32 v3, v35, v38
	v_sub_f32_e32 v18, v34, v74
	v_exp_f32_e32 v3, v3
	v_exp_f32_e32 v18, v18
	v_cmp_le_u32_e64 s[8:9], v210, v195
	v_mul_f32_e32 v3, v39, v3
	v_fma_f32 v38, v76, v18, 0
	v_sub_f32_e32 v18, v35, v75
	v_fma_f32 v3, v19, v3, 0
	v_exp_f32_e32 v39, v18
	ds_read2_b32 v[18:19], v216 offset0:137 offset1:139
	v_cndmask_b32_e64 v40, 0, v38, s[8:9]
	v_cmp_lt_u32_e64 s[8:9], v210, v195
	v_fmac_f32_e32 v40, v77, v39
	s_waitcnt lgkmcnt(0)
	v_sub_f32_e32 v18, v35, v18
	v_exp_f32_e32 v18, v18
	v_cndmask_b32_e64 v38, v40, v38, s[8:9]
	v_cmp_eq_u32_e64 s[8:9], v210, v195
	s_nop 1
	v_cndmask_b32_e64 v51, 0, v124, s[8:9]
	v_fmac_f32_e32 v51, v4, v38
	v_mul_f32_e32 v4, v19, v18
	v_fma_f32 v54, v20, v4, 0
	v_sub_f32_e32 v4, v34, v78
	v_exp_f32_e32 v4, v4
	v_sub_f32_e32 v18, v35, v79
	v_exp_f32_e32 v18, v18
	v_cmp_le_u32_e64 s[8:9], v208, v195
	v_fma_f32 v4, v80, v4, 0
	s_nop 0
	v_cndmask_b32_e64 v20, 0, v4, s[8:9]
	v_fmac_f32_e32 v20, v81, v18
	ds_read2_b32 v[18:19], v216 offset0:141 offset1:143
	v_cmp_lt_u32_e64 s[8:9], v208, v195
	ds_read_b128 v[38:41], v216 offset:128
	s_nop 0
	v_cndmask_b32_e64 v4, v20, v4, s[8:9]
	v_cmp_eq_u32_e64 s[8:9], v208, v195
	s_nop 1
	v_cndmask_b32_e64 v52, 0, v124, s[8:9]
	v_fmac_f32_e32 v52, v5, v4
	s_waitcnt lgkmcnt(1)
	v_sub_f32_e32 v4, v35, v18
	v_exp_f32_e32 v4, v4
	v_cmp_le_u32_e64 s[8:9], v200, v195
	v_mul_f32_e32 v4, v19, v4
	v_fma_f32 v55, v21, v4, 0
	ds_read_b128 v[18:21], v216 offset:144
	s_waitcnt lgkmcnt(1)
	v_sub_f32_e32 v4, v34, v38
	v_exp_f32_e32 v4, v4
	ds_read_b128 v[42:45], v216 offset:160
	ds_read_b128 v[46:49], v216 offset:176
	v_fma_f32 v38, v40, v4, 0
	v_sub_f32_e32 v4, v35, v39
	v_exp_f32_e32 v39, v4
	ds_read2_b32 v[4:5], v216 offset0:161 offset1:163
	v_cndmask_b32_e64 v40, 0, v38, s[8:9]
	v_cmp_lt_u32_e64 s[8:9], v200, v195
	v_fmac_f32_e32 v40, v41, v39
	s_waitcnt lgkmcnt(0)
	v_sub_f32_e32 v4, v35, v4
	v_exp_f32_e32 v4, v4
	v_cndmask_b32_e64 v38, v40, v38, s[8:9]
	v_cmp_eq_u32_e64 s[8:9], v200, v195
	v_mul_f32_e32 v4, v5, v4
	v_fma_f32 v56, v22, v4, 0
	v_sub_f32_e32 v4, v34, v18
	v_exp_f32_e32 v4, v4
	v_sub_f32_e32 v5, v35, v19
	v_exp_f32_e32 v5, v5
	v_cndmask_b32_e64 v53, 0, v124, s[8:9]
	v_fmac_f32_e32 v53, v6, v38
	v_fma_f32 v6, v20, v4, 0
	v_cmp_le_u32_e64 s[8:9], v204, v195
	s_nop 1
	v_cndmask_b32_e64 v18, 0, v6, s[8:9]
	v_fmac_f32_e32 v18, v21, v5
	ds_read2_b32 v[4:5], v216 offset0:165 offset1:167
	v_cmp_lt_u32_e64 s[8:9], v204, v195
	s_waitcnt lgkmcnt(0)
	v_sub_f32_e32 v4, v35, v4
	v_exp_f32_e32 v4, v4
	v_cndmask_b32_e64 v6, v18, v6, s[8:9]
	v_cmp_eq_u32_e64 s[8:9], v204, v195
	v_mul_f32_e32 v4, v5, v4
	s_nop 0
	v_cndmask_b32_e64 v57, 0, v124, s[8:9]
	v_fmac_f32_e32 v57, v7, v6
	v_sub_f32_e32 v6, v34, v42
	v_fma_f32 v42, v23, v4, 0
	v_sub_f32_e32 v4, v35, v43
	v_exp_f32_e32 v7, v4
	ds_read2_b32 v[4:5], v216 offset0:169 offset1:171
	v_exp_f32_e32 v6, v6
	v_cmp_le_u32_e64 s[8:9], v206, v195
	s_waitcnt lgkmcnt(0)
	v_sub_f32_e32 v4, v35, v4
	v_exp_f32_e32 v4, v4
	v_fma_f32 v6, v44, v6, 0
	v_cndmask_b32_e64 v18, 0, v6, s[8:9]
	v_fmac_f32_e32 v18, v45, v7
	v_mul_f32_e32 v4, v5, v4
	v_fma_f32 v44, v24, v4, 0
	v_sub_f32_e32 v4, v34, v46
	v_exp_f32_e32 v4, v4
	v_sub_f32_e32 v5, v35, v47
	v_cmp_lt_u32_e64 s[8:9], v206, v195
	v_exp_f32_e32 v5, v5
	v_fma_f32 v4, v48, v4, 0
	v_cndmask_b32_e64 v6, v18, v6, s[8:9]
	v_cmp_eq_u32_e64 s[8:9], v206, v195
	ds_read2_b32 v[18:19], v216 offset0:173 offset1:175
	s_nop 0
	v_cndmask_b32_e64 v43, 0, v124, s[8:9]
	v_cmp_le_u32_e64 s[8:9], v207, v195
	v_fmac_f32_e32 v43, v8, v6
	s_nop 0
	v_cndmask_b32_e64 v6, 0, v4, s[8:9]
	v_fmac_f32_e32 v6, v49, v5
	v_cmp_lt_u32_e64 s[8:9], v207, v195
	s_nop 1
	v_cndmask_b32_e64 v4, v6, v4, s[8:9]
	v_cmp_eq_u32_e64 s[8:9], v207, v195
	s_nop 1
	v_cndmask_b32_e64 v45, 0, v124, s[8:9]
	v_fmac_f32_e32 v45, v9, v4
	s_waitcnt lgkmcnt(0)
	v_sub_f32_e32 v4, v35, v18
	v_exp_f32_e32 v8, v4
	ds_read_b128 v[4:7], v216 offset:256
	v_cmp_le_u32_e64 s[8:9], v197, v195
	v_mul_f32_e32 v8, v19, v8
	ds_read_b128 v[18:21], v216 offset:272
	s_waitcnt lgkmcnt(1)
	v_sub_f32_e32 v4, v34, v4
	v_exp_f32_e32 v4, v4
	v_fma_f32 v46, v25, v8, 0
	ds_read_b128 v[22:25], v216 offset:288
	ds_read_b128 v[38:41], v216 offset:304
	v_fma_f32 v6, v6, v4, 0
	v_sub_f32_e32 v4, v35, v5
	v_exp_f32_e32 v8, v4
	ds_read2_b32 v[4:5], v216 offset0:193 offset1:195
	v_cndmask_b32_e64 v9, 0, v6, s[8:9]
	v_cmp_lt_u32_e64 s[8:9], v197, v195
	v_fmac_f32_e32 v9, v7, v8
	s_waitcnt lgkmcnt(0)
	v_sub_f32_e32 v4, v35, v4
	v_exp_f32_e32 v4, v4
	v_cndmask_b32_e64 v6, v9, v6, s[8:9]
	v_cmp_eq_u32_e64 s[8:9], v197, v195
	v_mul_f32_e32 v4, v5, v4
	v_fma_f32 v26, v26, v4, 0
	v_sub_f32_e32 v4, v34, v18
	v_exp_f32_e32 v4, v4
	v_sub_f32_e32 v5, v35, v19
	v_exp_f32_e32 v5, v5
	v_cndmask_b32_e64 v47, 0, v124, s[8:9]
	v_fmac_f32_e32 v47, v10, v6
	v_fma_f32 v6, v20, v4, 0
	v_cmp_le_u32_e64 s[8:9], v201, v195
	s_nop 1
	v_cndmask_b32_e64 v7, 0, v6, s[8:9]
	v_fmac_f32_e32 v7, v21, v5
	ds_read2_b32 v[4:5], v216 offset0:197 offset1:199
	v_cmp_lt_u32_e64 s[8:9], v201, v195
	s_waitcnt lgkmcnt(0)
	v_sub_f32_e32 v4, v35, v4
	v_exp_f32_e32 v4, v4
	v_cndmask_b32_e64 v6, v7, v6, s[8:9]
	v_cmp_eq_u32_e64 s[8:9], v201, v195
	v_mul_f32_e32 v4, v5, v4
	v_fma_f32 v27, v27, v4, 0
	v_sub_f32_e32 v4, v35, v23
	v_cndmask_b32_e64 v48, 0, v124, s[8:9]
	v_exp_f32_e32 v7, v4
	ds_read2_b32 v[4:5], v216 offset0:201 offset1:203
	v_fmac_f32_e32 v48, v11, v6
	v_sub_f32_e32 v6, v34, v22
	v_exp_f32_e32 v6, v6
	v_cmp_le_u32_e64 s[8:9], v202, v195
	s_waitcnt lgkmcnt(0)
	v_sub_f32_e32 v4, v35, v4
	v_exp_f32_e32 v4, v4
	v_fma_f32 v6, v24, v6, 0
	v_cndmask_b32_e64 v8, 0, v6, s[8:9]
	v_fmac_f32_e32 v8, v25, v7
	v_cmp_lt_u32_e64 s[8:9], v202, v195
	v_mul_f32_e32 v4, v5, v4
	v_sub_f32_e32 v5, v35, v39
	v_cndmask_b32_e64 v6, v8, v6, s[8:9]
	v_cmp_eq_u32_e64 s[8:9], v202, v195
	v_exp_f32_e32 v5, v5
	ds_read2_b32 v[8:9], v216 offset0:205 offset1:207
	v_cndmask_b32_e64 v49, 0, v124, s[8:9]
	v_fmac_f32_e32 v49, v12, v6
	v_fma_f32 v12, v28, v4, 0
	v_sub_f32_e32 v4, v34, v38
	v_exp_f32_e32 v4, v4
	v_cmp_le_u32_e64 s[8:9], v205, v195
	v_fma_f32 v4, v40, v4, 0
	s_nop 0
	v_cndmask_b32_e64 v6, 0, v4, s[8:9]
	v_fmac_f32_e32 v6, v41, v5
	v_cmp_lt_u32_e64 s[8:9], v205, v195
	s_nop 1
	v_cndmask_b32_e64 v4, v6, v4, s[8:9]
	v_cmp_eq_u32_e64 s[8:9], v205, v195
	s_nop 1
	v_cndmask_b32_e64 v28, 0, v124, s[8:9]
	v_fmac_f32_e32 v28, v13, v4
	s_waitcnt lgkmcnt(0)
	v_sub_f32_e32 v4, v35, v8
	v_exp_f32_e32 v8, v4
	ds_read_b128 v[4:7], v216 offset:384
	v_cmp_le_u32_e64 s[8:9], v196, v195
	v_mul_f32_e32 v8, v9, v8
	v_fma_f32 v13, v29, v8, 0
	ds_read_b128 v[8:11], v216 offset:400
	s_waitcnt lgkmcnt(1)
	v_sub_f32_e32 v4, v34, v4
	v_exp_f32_e32 v4, v4
	v_sub_f32_e32 v5, v35, v5
	v_exp_f32_e32 v5, v5
	ds_read_b128 v[18:21], v216 offset:416
	ds_read_b128 v[22:25], v216 offset:432
	v_fma_f32 v6, v6, v4, 0
	v_cndmask_b32_e64 v29, 0, v6, s[8:9]
	v_fmac_f32_e32 v29, v7, v5
	ds_read2_b32 v[4:5], v216 offset0:225 offset1:227
	v_cmp_lt_u32_e64 s[8:9], v196, v195
	s_waitcnt lgkmcnt(0)
	v_sub_f32_e32 v4, v35, v4
	v_exp_f32_e32 v4, v4
	v_cndmask_b32_e64 v6, v29, v6, s[8:9]
	v_cmp_eq_u32_e64 s[8:9], v196, v195
	v_mul_f32_e32 v4, v5, v4
	s_nop 0
	v_cndmask_b32_e64 v7, 0, v124, s[8:9]
	v_fmac_f32_e32 v7, v14, v6
	v_sub_f32_e32 v6, v34, v8
	v_fma_f32 v8, v30, v4, 0
	v_sub_f32_e32 v4, v35, v9
	v_exp_f32_e32 v9, v4
	ds_read2_b32 v[4:5], v216 offset0:229 offset1:231
	v_exp_f32_e32 v6, v6
	v_cmp_le_u32_e64 s[8:9], v198, v195
	s_waitcnt lgkmcnt(0)
	v_sub_f32_e32 v4, v35, v4
	v_fma_f32 v6, v10, v6, 0
	v_exp_f32_e32 v4, v4
	v_cndmask_b32_e64 v10, 0, v6, s[8:9]
	v_fmac_f32_e32 v10, v11, v9
	v_cmp_lt_u32_e64 s[8:9], v198, v195
	v_mul_f32_e32 v4, v5, v4
	v_sub_f32_e32 v5, v35, v19
	v_cndmask_b32_e64 v6, v10, v6, s[8:9]
	v_cmp_eq_u32_e64 s[8:9], v198, v195
	v_exp_f32_e32 v5, v5
	s_nop 0
	v_cndmask_b32_e64 v9, 0, v124, s[8:9]
	v_fmac_f32_e32 v9, v15, v6
	v_fma_f32 v6, v31, v4, 0
	v_sub_f32_e32 v4, v34, v18
	v_exp_f32_e32 v4, v4
	v_cmp_le_u32_e64 s[8:9], v199, v195
	v_fma_f32 v10, v20, v4, 0
	s_nop 0
	v_cndmask_b32_e64 v11, 0, v10, s[8:9]
	v_fmac_f32_e32 v11, v21, v5
	ds_read2_b32 v[4:5], v216 offset0:233 offset1:235
	v_cmp_lt_u32_e64 s[8:9], v199, v195
	s_waitcnt lgkmcnt(0)
	v_sub_f32_e32 v4, v35, v4
	v_exp_f32_e32 v4, v4
	v_cndmask_b32_e64 v10, v11, v10, s[8:9]
	v_cmp_eq_u32_e64 s[8:9], v199, v195
	v_mul_f32_e32 v4, v5, v4
	v_fma_f32 v14, v32, v4, 0
	v_sub_f32_e32 v4, v35, v23
	v_cndmask_b32_e64 v11, 0, v124, s[8:9]
	v_exp_f32_e32 v15, v4
	ds_read2_b32 v[4:5], v216 offset0:237 offset1:239
	v_fmac_f32_e32 v11, v16, v10
	v_sub_f32_e32 v10, v34, v22
	v_exp_f32_e32 v10, v10
	v_cmp_le_u32_e64 s[8:9], v203, v195
	s_waitcnt lgkmcnt(0)
	v_sub_f32_e32 v4, v35, v4
	v_exp_f32_e32 v4, v4
	v_fma_f32 v10, v24, v10, 0
	v_cndmask_b32_e64 v16, 0, v10, s[8:9]
	v_fmac_f32_e32 v16, v25, v15
	v_cmp_lt_u32_e64 s[8:9], v203, v195
	v_mul_f32_e32 v4, v5, v4
	v_fma_f32 v4, v33, v4, 0
	v_cndmask_b32_e64 v10, v16, v10, s[8:9]
	v_cmp_eq_u32_e64 s[8:9], v203, v195
	v_cvt_pk_bf16_f32 v50, v37, v50
	v_cvt_pk_bf16_f32 v51, v51, v52
	v_cvt_pk_bf16_f32 v52, v53, v57
	v_cvt_pk_bf16_f32 v53, v43, v45
	s_nop 1
	v_cndmask_b32_e64 v15, 0, v124, s[8:9]
	v_fmac_f32_e32 v15, v17, v10
	v_cvt_pk_bf16_f32 v66, v47, v48
	v_cvt_pk_bf16_f32 v67, v49, v28
	v_cvt_pk_bf16_f32 v68, v7, v9
	v_cvt_pk_bf16_f32 v69, v11, v15
	v_cvt_pk_bf16_f32 v70, v2, v3
	v_cvt_pk_bf16_f32 v71, v54, v55
	v_cvt_pk_bf16_f32 v72, v56, v42
	v_cvt_pk_bf16_f32 v73, v44, v46
	v_cvt_pk_bf16_f32 v74, v26, v27
	v_cvt_pk_bf16_f32 v75, v12, v13
	v_cvt_pk_bf16_f32 v76, v8, v6
	v_cvt_pk_bf16_f32 v77, v14, v4
	ds_read_b64_tr_b16 v[2:3], v125 offset:0
	ds_read_b64_tr_b16 v[4:5], v125 offset:0x800
	ds_read_b64_tr_b16 v[18:19], v125 offset:0x1000
	ds_read_b64_tr_b16 v[20:21], v125 offset:0x1800
	ds_read_b64_tr_b16 v[22:23], v125 offset:0x2000
	ds_read_b64_tr_b16 v[24:25], v125 offset:0x2800
	ds_read_b64_tr_b16 v[26:27], v125 offset:0x3000
	ds_read_b64_tr_b16 v[28:29], v125 offset:0x3800
	s_waitcnt lgkmcnt(0)
	v_permlane32_swap_b32_e32 v50, v52
	v_permlane32_swap_b32_e32 v51, v53
	v_permlane32_swap_b32_e32 v66, v68
	v_permlane32_swap_b32_e32 v67, v69
	v_permlane32_swap_b32_e32 v70, v72
	v_permlane32_swap_b32_e32 v71, v73
	v_permlane32_swap_b32_e32 v74, v76
	v_permlane32_swap_b32_e32 v75, v77
	v_mfma_f32_32x32x16_bf16 v[2:17], v[50:53], v[2:5], 0
	ds_read_b64_tr_b16 v[54:55], v125 offset:0x200
	ds_read_b64_tr_b16 v[56:57], v125 offset:0xa00
	ds_read_b64_tr_b16 v[118:119], v125 offset:0x1200
	ds_read_b64_tr_b16 v[120:121], v125 offset:0x1a00
	ds_read_b64_tr_b16 v[114:115], v125 offset:0x2200
	ds_read_b64_tr_b16 v[116:117], v125 offset:0x2a00
	ds_read_b64_tr_b16 v[78:79], v125 offset:0x3200
	v_mfma_f32_32x32x16_bf16 v[2:17], v[66:69], v[18:21], v[2:17]
	ds_read_b64_tr_b16 v[80:81], v125 offset:0x3a00
	s_waitcnt lgkmcnt(0)
	v_mfma_f32_32x32x16_bf16 v[2:17], v[70:73], v[22:25], v[2:17]
	v_mfma_f32_32x32x16_bf16 v[2:17], v[74:77], v[26:29], v[2:17]
	ds_read_b128 v[18:21], v215
	v_or_b32_e32 v127, 32, v195
	v_lshl_add_u32 v144, v127, 8, 0
	v_add_u32_e32 v22, v144, v36
	ds_read_b128 v[22:25], v22 offset:16384
	ds_read_b128 v[128:131], v216 offset:560
	v_add_u32_e32 v58, v144, v58
	s_waitcnt lgkmcnt(1)
	v_mfma_f32_32x32x16_bf16 v[34:49], v[18:21], v[22:25], 0
	ds_read_b128 v[18:21], v215 offset:8192
	ds_read_b128 v[132:135], v217
	ds_read_b128 v[136:139], v58 offset:16384
	v_add_u32_e32 v58, v144, v60
	ds_read_b128 v[140:143], v58 offset:16384
	v_add_u32_e32 v58, v144, v61
	s_waitcnt lgkmcnt(3)
	v_mfma_f32_32x32x16_bf16 v[18:33], v[18:21], v[22:25], 0
	s_waitcnt lgkmcnt(1)
	v_mfma_f32_32x32x16_bf16 v[34:49], v[132:135], v[136:139], v[34:49]
	ds_read_b128 v[132:135], v217 offset:8192
	ds_read_b128 v[224:227], v218
	s_waitcnt lgkmcnt(1)
	v_mfma_f32_32x32x16_bf16 v[18:33], v[132:135], v[136:139], v[18:33]
	ds_read_b128 v[132:135], v218 offset:8192
	ds_read_b128 v[136:139], v219
	s_waitcnt lgkmcnt(2)
	v_mfma_f32_32x32x16_bf16 v[34:49], v[224:227], v[140:143], v[34:49]
	s_waitcnt lgkmcnt(1)
	v_mfma_f32_32x32x16_bf16 v[18:33], v[132:135], v[140:143], v[18:33]
	ds_read_b128 v[132:135], v58 offset:16384
	v_add_u32_e32 v58, v144, v62
	ds_read_b128 v[140:143], v58 offset:16384
	v_add_u32_e32 v58, v144, v63
	s_waitcnt lgkmcnt(1)
	v_mfma_f32_32x32x16_bf16 v[34:49], v[136:139], v[132:135], v[34:49]
	ds_read_b128 v[136:139], v219 offset:8192
	ds_read_b128 v[224:227], v220
	s_waitcnt lgkmcnt(0)
	v_mfma_f32_32x32x16_bf16 v[34:49], v[224:227], v[140:143], v[34:49]
	v_mfma_f32_32x32x16_bf16 v[18:33], v[136:139], v[132:135], v[18:33]
	ds_read_b128 v[132:135], v220 offset:8192
	ds_read_b128 v[136:139], v221
	ds_read_b128 v[60:63], v58 offset:16384
	v_add_u32_e32 v58, v144, v64
	s_waitcnt lgkmcnt(0)
	v_mfma_f32_32x32x16_bf16 v[34:49], v[136:139], v[60:63], v[34:49]
	v_mfma_f32_32x32x16_bf16 v[18:33], v[132:135], v[140:143], v[18:33]
	ds_read_b128 v[132:135], v58 offset:16384
	ds_read_b128 v[136:139], v221 offset:8192
	ds_read_b128 v[140:143], v222
	ds_read_b64 v[122:123], v59 offset:512
	s_waitcnt lgkmcnt(1)
	v_mfma_f32_32x32x16_bf16 v[34:49], v[140:143], v[132:135], v[34:49]
	v_mfma_f32_32x32x16_bf16 v[18:33], v[136:139], v[60:63], v[18:33]
	v_add_u32_e32 v136, v144, v65
	ds_read_b128 v[58:61], v222 offset:8192
	ds_read_b128 v[62:65], v223
	ds_read2_b32 v[144:145], v216 offset1:2
	ds_read_b128 v[136:139], v136 offset:16384
	ds_read2_b32 v[228:229], v216 offset0:4 offset1:6
	ds_read2_b32 v[230:231], v216 offset0:8 offset1:10
	s_waitcnt lgkmcnt(3)
	v_sub_f32_e32 v140, v122, v144
	s_waitcnt lgkmcnt(2)
	v_mfma_f32_32x32x16_bf16 v[34:49], v[62:65], v[136:139], v[34:49]
	v_exp_f32_e32 v144, v140
	ds_read_b128 v[140:143], v223 offset:8192
	ds_read_b128 v[224:227], v216 offset:512
	ds_read2_b32 v[232:233], v216 offset0:12 offset1:14
	v_mul_f32_e32 v62, v145, v144
	s_nop 6
	v_fma_f32 v144, v34, v62, 0
	v_mfma_f32_32x32x16_bf16 v[18:33], v[58:61], v[132:135], v[18:33]
	s_waitcnt lgkmcnt(1)
	v_sub_f32_e32 v34, v122, v224
	v_exp_f32_e32 v34, v34
	v_sub_f32_e32 v62, v123, v225
	v_exp_f32_e32 v62, v62
	v_fma_f32 v34, v226, v34, 0
	v_cndmask_b32_e64 v58, v34, 0, vcc
	v_mfma_f32_32x32x16_bf16 v[18:33], v[140:143], v[136:139], v[18:33]
	v_fmac_f32_e32 v58, v227, v62
	v_cndmask_b32_e64 v34, v58, v34, s[6:7]
	v_sub_f32_e32 v58, v122, v228
	v_exp_f32_e32 v62, v58
	ds_read_b128 v[58:61], v216 offset:528
	v_cmp_le_u32_e32 vcc, v190, v127
	s_nop 5
	v_fmac_f32_e32 v126, v18, v34
	v_mul_f32_e32 v18, v229, v62
	ds_read_b128 v[62:65], v216 offset:544
	s_waitcnt lgkmcnt(1)
	v_sub_f32_e32 v34, v122, v58
	v_exp_f32_e32 v34, v34
	v_fma_f32 v136, v35, v18, 0
	v_sub_f32_e32 v18, v123, v59
	v_exp_f32_e32 v18, v18
	v_fma_f32 v34, v60, v34, 0
	v_cndmask_b32_e32 v35, 0, v34, vcc
	v_cmp_lt_u32_e32 vcc, v190, v127
	v_fmac_f32_e32 v35, v61, v18
	s_nop 0
	v_cndmask_b32_e32 v18, v35, v34, vcc
	v_sub_f32_e32 v34, v122, v230
	v_exp_f32_e32 v34, v34
	v_cmp_eq_u32_e32 vcc, v190, v127
	s_nop 1
	v_cndmask_b32_e32 v137, 0, v124, vcc
	v_fmac_f32_e32 v137, v19, v18
	s_waitcnt lgkmcnt(0)
	v_sub_f32_e32 v19, v122, v62
	v_mul_f32_e32 v18, v231, v34
	v_exp_f32_e32 v19, v19
	v_fma_f32 v138, v36, v18, 0
	v_sub_f32_e32 v18, v123, v63
	v_exp_f32_e32 v18, v18
	v_fma_f32 v19, v64, v19, 0
	v_cmp_le_u32_e32 vcc, v191, v127
	s_nop 1
	v_cndmask_b32_e32 v34, 0, v19, vcc
	v_fmac_f32_e32 v34, v65, v18
	v_cmp_lt_u32_e32 vcc, v191, v127
	v_mfma_f32_32x32x16_bf16 v[50:65], v[50:53], v[54:57], 0
	s_nop 0
	v_cndmask_b32_e32 v18, v34, v19, vcc
	v_sub_f32_e32 v19, v122, v232
	v_exp_f32_e32 v19, v19
	v_cmp_eq_u32_e32 vcc, v191, v127
	s_nop 1
	v_cndmask_b32_e32 v139, 0, v124, vcc
	v_fmac_f32_e32 v139, v20, v18
	v_mul_f32_e32 v18, v233, v19
	v_sub_f32_e32 v19, v122, v128
	v_exp_f32_e32 v19, v19
	v_fma_f32 v140, v37, v18, 0
	v_sub_f32_e32 v18, v123, v129
	v_exp_f32_e32 v18, v18
	v_fma_f32 v19, v130, v19, 0
	v_cmp_le_u32_e32 vcc, v193, v127
	v_mfma_f32_32x32x16_bf16 v[50:65], v[66:69], v[118:121], v[50:65]
	s_nop 0
	v_cndmask_b32_e32 v20, 0, v19, vcc
	v_fmac_f32_e32 v20, v131, v18
	v_cmp_lt_u32_e32 vcc, v193, v127
	s_nop 1
	v_cndmask_b32_e32 v18, v20, v19, vcc
	v_cmp_eq_u32_e32 vcc, v193, v127
	v_mfma_f32_32x32x16_bf16 v[50:65], v[70:73], v[114:117], v[50:65]
	s_nop 0
	v_cndmask_b32_e32 v141, 0, v124, vcc
	v_fmac_f32_e32 v141, v21, v18
	ds_read2_b32 v[128:129], v216 offset0:32 offset1:34
	ds_read2_b32 v[130:131], v216 offset0:36 offset1:38
	ds_read2_b32 v[132:133], v216 offset0:40 offset1:42
	ds_read_b128 v[18:21], v216 offset:640
	ds_read2_b32 v[134:135], v216 offset0:44 offset1:46
	v_cmp_le_u32_e32 vcc, v184, v127
	s_waitcnt lgkmcnt(4)
	v_sub_f32_e32 v34, v122, v128
	v_exp_f32_e32 v128, v34
	s_waitcnt lgkmcnt(1)
	v_sub_f32_e32 v18, v122, v18
	v_exp_f32_e32 v18, v18
	v_sub_f32_e32 v19, v123, v19
	v_exp_f32_e32 v19, v19
	ds_read_b128 v[34:37], v216 offset:656
	v_fma_f32 v18, v20, v18, 0
	v_cndmask_b32_e32 v20, 0, v18, vcc
	v_fmac_f32_e32 v20, v21, v19
	v_sub_f32_e32 v19, v122, v130
	v_exp_f32_e32 v19, v19
	v_cmp_lt_u32_e32 vcc, v184, v127
	v_mfma_f32_32x32x16_bf16 v[50:65], v[74:77], v[78:81], v[50:65]
	v_mul_f32_e32 v128, v129, v128
	v_cndmask_b32_e32 v18, v20, v18, vcc
	v_cmp_eq_u32_e32 vcc, v184, v127
	v_fma_f32 v128, v38, v128, 0
	s_nop 0
	v_cndmask_b32_e32 v118, 0, v124, vcc
	v_fmac_f32_e32 v118, v22, v18
	v_mul_f32_e32 v18, v131, v19
	v_fma_f32 v66, v39, v18, 0
	s_waitcnt lgkmcnt(0)
	v_sub_f32_e32 v18, v122, v34
	v_exp_f32_e32 v18, v18
	v_sub_f32_e32 v19, v123, v35
	v_exp_f32_e32 v19, v19
	v_cmp_le_u32_e32 vcc, v187, v127
	v_fma_f32 v18, v36, v18, 0
	s_nop 0
	v_cndmask_b32_e32 v20, 0, v18, vcc
	v_fmac_f32_e32 v20, v37, v19
	v_cmp_lt_u32_e32 vcc, v187, v127
	s_nop 1
	v_cndmask_b32_e32 v22, v20, v18, vcc
	v_sub_f32_e32 v18, v122, v132
	v_exp_f32_e32 v34, v18
	ds_read_b128 v[18:21], v216 offset:672
	v_cmp_eq_u32_e32 vcc, v187, v127
	s_nop 1
	v_cndmask_b32_e32 v72, 0, v124, vcc
	v_fmac_f32_e32 v72, v23, v22
	v_mul_f32_e32 v22, v133, v34
	ds_read_b128 v[34:37], v216 offset:688
	s_waitcnt lgkmcnt(1)
	v_sub_f32_e32 v18, v122, v18
	v_exp_f32_e32 v18, v18
	v_sub_f32_e32 v19, v123, v19
	v_exp_f32_e32 v19, v19
	v_cmp_le_u32_e32 vcc, v189, v127
	v_fma_f32 v18, v20, v18, 0
	v_fma_f32 v40, v40, v22, 0
	v_cndmask_b32_e32 v20, 0, v18, vcc
	v_fmac_f32_e32 v20, v21, v19
	v_sub_f32_e32 v19, v122, v134
	v_exp_f32_e32 v19, v19
	v_cmp_lt_u32_e32 vcc, v189, v127
	ds_read2_b32 v[22:23], v216 offset0:64 offset1:66
	s_nop 0
	v_cndmask_b32_e32 v18, v20, v18, vcc
	v_cmp_eq_u32_e32 vcc, v189, v127
	s_nop 1
	v_cndmask_b32_e32 v73, 0, v124, vcc
	v_fmac_f32_e32 v73, v24, v18
	v_mul_f32_e32 v18, v135, v19
	s_waitcnt lgkmcnt(1)
	v_sub_f32_e32 v19, v122, v34
	v_exp_f32_e32 v19, v19
	v_fma_f32 v41, v41, v18, 0
	v_sub_f32_e32 v18, v123, v35
	v_exp_f32_e32 v18, v18
	v_fma_f32 v19, v36, v19, 0
	v_cmp_le_u32_e32 vcc, v192, v127
	ds_read2_b32 v[34:35], v216 offset0:68 offset1:70
	s_nop 0
	v_cndmask_b32_e32 v20, 0, v19, vcc
	v_fmac_f32_e32 v20, v37, v18
	v_cmp_lt_u32_e32 vcc, v192, v127
	s_nop 1
	v_cndmask_b32_e32 v18, v20, v19, vcc
	v_cmp_eq_u32_e32 vcc, v192, v127
	s_nop 1
	v_cndmask_b32_e32 v74, 0, v124, vcc
	v_fmac_f32_e32 v74, v25, v18
	s_waitcnt lgkmcnt(1)
	v_sub_f32_e32 v18, v122, v22
	v_exp_f32_e32 v22, v18
	ds_read_b128 v[18:21], v216 offset:768
	ds_read2_b32 v[36:37], v216 offset0:72 offset1:74
	ds_read2_b32 v[38:39], v216 offset0:76 offset1:78
	v_cmp_le_u32_e32 vcc, v180, v127
	s_waitcnt lgkmcnt(2)
	v_sub_f32_e32 v18, v122, v18
	v_exp_f32_e32 v18, v18
	v_sub_f32_e32 v19, v123, v19
	v_exp_f32_e32 v19, v19
	v_mul_f32_e32 v67, v23, v22
	v_fma_f32 v18, v20, v18, 0
	v_cndmask_b32_e32 v20, 0, v18, vcc
	ds_read_b128 v[22:25], v216 offset:784
	v_fmac_f32_e32 v20, v21, v19
	v_sub_f32_e32 v19, v122, v34
	v_exp_f32_e32 v19, v19
	v_cmp_lt_u32_e32 vcc, v180, v127
	v_fma_f32 v42, v42, v67, 0
	s_nop 0
	v_cndmask_b32_e32 v18, v20, v18, vcc
	v_cmp_eq_u32_e32 vcc, v180, v127
	s_nop 1
	v_cndmask_b32_e32 v75, 0, v124, vcc
	v_fmac_f32_e32 v75, v26, v18
	v_mul_f32_e32 v18, v35, v19
	s_waitcnt lgkmcnt(0)
	v_sub_f32_e32 v19, v122, v22
	v_exp_f32_e32 v19, v19
	v_fma_f32 v43, v43, v18, 0
	v_sub_f32_e32 v18, v123, v23
	v_exp_f32_e32 v18, v18
	v_fma_f32 v19, v24, v19, 0
	v_cmp_le_u32_e32 vcc, v183, v127
	s_nop 1
	v_cndmask_b32_e32 v20, 0, v19, vcc
	v_fmac_f32_e32 v20, v25, v18
	v_cmp_lt_u32_e32 vcc, v183, v127
	v_sub_f32_e32 v18, v122, v36
	v_exp_f32_e32 v23, v18
	v_cndmask_b32_e32 v22, v20, v19, vcc
	ds_read_b128 v[18:21], v216 offset:800
	v_cmp_eq_u32_e32 vcc, v183, v127
	v_mul_f32_e32 v26, v37, v23
	v_fma_f32 v44, v44, v26, 0
	v_cndmask_b32_e32 v76, 0, v124, vcc
	v_fmac_f32_e32 v76, v27, v22
	ds_read_b128 v[22:25], v216 offset:816
	s_waitcnt lgkmcnt(1)
	v_sub_f32_e32 v18, v122, v18
	v_exp_f32_e32 v18, v18
	v_sub_f32_e32 v19, v123, v19
	v_exp_f32_e32 v19, v19
	v_cmp_le_u32_e32 vcc, v185, v127
	v_fma_f32 v18, v20, v18, 0
	ds_read2_b32 v[26:27], v216 offset0:100 offset1:102
	v_cndmask_b32_e32 v20, 0, v18, vcc
	v_fmac_f32_e32 v20, v21, v19
	v_sub_f32_e32 v19, v122, v38
	v_exp_f32_e32 v19, v19
	v_cmp_lt_u32_e32 vcc, v185, v127
	s_nop 1
	v_cndmask_b32_e32 v18, v20, v18, vcc
	v_cmp_eq_u32_e32 vcc, v185, v127
	s_nop 1
	v_cndmask_b32_e32 v38, 0, v124, vcc
	v_fmac_f32_e32 v38, v28, v18
	v_mul_f32_e32 v18, v39, v19
	s_waitcnt lgkmcnt(1)
	v_sub_f32_e32 v19, v122, v22
	v_exp_f32_e32 v19, v19
	v_fma_f32 v39, v45, v18, 0
	v_sub_f32_e32 v18, v123, v23
	v_exp_f32_e32 v18, v18
	v_fma_f32 v19, v24, v19, 0
	v_cmp_le_u32_e32 vcc, v188, v127
	ds_read2_b32 v[22:23], v216 offset0:96 offset1:98
	s_nop 0
	v_cndmask_b32_e32 v20, 0, v19, vcc
	v_fmac_f32_e32 v20, v25, v18
	v_cmp_lt_u32_e32 vcc, v188, v127
	s_nop 1
	v_cndmask_b32_e32 v18, v20, v19, vcc
	v_cmp_eq_u32_e32 vcc, v188, v127
	s_nop 1
	v_cndmask_b32_e32 v45, 0, v124, vcc
	v_fmac_f32_e32 v45, v29, v18
	s_waitcnt lgkmcnt(0)
	v_sub_f32_e32 v18, v122, v22
	v_exp_f32_e32 v22, v18
	ds_read_b128 v[18:21], v216 offset:896
	ds_read2_b32 v[28:29], v216 offset0:104 offset1:106
	ds_read2_b32 v[34:35], v216 offset0:108 offset1:110
	v_cmp_le_u32_e32 vcc, v149, v127
	s_waitcnt lgkmcnt(2)
	v_sub_f32_e32 v18, v122, v18
	v_exp_f32_e32 v18, v18
	v_sub_f32_e32 v19, v123, v19
	v_exp_f32_e32 v19, v19
	v_mul_f32_e32 v36, v23, v22
	v_fma_f32 v18, v20, v18, 0
	v_cndmask_b32_e32 v20, 0, v18, vcc
	ds_read_b128 v[22:25], v216 offset:912
	v_fmac_f32_e32 v20, v21, v19
	v_sub_f32_e32 v19, v122, v26
	v_exp_f32_e32 v19, v19
	v_cmp_lt_u32_e32 vcc, v149, v127
	v_fma_f32 v46, v46, v36, 0
	s_nop 0
	v_cndmask_b32_e32 v18, v20, v18, vcc
	v_cmp_eq_u32_e32 vcc, v149, v127
	s_nop 1
	v_cndmask_b32_e32 v26, 0, v124, vcc
	v_fmac_f32_e32 v26, v30, v18
	v_mul_f32_e32 v18, v27, v19
	s_waitcnt lgkmcnt(0)
	v_sub_f32_e32 v19, v122, v22
	v_exp_f32_e32 v19, v19
	v_fma_f32 v27, v47, v18, 0
	v_sub_f32_e32 v18, v123, v23
	v_exp_f32_e32 v18, v18
	v_fma_f32 v19, v24, v19, 0
	v_cmp_le_u32_e32 vcc, v181, v127
	s_nop 1
	v_cndmask_b32_e32 v20, 0, v19, vcc
	v_fmac_f32_e32 v20, v25, v18
	v_cmp_lt_u32_e32 vcc, v181, v127
	v_sub_f32_e32 v18, v122, v28
	v_exp_f32_e32 v23, v18
	v_cndmask_b32_e32 v22, v20, v19, vcc
	ds_read_b128 v[18:21], v216 offset:928
	v_cmp_eq_u32_e32 vcc, v181, v127
	v_mul_f32_e32 v29, v29, v23
	v_fma_f32 v29, v48, v29, 0
	v_cndmask_b32_e32 v28, 0, v124, vcc
	v_fmac_f32_e32 v28, v31, v22
	ds_read_b128 v[22:25], v216 offset:944
	s_waitcnt lgkmcnt(1)
	v_sub_f32_e32 v18, v122, v18
	v_exp_f32_e32 v18, v18
	v_sub_f32_e32 v19, v123, v19
	v_exp_f32_e32 v19, v19
	v_cmp_le_u32_e32 vcc, v182, v127
	v_fma_f32 v18, v20, v18, 0
	s_nop 0
	v_cndmask_b32_e32 v20, 0, v18, vcc
	v_fmac_f32_e32 v20, v21, v19
	v_sub_f32_e32 v19, v122, v34
	v_exp_f32_e32 v19, v19
	v_cmp_lt_u32_e32 vcc, v182, v127
	s_waitcnt lgkmcnt(0)
	v_sub_f32_e32 v21, v123, v23
	v_exp_f32_e32 v21, v21
	v_cndmask_b32_e32 v18, v20, v18, vcc
	v_cmp_eq_u32_e32 vcc, v182, v127
	v_cvt_pk_bf16_f32 v34, v144, v136
	s_nop 1
	v_cndmask_b32_e32 v20, 0, v124, vcc
	v_fmac_f32_e32 v20, v32, v18
	v_mul_f32_e32 v18, v35, v19
	v_sub_f32_e32 v19, v122, v22
	v_exp_f32_e32 v19, v19
	v_cmp_le_u32_e32 vcc, v186, v127
	v_fma_f32 v18, v49, v18, 0
	v_cvt_pk_bf16_f32 v35, v138, v140
	v_fma_f32 v19, v24, v19, 0
	v_cndmask_b32_e32 v22, 0, v19, vcc
	v_fmac_f32_e32 v22, v25, v21
	v_cmp_lt_u32_e32 vcc, v186, v127
	v_cvt_pk_bf16_f32 v36, v128, v66
	v_cvt_pk_bf16_f32 v37, v40, v41
	v_cvt_pk_bf16_f32 v66, v42, v43
	v_cvt_pk_bf16_f32 v67, v44, v39
	v_cvt_pk_bf16_f32 v68, v46, v27
	s_nop 1
	v_cndmask_b32_e32 v19, v22, v19, vcc
	v_cmp_eq_u32_e32 vcc, v186, v127
	v_cvt_pk_bf16_f32 v69, v29, v18
	v_cvt_pk_bf16_f32 v70, v126, v137
	v_cvt_pk_bf16_f32 v71, v139, v141
	v_cvt_pk_bf16_f32 v72, v118, v72
	v_cvt_pk_bf16_f32 v73, v73, v74
	s_nop 1
	v_cndmask_b32_e32 v21, 0, v124, vcc
	v_fmac_f32_e32 v21, v33, v19
	v_cvt_pk_bf16_f32 v74, v75, v76
	v_cvt_pk_bf16_f32 v75, v38, v45
	v_cvt_pk_bf16_f32 v76, v26, v28
	v_cvt_pk_bf16_f32 v77, v20, v21
	ds_read_b64_tr_b16 v[18:19], v125 offset:0
	ds_read_b64_tr_b16 v[20:21], v125 offset:0x800
	ds_read_b64_tr_b16 v[38:39], v125 offset:0x1000
	ds_read_b64_tr_b16 v[40:41], v125 offset:0x1800
	ds_read_b64_tr_b16 v[42:43], v125 offset:0x2000
	ds_read_b64_tr_b16 v[44:45], v125 offset:0x2800
	ds_read_b64_tr_b16 v[46:47], v125 offset:0x3000
	ds_read_b64_tr_b16 v[48:49], v125 offset:0x3800
	s_waitcnt lgkmcnt(0)
	v_permlane32_swap_b32_e32 v34, v36
	v_permlane32_swap_b32_e32 v35, v37
	v_permlane32_swap_b32_e32 v66, v68
	v_permlane32_swap_b32_e32 v67, v69
	v_permlane32_swap_b32_e32 v70, v72
	v_permlane32_swap_b32_e32 v71, v73
	v_permlane32_swap_b32_e32 v74, v76
	v_permlane32_swap_b32_e32 v75, v77
	v_mfma_f32_32x32x16_bf16 v[18:33], v[34:37], v[18:21], 0
	v_mfma_f32_32x32x16_bf16 v[18:33], v[66:69], v[38:41], v[18:33]
	ds_read_b64_tr_b16 v[38:39], v125 offset:0x200
	ds_read_b64_tr_b16 v[40:41], v125 offset:0xa00
	ds_read_b64_tr_b16 v[78:79], v125 offset:0x1200
	ds_read_b64_tr_b16 v[80:81], v125 offset:0x1a00
	ds_read_b64_tr_b16 v[114:115], v125 offset:0x2200
	ds_read_b64_tr_b16 v[116:117], v125 offset:0x2a00
	ds_read_b64_tr_b16 v[118:119], v125 offset:0x3200
	v_mfma_f32_32x32x16_bf16 v[18:33], v[70:73], v[42:45], v[18:33]
	ds_read_b64_tr_b16 v[120:121], v125 offset:0x3a00
	s_waitcnt lgkmcnt(0)
	v_mfma_f32_32x32x16_bf16 v[18:33], v[74:77], v[46:49], v[18:33]
	v_mfma_f32_32x32x16_bf16 v[34:49], v[34:37], v[38:41], 0
	s_andn2_b64 vcc, exec, s[12:13]
	v_mfma_f32_32x32x16_bf16 v[34:49], v[66:69], v[78:81], v[34:49]
	v_cndmask_b32_e64 v66, 0, 1, s[12:13]
	v_cmp_ne_u32_e64 s[6:7], 1, v66
	v_mfma_f32_32x32x16_bf16 v[34:49], v[70:73], v[114:117], v[34:49]
	v_mfma_f32_32x32x16_bf16 v[34:49], v[74:77], v[118:121], v[34:49]
	s_cbranch_vccnz .LBB0_820
	v_lshl_add_u64 v[66:67], v[150:151], 0, v[146:147]
	v_add_co_u32_e32 v68, vcc, 0x2000, v66
	s_nop 1
	v_addc_co_u32_e32 v69, vcc, 0, v67, vcc
	v_add_co_u32_e32 v66, vcc, 0x3000, v66
	global_load_dwordx4 v[142:145], v[68:69], off nt
	global_load_dwordx4 v[138:141], v[68:69], off offset:1024 nt
	global_load_dwordx4 v[134:137], v[68:69], off offset:2048 nt
	global_load_dwordx4 v[130:133], v[68:69], off offset:3072 nt
	v_addc_co_u32_e32 v67, vcc, 0, v67, vcc
	global_load_dwordx4 v[126:129], v[66:67], off nt
	global_load_dwordx4 v[122:125], v[66:67], off offset:1024 nt
	global_load_dwordx4 v[118:121], v[66:67], off offset:2048 nt
	global_load_dwordx4 v[114:117], v[66:67], off offset:3072 nt
	ds_read_b128 v[66:69], v215 offset:16384
	ds_read_b128 v[224:227], v217 offset:16384
	s_waitcnt lgkmcnt(1)
	v_mfma_f32_32x32x16_bf16 v[66:81], v[66:69], v[110:113], 0
	s_waitcnt lgkmcnt(0)
	v_mfma_f32_32x32x16_bf16 v[66:81], v[224:227], v[106:109], v[66:81]
	ds_read_b128 v[224:227], v218 offset:16384
	s_waitcnt lgkmcnt(0)
	v_mfma_f32_32x32x16_bf16 v[66:81], v[224:227], v[102:105], v[66:81]
	ds_read_b128 v[224:227], v219 offset:16384
	s_waitcnt lgkmcnt(0)
	v_mfma_f32_32x32x16_bf16 v[66:81], v[224:227], v[98:101], v[66:81]
	ds_read_b128 v[224:227], v220 offset:16384
	s_waitcnt lgkmcnt(0)
	v_mfma_f32_32x32x16_bf16 v[66:81], v[224:227], v[94:97], v[66:81]
	ds_read_b128 v[224:227], v221 offset:16384
	s_waitcnt lgkmcnt(0)
	v_mfma_f32_32x32x16_bf16 v[66:81], v[224:227], v[90:93], v[66:81]
	ds_read_b128 v[224:227], v222 offset:16384
	s_waitcnt lgkmcnt(0)
	v_mfma_f32_32x32x16_bf16 v[66:81], v[224:227], v[86:89], v[66:81]
	ds_read_b128 v[224:227], v223 offset:16384
	s_waitcnt lgkmcnt(0)
	v_mfma_f32_32x32x16_bf16 v[66:81], v[224:227], v[82:85], v[66:81]
	ds_read2_b32 v[224:225], v216 offset1:4
	ds_read2_b32 v[226:227], v216 offset0:8 offset1:12
	ds_read2_b32 v[228:229], v216 offset0:32 offset1:36
	ds_read2_b32 v[230:231], v216 offset0:40 offset1:44
	ds_read2_b32 v[232:233], v216 offset0:64 offset1:68
	s_waitcnt lgkmcnt(4)
	v_exp_f32_e32 v224, v224
	v_exp_f32_e32 v225, v225
	s_waitcnt lgkmcnt(3)
	v_exp_f32_e32 v226, v226
	v_exp_f32_e32 v227, v227
	ds_read2_b32 v[234:235], v216 offset0:72 offset1:76
	ds_read2_b32 v[236:237], v216 offset0:96 offset1:100
	ds_read2_b32 v[238:239], v216 offset0:104 offset1:108
	v_pk_fma_f32 v[4:5], v[68:69], v[226:227], v[4:5]
	v_pk_fma_f32 v[2:3], v[66:67], v[224:225], v[2:3]
	ds_read_b128 v[66:69], v215 offset:24576
	ds_read_b128 v[224:227], v217 offset:24576
	s_waitcnt lgkmcnt(7)
	v_exp_f32_e32 v228, v228
	v_exp_f32_e32 v229, v229
	s_waitcnt lgkmcnt(6)
	v_exp_f32_e32 v230, v230
	v_exp_f32_e32 v231, v231
	s_waitcnt lgkmcnt(5)
	v_exp_f32_e32 v232, v232
	v_exp_f32_e32 v233, v233
	s_waitcnt lgkmcnt(4)
	v_exp_f32_e32 v234, v234
	v_exp_f32_e32 v235, v235
	s_waitcnt lgkmcnt(3)
	v_exp_f32_e32 v236, v236
	v_exp_f32_e32 v237, v237
	s_waitcnt lgkmcnt(2)
	v_exp_f32_e32 v238, v238
	v_exp_f32_e32 v239, v239
	v_pk_fma_f32 v[12:13], v[76:77], v[234:235], v[12:13]
	v_pk_fma_f32 v[14:15], v[78:79], v[236:237], v[14:15]
	v_pk_fma_f32 v[10:11], v[74:75], v[232:233], v[10:11]
	v_pk_fma_f32 v[16:17], v[80:81], v[238:239], v[16:17]
	v_pk_fma_f32 v[8:9], v[72:73], v[230:231], v[8:9]
	v_pk_fma_f32 v[6:7], v[70:71], v[228:229], v[6:7]
	s_waitcnt lgkmcnt(1)
	v_mfma_f32_32x32x16_bf16 v[66:81], v[66:69], v[110:113], 0
	ds_read2_b32 v[228:229], v216 offset0:160 offset1:164
	ds_read2_b32 v[230:231], v216 offset0:168 offset1:172
	ds_read2_b32 v[232:233], v216 offset0:192 offset1:196
	ds_read2_b32 v[234:235], v216 offset0:200 offset1:204
	ds_read2_b32 v[236:237], v216 offset0:224 offset1:228
	ds_read2_b32 v[238:239], v216 offset0:232 offset1:236
	s_waitcnt lgkmcnt(5)
	v_exp_f32_e32 v228, v228
	v_mfma_f32_32x32x16_bf16 v[66:81], v[224:227], v[106:109], v[66:81]
	ds_read_b128 v[224:227], v218 offset:24576
	v_exp_f32_e32 v229, v229
	s_waitcnt lgkmcnt(5)
	v_exp_f32_e32 v230, v230
	v_exp_f32_e32 v231, v231
	s_waitcnt lgkmcnt(4)
	v_exp_f32_e32 v232, v232
	v_exp_f32_e32 v233, v233
	s_waitcnt lgkmcnt(3)
	v_exp_f32_e32 v234, v234
	s_waitcnt lgkmcnt(0)
	v_mfma_f32_32x32x16_bf16 v[66:81], v[224:227], v[102:105], v[66:81]
	ds_read_b128 v[224:227], v219 offset:24576
	v_exp_f32_e32 v235, v235
	v_exp_f32_e32 v236, v236
	v_exp_f32_e32 v237, v237
	v_exp_f32_e32 v238, v238
	v_exp_f32_e32 v239, v239
	s_waitcnt lgkmcnt(0)
	v_mfma_f32_32x32x16_bf16 v[66:81], v[224:227], v[98:101], v[66:81]
	ds_read_b128 v[224:227], v220 offset:24576
	s_waitcnt lgkmcnt(0)
	v_mfma_f32_32x32x16_bf16 v[66:81], v[224:227], v[94:97], v[66:81]
	ds_read_b128 v[224:227], v221 offset:24576
	s_waitcnt lgkmcnt(0)
	v_mfma_f32_32x32x16_bf16 v[66:81], v[224:227], v[90:93], v[66:81]
	ds_read_b128 v[224:227], v222 offset:24576
	s_waitcnt lgkmcnt(0)
	v_mfma_f32_32x32x16_bf16 v[66:81], v[224:227], v[86:89], v[66:81]
	ds_read_b128 v[224:227], v223 offset:24576
	s_waitcnt lgkmcnt(0)
	v_mfma_f32_32x32x16_bf16 v[66:81], v[224:227], v[82:85], v[66:81]
	ds_read2_b32 v[224:225], v216 offset0:128 offset1:132
	ds_read2_b32 v[226:227], v216 offset0:136 offset1:140
	s_waitcnt lgkmcnt(1)
	v_exp_f32_e32 v224, v224
	v_exp_f32_e32 v225, v225
	s_waitcnt lgkmcnt(0)
	v_exp_f32_e32 v226, v226
	v_exp_f32_e32 v227, v227
	s_nop 3
	v_pk_fma_f32 v[32:33], v[80:81], v[238:239], v[32:33]
	v_pk_fma_f32 v[30:31], v[78:79], v[236:237], v[30:31]
	v_pk_fma_f32 v[28:29], v[76:77], v[234:235], v[28:29]
	v_pk_fma_f32 v[26:27], v[74:75], v[232:233], v[26:27]
	v_pk_fma_f32 v[24:25], v[72:73], v[230:231], v[24:25]
	v_pk_fma_f32 v[22:23], v[70:71], v[228:229], v[22:23]
	v_pk_fma_f32 v[20:21], v[68:69], v[226:227], v[20:21]
	v_pk_fma_f32 v[18:19], v[66:67], v[224:225], v[18:19]
	s_branch .LBB0_821
.LBB0_820:
.LBB0_821:
	s_sub_i32 s0, s10, 31
	s_cmp_lg_u32 s0, 0
	s_cselect_b64 s[8:9], -1, 0
	s_cmp_eq_u32 s0, 0
	v_lshl_add_u64 v[150:151], v[150:151], 0, s[56:57]
	s_cbranch_scc1 .LBB0_823
	v_lshl_add_u64 v[66:67], v[150:151], 0, v[146:147]
	global_load_dwordx4 v[110:113], v[66:67], off nt
	global_load_dwordx4 v[106:109], v[66:67], off offset:1024 nt
	global_load_dwordx4 v[102:105], v[66:67], off offset:2048 nt
	global_load_dwordx4 v[98:101], v[66:67], off offset:3072 nt
	v_add_co_u32_e32 v66, vcc, 0x1000, v66
	s_nop 1
	v_addc_co_u32_e32 v67, vcc, 0, v67, vcc
	global_load_dwordx4 v[94:97], v[66:67], off nt
	global_load_dwordx4 v[90:93], v[66:67], off offset:1024 nt
	global_load_dwordx4 v[86:89], v[66:67], off offset:2048 nt
	global_load_dwordx4 v[82:85], v[66:67], off offset:3072 nt

.LBB0_825:
	v_cndmask_b32_e64 v66, 0, 1, s[8:9]
	v_cmp_ne_u32_e64 s[6:7], 1, v66
	s_andn2_b64 vcc, exec, s[8:9]
	s_cbranch_vccnz .LBB0_827
	v_lshl_add_u64 v[66:67], v[150:151], 0, v[146:147]
	v_add_co_u32_e32 v68, vcc, 0x2000, v66
	s_nop 1
	v_addc_co_u32_e32 v69, vcc, 0, v67, vcc
	v_add_co_u32_e32 v66, vcc, 0x3000, v66
	global_load_dwordx4 v[142:145], v[68:69], off nt
	global_load_dwordx4 v[138:141], v[68:69], off offset:1024 nt
	global_load_dwordx4 v[134:137], v[68:69], off offset:2048 nt
	global_load_dwordx4 v[130:133], v[68:69], off offset:3072 nt
	v_addc_co_u32_e32 v67, vcc, 0, v67, vcc
	global_load_dwordx4 v[126:129], v[66:67], off nt
	global_load_dwordx4 v[122:125], v[66:67], off offset:1024 nt
	global_load_dwordx4 v[118:121], v[66:67], off offset:2048 nt
	global_load_dwordx4 v[114:117], v[66:67], off offset:3072 nt
	ds_read_b128 v[66:69], v215 offset:16384
	ds_read_b128 v[224:227], v217 offset:16384
	s_waitcnt vmcnt(15) lgkmcnt(1)
	v_mfma_f32_32x32x16_bf16 v[66:81], v[66:69], v[110:113], 0
	s_waitcnt vmcnt(14) lgkmcnt(0)
	v_mfma_f32_32x32x16_bf16 v[66:81], v[224:227], v[106:109], v[66:81]
	ds_read_b128 v[224:227], v218 offset:16384
	s_waitcnt vmcnt(13) lgkmcnt(0)
	v_mfma_f32_32x32x16_bf16 v[66:81], v[224:227], v[102:105], v[66:81]
	ds_read_b128 v[224:227], v219 offset:16384
	s_waitcnt vmcnt(12) lgkmcnt(0)
	v_mfma_f32_32x32x16_bf16 v[66:81], v[224:227], v[98:101], v[66:81]
	ds_read_b128 v[224:227], v220 offset:16384
	s_waitcnt vmcnt(11) lgkmcnt(0)
	v_mfma_f32_32x32x16_bf16 v[66:81], v[224:227], v[94:97], v[66:81]
	ds_read_b128 v[224:227], v221 offset:16384
	s_waitcnt vmcnt(10) lgkmcnt(0)
	v_mfma_f32_32x32x16_bf16 v[66:81], v[224:227], v[90:93], v[66:81]
	ds_read_b128 v[224:227], v222 offset:16384
	s_waitcnt vmcnt(9) lgkmcnt(0)
	v_mfma_f32_32x32x16_bf16 v[66:81], v[224:227], v[86:89], v[66:81]
	ds_read_b128 v[224:227], v223 offset:16384
	s_waitcnt vmcnt(8) lgkmcnt(0)
	v_mfma_f32_32x32x16_bf16 v[66:81], v[224:227], v[82:85], v[66:81]
	ds_read2_b32 v[150:151], v216 offset0:1 offset1:5
	ds_read2_b32 v[224:225], v216 offset0:9 offset1:13
	ds_read2_b32 v[226:227], v216 offset0:33 offset1:37
	ds_read2_b32 v[228:229], v216 offset0:41 offset1:45
	ds_read2_b32 v[230:231], v216 offset0:65 offset1:69
	s_waitcnt lgkmcnt(4)
	v_exp_f32_e32 v150, v150
	v_exp_f32_e32 v151, v151
	s_waitcnt lgkmcnt(3)
	v_exp_f32_e32 v224, v224
	v_exp_f32_e32 v225, v225
	ds_read2_b32 v[232:233], v216 offset0:73 offset1:77
	ds_read2_b32 v[234:235], v216 offset0:97 offset1:101
	ds_read2_b32 v[236:237], v216 offset0:105 offset1:109
	v_pk_fma_f32 v[4:5], v[68:69], v[224:225], v[4:5]
	v_pk_fma_f32 v[2:3], v[66:67], v[150:151], v[2:3]
	ds_read_b128 v[66:69], v215 offset:24576
	s_waitcnt lgkmcnt(6)
	v_exp_f32_e32 v226, v226
	v_exp_f32_e32 v227, v227
	s_waitcnt lgkmcnt(5)
	v_exp_f32_e32 v228, v228
	v_exp_f32_e32 v229, v229
	s_waitcnt lgkmcnt(4)
	v_exp_f32_e32 v230, v230
	v_exp_f32_e32 v231, v231
	s_waitcnt lgkmcnt(3)
	v_exp_f32_e32 v232, v232
	v_exp_f32_e32 v233, v233
	s_waitcnt lgkmcnt(2)
	v_exp_f32_e32 v234, v234
	v_exp_f32_e32 v235, v235
	s_waitcnt lgkmcnt(1)
	v_exp_f32_e32 v236, v236
	v_exp_f32_e32 v237, v237
	v_pk_fma_f32 v[12:13], v[76:77], v[232:233], v[12:13]
	v_pk_fma_f32 v[14:15], v[78:79], v[234:235], v[14:15]
	v_pk_fma_f32 v[10:11], v[74:75], v[230:231], v[10:11]
	v_pk_fma_f32 v[16:17], v[80:81], v[236:237], v[16:17]
	v_pk_fma_f32 v[8:9], v[72:73], v[228:229], v[8:9]
	v_pk_fma_f32 v[6:7], v[70:71], v[226:227], v[6:7]
	s_waitcnt lgkmcnt(0)
	v_mfma_f32_32x32x16_bf16 v[66:81], v[66:69], v[110:113], 0
	ds_read_b128 v[110:113], v217 offset:24576
	s_waitcnt lgkmcnt(0)
	v_mfma_f32_32x32x16_bf16 v[66:81], v[110:113], v[106:109], v[66:81]
	ds_read_b128 v[106:109], v218 offset:24576
	s_waitcnt lgkmcnt(0)
	v_mfma_f32_32x32x16_bf16 v[66:81], v[106:109], v[102:105], v[66:81]
	ds_read_b128 v[102:105], v219 offset:24576
	s_waitcnt lgkmcnt(0)
	v_mfma_f32_32x32x16_bf16 v[66:81], v[102:105], v[98:101], v[66:81]
	ds_read_b128 v[98:101], v220 offset:24576
	s_waitcnt lgkmcnt(0)
	v_mfma_f32_32x32x16_bf16 v[66:81], v[98:101], v[94:97], v[66:81]
	ds_read_b128 v[94:97], v221 offset:24576
	s_waitcnt lgkmcnt(0)
	v_mfma_f32_32x32x16_bf16 v[66:81], v[94:97], v[90:93], v[66:81]
	ds_read_b128 v[90:93], v222 offset:24576
	ds_read2_b32 v[94:95], v216 offset0:225 offset1:229
	ds_read2_b32 v[96:97], v216 offset0:233 offset1:237
	s_waitcnt lgkmcnt(1)
	v_exp_f32_e32 v94, v94
	v_mfma_f32_32x32x16_bf16 v[66:81], v[90:93], v[86:89], v[66:81]
	ds_read_b128 v[86:89], v223 offset:24576
	ds_read2_b32 v[90:91], v216 offset0:193 offset1:197
	ds_read2_b32 v[92:93], v216 offset0:201 offset1:205
	v_exp_f32_e32 v95, v95
	s_waitcnt lgkmcnt(3)
	v_exp_f32_e32 v96, v96
	v_exp_f32_e32 v97, v97
	s_waitcnt lgkmcnt(1)
	v_exp_f32_e32 v90, v90
	v_mfma_f32_32x32x16_bf16 v[66:81], v[86:89], v[82:85], v[66:81]
	ds_read2_b32 v[82:83], v216 offset0:129 offset1:133
	ds_read2_b32 v[84:85], v216 offset0:137 offset1:141
	ds_read2_b32 v[86:87], v216 offset0:161 offset1:165
	ds_read2_b32 v[88:89], v216 offset0:169 offset1:173
	v_exp_f32_e32 v91, v91
	s_waitcnt lgkmcnt(3)
	v_exp_f32_e32 v82, v82
	v_exp_f32_e32 v83, v83
	s_waitcnt lgkmcnt(2)
	v_exp_f32_e32 v84, v84
	v_exp_f32_e32 v85, v85
	s_waitcnt lgkmcnt(1)
	v_exp_f32_e32 v86, v86
	v_exp_f32_e32 v87, v87
	s_waitcnt lgkmcnt(0)
	v_exp_f32_e32 v88, v88
	v_exp_f32_e32 v89, v89
	v_exp_f32_e32 v92, v92
	v_exp_f32_e32 v93, v93
	v_pk_fma_f32 v[32:33], v[80:81], v[96:97], v[32:33]
	v_pk_fma_f32 v[30:31], v[78:79], v[94:95], v[30:31]
	v_pk_fma_f32 v[26:27], v[74:75], v[90:91], v[26:27]
	v_pk_fma_f32 v[28:29], v[76:77], v[92:93], v[28:29]
	v_pk_fma_f32 v[24:25], v[72:73], v[88:89], v[24:25]
	v_pk_fma_f32 v[22:23], v[70:71], v[86:87], v[22:23]
	v_pk_fma_f32 v[20:21], v[68:69], v[84:85], v[20:21]
	v_pk_fma_f32 v[18:19], v[66:67], v[82:83], v[18:19]

.LBB0_1026:
	v_or_b32_e32 v52, s0, v83
	v_ashrrev_i32_e32 v53, 31, v52
	v_lshlrev_b64 v[50:51], 12, v[52:53]
	v_lshl_add_u64 v[2:3], v[72:73], 0, v[50:51]
	global_load_dwordx4 v[88:91], v[2:3], off nt
	global_load_dwordx4 v[96:99], v[2:3], off offset:1024 nt
	global_load_dwordx4 v[236:239], v[2:3], off offset:2048 nt
	global_load_dwordx4 v[240:243], v[2:3], off offset:3072 nt
	v_or_b32_e32 v86, 1, v52
	v_ashrrev_i32_e32 v87, 31, v86
	v_or_b32_e32 v64, 2, v52
	v_lshlrev_b64 v[84:85], 12, v[86:87]
	v_ashrrev_i32_e32 v65, 31, v64
	v_or_b32_e32 v60, 3, v52
	v_lshl_add_u64 v[2:3], v[72:73], 0, v[84:85]
	v_lshlrev_b64 v[62:63], 12, v[64:65]
	v_ashrrev_i32_e32 v61, 31, v60
	global_load_dwordx4 v[46:49], v[2:3], off nt
	global_load_dwordx4 v[42:45], v[2:3], off offset:1024 nt
	global_load_dwordx4 v[38:41], v[2:3], off offset:2048 nt
	global_load_dwordx4 v[34:37], v[2:3], off offset:3072 nt
	v_lshl_add_u64 v[2:3], v[72:73], 0, v[62:63]
	v_lshlrev_b64 v[58:59], 12, v[60:61]
	global_load_dwordx4 v[30:33], v[2:3], off nt
	global_load_dwordx4 v[26:29], v[2:3], off offset:1024 nt
	global_load_dwordx4 v[22:25], v[2:3], off offset:2048 nt
	global_load_dwordx4 v[18:21], v[2:3], off offset:3072 nt
	v_lshl_add_u64 v[2:3], v[72:73], 0, v[58:59]
	global_load_dwordx4 v[14:17], v[2:3], off nt
	global_load_dwordx4 v[10:13], v[2:3], off offset:1024 nt
	global_load_dwordx4 v[6:9], v[2:3], off offset:2048 nt
	s_nop 0
	global_load_dwordx4 v[2:5], v[2:3], off offset:3072 nt
	v_lshlrev_b64 v[52:53], 11, v[52:53]
	s_waitcnt vmcnt(15)
	v_lshlrev_b32_e32 v94, 16, v88
	v_and_b32_e32 v92, 0xffff0000, v88
	v_add_f32_e32 v88, 0, v94
	v_lshlrev_b32_e32 v56, 16, v89
	v_add_f32_e32 v88, v88, v92
	v_and_b32_e32 v54, 0xffff0000, v89
	v_add_f32_e32 v88, v88, v56
	v_lshlrev_b32_e32 v95, 16, v90
	v_add_f32_e32 v88, v88, v54
	v_and_b32_e32 v93, 0xffff0000, v90
	v_add_f32_e32 v88, v88, v95
	v_lshlrev_b32_e32 v57, 16, v91
	v_add_f32_e32 v88, v88, v93
	v_and_b32_e32 v55, 0xffff0000, v91
	v_add_f32_e32 v88, v88, v57
	s_waitcnt vmcnt(14)
	v_lshlrev_b32_e32 v235, 16, v96
	v_add_f32_e32 v88, v88, v55
	v_and_b32_e32 v233, 0xffff0000, v96
	v_add_f32_e32 v88, v88, v235
	v_lshlrev_b32_e32 v231, 16, v97
	v_add_f32_e32 v88, v88, v233
	v_and_b32_e32 v228, 0xffff0000, v97
	v_add_f32_e32 v88, v88, v231
	v_lshlrev_b32_e32 v234, 16, v98
	v_add_f32_e32 v88, v88, v228
	v_and_b32_e32 v232, 0xffff0000, v98
	v_add_f32_e32 v88, v88, v234
	v_lshlrev_b32_e32 v230, 16, v99
	v_add_f32_e32 v88, v88, v232
	v_and_b32_e32 v229, 0xffff0000, v99
	v_add_f32_e32 v88, v88, v230
	s_waitcnt vmcnt(13)
	v_lshlrev_b32_e32 v226, 16, v236
	v_add_f32_e32 v88, v88, v229
	v_and_b32_e32 v224, 0xffff0000, v236
	v_add_f32_e32 v88, v88, v226
	v_lshlrev_b32_e32 v222, 16, v237
	v_add_f32_e32 v88, v88, v224
	v_and_b32_e32 v100, 0xffff0000, v237
	v_add_f32_e32 v88, v88, v222
	v_lshlrev_b32_e32 v227, 16, v238
	v_add_f32_e32 v88, v88, v100
	v_and_b32_e32 v225, 0xffff0000, v238
	v_add_f32_e32 v88, v88, v227
	v_lshlrev_b32_e32 v223, 16, v239
	v_add_f32_e32 v88, v88, v225
	v_and_b32_e32 v101, 0xffff0000, v239
	v_add_f32_e32 v88, v88, v223
	s_waitcnt vmcnt(12)
	v_lshlrev_b32_e32 v99, 16, v240
	v_add_f32_e32 v88, v88, v101
	v_and_b32_e32 v98, 0xffff0000, v240
	v_add_f32_e32 v88, v88, v99
	v_lshlrev_b32_e32 v97, 16, v241
	v_add_f32_e32 v88, v88, v98
	v_and_b32_e32 v96, 0xffff0000, v241
	v_add_f32_e32 v88, v88, v97
	v_add_f32_e32 v122, v88, v96
	v_lshlrev_b32_e32 v91, 16, v242
	v_and_b32_e32 v90, 0xffff0000, v242
	v_add_f32_e32 v122, v122, v91
	v_lshlrev_b32_e32 v89, 16, v243
	v_add_f32_e32 v122, v122, v90
	v_and_b32_e32 v88, 0xffff0000, v243
	v_add_f32_e32 v122, v122, v89
	v_add_f32_e32 v122, v122, v88
	v_mov_b32_e32 v123, v122
	s_nop 1
	v_permlane32_swap_b32_e32 v123, v122
	s_waitcnt lgkmcnt(0)
	v_add_f32_e32 v122, v122, v123
	v_mov_b32_e32 v123, v122
	s_nop 1
	v_permlane16_swap_b32_e32 v123, v122
	s_waitcnt lgkmcnt(0)
	v_add_f32_e32 v122, v122, v123
	s_nop 1
	v_mov_b32_dpp v123, v122 row_ror:8 row_mask:0xf bank_mask:0xf
	s_waitcnt lgkmcnt(0)
	v_add_f32_e32 v122, v122, v123
	s_nop 1
	v_mov_b32_dpp v123, v122 row_shr:4 row_mask:0xf bank_mask:0xa
	v_mov_b32_dpp v123, v122 row_shl:4 row_mask:0xf bank_mask:0x5
	s_waitcnt lgkmcnt(0)
	v_add_f32_e32 v122, v122, v123
	s_nop 1
	v_mov_b32_dpp v123, v122 quad_perm:[2,3,0,1] row_mask:0xf bank_mask:0xf
	s_waitcnt lgkmcnt(0)
	v_add_f32_e32 v122, v122, v123
	s_nop 1
	v_mov_b32_dpp v123, v122 quad_perm:[1,0,3,2] row_mask:0xf bank_mask:0xf
	s_waitcnt lgkmcnt(0)
	v_add_f32_e32 v122, v122, v123
	v_fmamk_f32 v236, v122, 0xba000000, v92
	v_fmamk_f32 v123, v122, 0xba000000, v94
	v_mul_f32_e32 v239, v236, v236
	v_fmac_f32_e32 v239, v123, v123
	v_fmamk_f32 v123, v122, 0xba000000, v56
	v_fmac_f32_e32 v239, v123, v123
	v_fmamk_f32 v123, v122, 0xba000000, v54
	v_fmac_f32_e32 v239, v123, v123
	v_fmamk_f32 v123, v122, 0xba000000, v95
	v_fmac_f32_e32 v239, v123, v123
	v_fmamk_f32 v123, v122, 0xba000000, v93
	v_fmac_f32_e32 v239, v123, v123
	v_fmamk_f32 v123, v122, 0xba000000, v57
	v_fmac_f32_e32 v239, v123, v123
	v_fmamk_f32 v123, v122, 0xba000000, v55
	v_fmac_f32_e32 v239, v123, v123
	v_fmamk_f32 v123, v122, 0xba000000, v235
	v_fmac_f32_e32 v239, v123, v123
	v_fmamk_f32 v123, v122, 0xba000000, v233
	v_fmac_f32_e32 v239, v123, v123
	v_fmamk_f32 v123, v122, 0xba000000, v231
	v_fmac_f32_e32 v239, v123, v123
	v_fmamk_f32 v123, v122, 0xba000000, v228
	v_fmac_f32_e32 v239, v123, v123
	v_fmamk_f32 v123, v122, 0xba000000, v234
	v_fmac_f32_e32 v239, v123, v123
	v_fmamk_f32 v123, v122, 0xba000000, v232
	v_fmac_f32_e32 v239, v123, v123
	v_fmamk_f32 v123, v122, 0xba000000, v230
	v_fmac_f32_e32 v239, v123, v123
	v_fmamk_f32 v123, v122, 0xba000000, v229
	v_fmac_f32_e32 v239, v123, v123
	v_fmamk_f32 v123, v122, 0xba000000, v226
	v_fmac_f32_e32 v239, v123, v123
	v_fmamk_f32 v123, v122, 0xba000000, v224
	v_fmac_f32_e32 v239, v123, v123
	v_fmamk_f32 v123, v122, 0xba000000, v222
	v_fmac_f32_e32 v239, v123, v123
	v_fmamk_f32 v123, v122, 0xba000000, v100
	v_fmac_f32_e32 v239, v123, v123
	v_fmamk_f32 v123, v122, 0xba000000, v227
	v_fmac_f32_e32 v239, v123, v123
	v_fmamk_f32 v123, v122, 0xba000000, v225
	v_fmac_f32_e32 v239, v123, v123
	v_fmamk_f32 v123, v122, 0xba000000, v223
	v_fmac_f32_e32 v239, v123, v123
	v_fmamk_f32 v123, v122, 0xba000000, v101
	v_fmac_f32_e32 v239, v123, v123
	v_fmamk_f32 v123, v122, 0xba000000, v99
	v_fmac_f32_e32 v239, v123, v123
	v_fmamk_f32 v123, v122, 0xba000000, v98
	v_fmac_f32_e32 v239, v123, v123
	v_fmamk_f32 v123, v122, 0xba000000, v97
	v_mul_f32_e32 v238, 0x3a000000, v122
	v_fmac_f32_e32 v239, v123, v123
	v_fmamk_f32 v122, v122, 0xba000000, v96
	v_fmac_f32_e32 v239, v122, v122
	v_pk_add_f32 v[236:237], v[90:91], v[238:239] op_sel_hi:[1,0] neg_lo:[0,1] neg_hi:[0,1]
	s_nop 0
	v_pk_mul_f32 v[236:237], v[236:237], v[236:237]
	s_nop 0
	v_add_f32_e32 v122, v237, v239
	v_add_f32_e32 v122, v236, v122
	v_pk_add_f32 v[236:237], v[88:89], v[238:239] op_sel_hi:[1,0] neg_lo:[0,1] neg_hi:[0,1]
	s_nop 0
	v_pk_mul_f32 v[236:237], v[236:237], v[236:237]
	s_nop 0
	v_add_f32_e32 v122, v237, v122
	v_add_f32_e32 v122, v236, v122
	v_mov_b32_e32 v123, v122
	s_nop 1
	v_permlane32_swap_b32_e32 v123, v122
	s_waitcnt lgkmcnt(0)
	v_add_f32_e32 v122, v122, v123
	v_mov_b32_e32 v123, v122
	s_nop 1
	v_permlane16_swap_b32_e32 v123, v122
	s_waitcnt lgkmcnt(0)
	v_add_f32_e32 v122, v122, v123
	s_nop 1
	v_mov_b32_dpp v123, v122 row_ror:8 row_mask:0xf bank_mask:0xf
	s_waitcnt lgkmcnt(0)
	v_add_f32_e32 v122, v122, v123
	s_nop 1
	v_mov_b32_dpp v123, v122 row_shr:4 row_mask:0xf bank_mask:0xa
	v_mov_b32_dpp v123, v122 row_shl:4 row_mask:0xf bank_mask:0x5
	s_waitcnt lgkmcnt(0)
	v_add_f32_e32 v122, v122, v123
	s_nop 1
	v_mov_b32_dpp v123, v122 quad_perm:[2,3,0,1] row_mask:0xf bank_mask:0xf
	s_waitcnt lgkmcnt(0)
	v_add_f32_e32 v122, v122, v123
	s_nop 1
	v_mov_b32_dpp v123, v122 quad_perm:[1,0,3,2] row_mask:0xf bank_mask:0xf
	s_waitcnt lgkmcnt(0)
	v_add_f32_e32 v122, v122, v123
	v_fmamk_f32 v122, v122, 0x3a000000, v219
	v_cmp_gt_f32_e32 vcc, s33, v122
	v_mul_f32_e32 v123, 0x4b800000, v122
	s_nop 0
	v_cndmask_b32_e32 v122, v122, v123, vcc
	v_rsq_f32_e32 v122, v122
	s_nop 0
	v_mul_f32_e32 v123, 0x45800000, v122
	v_cndmask_b32_e32 v236, v122, v123, vcc
	v_mul_f32_e64 v237, v236, -v238
	ds_read_b128 v[238:241], v112 offset:4096
	ds_read_b128 v[242:245], v112 offset:4112
	ds_read_b128 v[246:249], v112 offset:12288
	ds_read_b128 v[250:253], v112 offset:12304
	v_fma_f32 v94, v94, v236, v237
	v_fma_f32 v92, v92, v236, v237
	v_fma_f32 v93, v93, v236, v237
	s_waitcnt lgkmcnt(1)
	v_fma_f32 v122, v94, v238, v246
	v_fma_f32 v94, v95, v236, v237
	v_fma_f32 v56, v56, v236, v237
	v_fma_f32 v54, v54, v236, v237
	s_waitcnt lgkmcnt(0)
	v_fma_f32 v123, v94, v242, v250
	v_fma_f32 v92, v92, v239, v247
	v_fma_f32 v93, v93, v243, v251
	v_fma_f32 v238, v56, v240, v248
	v_fma_f32 v56, v57, v236, v237
	v_fmac_f32_e32 v249, v54, v241
	v_fma_f32 v54, v55, v236, v237
	v_fma_f32 v239, v56, v244, v252
	v_fmac_f32_e32 v253, v54, v245
	v_cvt_pk_bf16_f32 v54, v122, v92
	v_cvt_pk_bf16_f32 v55, v238, v249
	v_cvt_pk_bf16_f32 v56, v123, v93
	v_cvt_pk_fp8_f32 v122, v122, v92
	v_cvt_pk_fp8_f32 v123, v123, v93
	v_lshl_add_u64 v[94:95], v[76:77], 0, v[50:51]
	v_lshl_add_u64 v[92:93], v[78:79], 0, v[52:53]
	v_cvt_pk_fp8_f32 v122, v238, v249 op_sel:[0,0,1]
	v_cvt_pk_fp8_f32 v123, v239, v253 op_sel:[0,0,1]
	v_cvt_pk_bf16_f32 v57, v239, v253
	global_store_dwordx4 v[94:95], v[54:57], off
	v_fma_f32 v99, v99, v236, v237
	global_store_dwordx2 v[92:93], v[122:123], off
	ds_read_b128 v[238:241], v112 offset:6144
	ds_read_b128 v[242:245], v112 offset:6160
	ds_read_b128 v[54:57], v112 offset:14336
	ds_read_b128 v[50:53], v112 offset:14352
	v_fma_f32 v122, v235, v236, v237
	s_waitcnt lgkmcnt(1)
	v_fma_f32 v122, v122, v238, v54
	v_fma_f32 v54, v234, v236, v237
	s_waitcnt lgkmcnt(0)
	v_fma_f32 v123, v54, v242, v50
	v_fma_f32 v50, v233, v236, v237
	v_fma_f32 v50, v50, v239, v55
	v_fma_f32 v54, v232, v236, v237
	v_fma_f32 v55, v230, v236, v237
	v_fma_f32 v51, v54, v243, v51
	v_fma_f32 v54, v231, v236, v237
	v_fma_f32 v52, v55, v244, v52
	v_fma_f32 v55, v228, v236, v237
	v_fma_f32 v54, v54, v240, v56
	v_fmac_f32_e32 v57, v55, v241
	v_fma_f32 v55, v229, v236, v237
	v_cvt_pk_bf16_f32 v228, v122, v50
	v_cvt_pk_bf16_f32 v229, v54, v57
	v_cvt_pk_bf16_f32 v230, v123, v51
	v_cvt_pk_fp8_f32 v122, v122, v50
	v_cvt_pk_fp8_f32 v123, v123, v51
	v_fmac_f32_e32 v53, v55, v245
	v_cvt_pk_bf16_f32 v231, v52, v53
	v_cvt_pk_fp8_f32 v122, v54, v57 op_sel:[0,0,1]
	v_cvt_pk_fp8_f32 v123, v52, v53 op_sel:[0,0,1]
	global_store_dwordx4 v[94:95], v[228:231], off offset:1024
	global_store_dwordx2 v[92:93], v[122:123], off offset:512
	ds_read_b128 v[50:53], v112 offset:8192
	ds_read_b128 v[54:57], v112 offset:8208
	ds_read_b128 v[228:231], v112 offset:16384
	ds_read_b128 v[232:235], v112 offset:16400
	v_fma_f32 v122, v226, v236, v237
	s_waitcnt lgkmcnt(1)
	v_fma_f32 v122, v122, v50, v228
	v_fma_f32 v50, v227, v236, v237
	s_waitcnt lgkmcnt(0)
	v_fma_f32 v123, v50, v54, v232
	v_fma_f32 v50, v224, v236, v237
	v_fma_f32 v54, v50, v51, v229
	v_fma_f32 v50, v225, v236, v237
	v_fma_f32 v55, v50, v55, v233
	v_fma_f32 v50, v222, v236, v237
	v_fma_f32 v222, v50, v52, v230
	v_fma_f32 v50, v223, v236, v237
	v_fma_f32 v56, v50, v56, v234
	v_fma_f32 v50, v100, v236, v237
	v_fmac_f32_e32 v231, v50, v53
	v_fma_f32 v50, v101, v236, v237
	v_fmac_f32_e32 v235, v50, v57
	v_cvt_pk_bf16_f32 v50, v122, v54
	v_cvt_pk_bf16_f32 v51, v222, v231
	v_cvt_pk_bf16_f32 v52, v123, v55
	v_cvt_pk_fp8_f32 v122, v122, v54
	v_cvt_pk_fp8_f32 v123, v123, v55
	v_cvt_pk_bf16_f32 v53, v56, v235
	global_store_dwordx4 v[94:95], v[50:53], off offset:2048
	v_cvt_pk_fp8_f32 v122, v222, v231 op_sel:[0,0,1]
	v_cvt_pk_fp8_f32 v123, v56, v235 op_sel:[0,0,1]
	global_store_dwordx2 v[92:93], v[122:123], off offset:1024
	ds_read_b128 v[50:53], v112 offset:10240
	ds_read_b128 v[54:57], v112 offset:10256
	ds_read_b128 v[222:225], v112 offset:18432
	ds_read_b128 v[226:229], v112 offset:18448
	s_waitcnt lgkmcnt(1)
	v_fma_f32 v100, v99, v50, v222
	v_fma_f32 v50, v91, v236, v237
	s_waitcnt lgkmcnt(0)
	v_fma_f32 v101, v50, v54, v226
	v_fma_f32 v50, v98, v236, v237
	v_fma_f32 v54, v50, v51, v223
	v_fma_f32 v50, v90, v236, v237
	v_fma_f32 v55, v50, v55, v227
	v_fma_f32 v50, v97, v236, v237
	v_fma_f32 v90, v50, v52, v224
	v_fma_f32 v50, v89, v236, v237
	v_fma_f32 v56, v50, v56, v228
	v_fma_f32 v50, v96, v236, v237
	v_fmac_f32_e32 v225, v50, v53
	v_cvt_pk_bf16_f32 v50, v100, v54
	v_cvt_pk_bf16_f32 v51, v90, v225
	v_cvt_pk_bf16_f32 v52, v101, v55
	v_cvt_pk_fp8_f32 v100, v100, v54
	v_cvt_pk_fp8_f32 v101, v101, v55
	v_fmac_f32_e32 v237, v88, v236
	v_fmac_f32_e32 v229, v237, v57
	v_cvt_pk_fp8_f32 v100, v90, v225 op_sel:[0,0,1]
	v_cvt_pk_fp8_f32 v101, v56, v229 op_sel:[0,0,1]
	v_cvt_pk_bf16_f32 v53, v56, v229
	global_store_dwordx4 v[94:95], v[50:53], off offset:3072
	global_store_dwordx2 v[92:93], v[100:101], off offset:1536
	s_waitcnt vmcnt(19)
	v_lshlrev_b32_e32 v56, 16, v46
	v_and_b32_e32 v88, 0xffff0000, v46
	s_waitcnt vmcnt(16)
	v_lshlrev_b32_e32 v228, 16, v34
	v_and_b32_e32 v229, 0xffff0000, v34
	v_add_f32_e32 v34, 0, v56
	v_lshlrev_b32_e32 v89, 16, v47
	v_add_f32_e32 v34, v34, v88
	v_and_b32_e32 v90, 0xffff0000, v47
	v_add_f32_e32 v34, v34, v89
	v_lshlrev_b32_e32 v57, 16, v48
	v_add_f32_e32 v34, v34, v90
	v_and_b32_e32 v91, 0xffff0000, v48
	v_add_f32_e32 v34, v34, v57
	v_lshlrev_b32_e32 v92, 16, v49
	v_add_f32_e32 v34, v34, v91
	v_and_b32_e32 v93, 0xffff0000, v49
	v_add_f32_e32 v34, v34, v92
	v_lshlrev_b32_e32 v94, 16, v42
	v_add_f32_e32 v34, v34, v93
	v_and_b32_e32 v95, 0xffff0000, v42
	v_add_f32_e32 v34, v34, v94
	v_lshlrev_b32_e32 v96, 16, v43
	v_add_f32_e32 v34, v34, v95
	v_and_b32_e32 v97, 0xffff0000, v43
	v_add_f32_e32 v34, v34, v96
	v_lshlrev_b32_e32 v98, 16, v44
	v_add_f32_e32 v34, v34, v97
	v_and_b32_e32 v99, 0xffff0000, v44
	v_add_f32_e32 v34, v34, v98
	v_lshlrev_b32_e32 v100, 16, v45
	v_add_f32_e32 v34, v34, v99
	v_and_b32_e32 v101, 0xffff0000, v45
	v_add_f32_e32 v34, v34, v100
	v_lshlrev_b32_e32 v122, 16, v38
	v_add_f32_e32 v34, v34, v101
	v_and_b32_e32 v123, 0xffff0000, v38
	v_add_f32_e32 v34, v34, v122
	v_lshlrev_b32_e32 v222, 16, v39
	v_add_f32_e32 v34, v34, v123
	v_and_b32_e32 v223, 0xffff0000, v39
	v_add_f32_e32 v34, v34, v222
	v_lshlrev_b32_e32 v224, 16, v40
	v_add_f32_e32 v34, v34, v223
	v_and_b32_e32 v225, 0xffff0000, v40
	v_add_f32_e32 v34, v34, v224
	v_lshlrev_b32_e32 v226, 16, v41
	v_add_f32_e32 v34, v34, v225
	v_and_b32_e32 v227, 0xffff0000, v41
	v_add_f32_e32 v34, v34, v226
	v_add_f32_e32 v34, v34, v227
	v_add_f32_e32 v34, v34, v228
	v_lshlrev_b32_e32 v230, 16, v35
	v_add_f32_e32 v34, v34, v229
	v_and_b32_e32 v231, 0xffff0000, v35
	v_add_f32_e32 v34, v34, v230
	v_add_f32_e32 v40, v34, v231
	v_lshlrev_b32_e32 v39, 16, v36
	v_and_b32_e32 v38, 0xffff0000, v36
	v_add_f32_e32 v36, v40, v39
	v_lshlrev_b32_e32 v35, 16, v37
	v_add_f32_e32 v36, v36, v38
	v_and_b32_e32 v34, 0xffff0000, v37
	v_add_f32_e32 v36, v36, v35
	v_add_f32_e32 v36, v36, v34
	v_mov_b32_e32 v37, v36
	s_nop 1
	v_permlane32_swap_b32_e32 v37, v36
	v_lshl_add_u64 v[84:85], v[76:77], 0, v[84:85]
	s_waitcnt lgkmcnt(0)
	v_add_f32_e32 v36, v36, v37
	v_mov_b32_e32 v37, v36
	s_nop 1
	v_permlane16_swap_b32_e32 v37, v36
	s_waitcnt lgkmcnt(0)
	v_add_f32_e32 v36, v36, v37
	s_nop 1
	v_mov_b32_dpp v37, v36 row_ror:8 row_mask:0xf bank_mask:0xf
	s_waitcnt lgkmcnt(0)
	v_add_f32_e32 v36, v36, v37
	s_nop 1
	v_mov_b32_dpp v37, v36 row_shr:4 row_mask:0xf bank_mask:0xa
	v_mov_b32_dpp v37, v36 row_shl:4 row_mask:0xf bank_mask:0x5
	s_waitcnt lgkmcnt(0)
	v_add_f32_e32 v36, v36, v37
	s_nop 1
	v_mov_b32_dpp v37, v36 quad_perm:[2,3,0,1] row_mask:0xf bank_mask:0xf
	s_waitcnt lgkmcnt(0)
	v_add_f32_e32 v36, v36, v37
	s_nop 1
	v_mov_b32_dpp v37, v36 quad_perm:[1,0,3,2] row_mask:0xf bank_mask:0xf
	s_waitcnt lgkmcnt(0)
	v_add_f32_e32 v37, v36, v37
	v_fmamk_f32 v41, v37, 0xba000000, v88
	v_fmamk_f32 v40, v37, 0xba000000, v56
	v_mul_f32_e32 v42, v41, v41
	v_fmac_f32_e32 v42, v40, v40
	v_fmamk_f32 v40, v37, 0xba000000, v89
	v_fmac_f32_e32 v42, v40, v40
	v_fmamk_f32 v40, v37, 0xba000000, v90
	v_fmac_f32_e32 v42, v40, v40
	v_fmamk_f32 v40, v37, 0xba000000, v57
	v_fmac_f32_e32 v42, v40, v40
	v_fmamk_f32 v40, v37, 0xba000000, v91
	v_fmac_f32_e32 v42, v40, v40
	v_fmamk_f32 v40, v37, 0xba000000, v92
	v_fmac_f32_e32 v42, v40, v40
	v_fmamk_f32 v40, v37, 0xba000000, v93
	v_fmac_f32_e32 v42, v40, v40
	v_fmamk_f32 v40, v37, 0xba000000, v94
	v_fmac_f32_e32 v42, v40, v40
	v_fmamk_f32 v40, v37, 0xba000000, v95
	v_fmac_f32_e32 v42, v40, v40
	v_fmamk_f32 v40, v37, 0xba000000, v96
	v_fmac_f32_e32 v42, v40, v40
	v_fmamk_f32 v40, v37, 0xba000000, v97
	v_fmac_f32_e32 v42, v40, v40
	v_fmamk_f32 v40, v37, 0xba000000, v98
	v_fmac_f32_e32 v42, v40, v40
	v_fmamk_f32 v40, v37, 0xba000000, v99
	v_fmac_f32_e32 v42, v40, v40
	v_fmamk_f32 v40, v37, 0xba000000, v100
	v_fmac_f32_e32 v42, v40, v40
	v_fmamk_f32 v40, v37, 0xba000000, v101
	v_fmac_f32_e32 v42, v40, v40
	v_fmamk_f32 v40, v37, 0xba000000, v122
	v_fmac_f32_e32 v42, v40, v40
	v_fmamk_f32 v40, v37, 0xba000000, v123
	v_fmac_f32_e32 v42, v40, v40
	v_fmamk_f32 v40, v37, 0xba000000, v222
	v_fmac_f32_e32 v42, v40, v40
	v_fmamk_f32 v40, v37, 0xba000000, v223
	v_fmac_f32_e32 v42, v40, v40
	v_fmamk_f32 v40, v37, 0xba000000, v224
	v_fmac_f32_e32 v42, v40, v40
	v_fmamk_f32 v40, v37, 0xba000000, v225
	v_fmac_f32_e32 v42, v40, v40
	v_fmamk_f32 v40, v37, 0xba000000, v226
	v_fmac_f32_e32 v42, v40, v40
	v_fmamk_f32 v40, v37, 0xba000000, v227
	v_fmac_f32_e32 v42, v40, v40
	v_fmamk_f32 v40, v37, 0xba000000, v228
	v_fmac_f32_e32 v42, v40, v40
	v_fmamk_f32 v40, v37, 0xba000000, v229
	v_mul_f32_e32 v36, 0x3a000000, v37
	v_fmac_f32_e32 v42, v40, v40
	v_fmamk_f32 v40, v37, 0xba000000, v230
	v_fmamk_f32 v37, v37, 0xba000000, v231
	v_fmac_f32_e32 v42, v40, v40
	v_pk_add_f32 v[40:41], v[38:39], v[36:37] op_sel_hi:[1,0] neg_lo:[0,1] neg_hi:[0,1]
	v_fmac_f32_e32 v42, v37, v37
	v_pk_mul_f32 v[40:41], v[40:41], v[40:41]
	s_nop 0
	v_add_f32_e32 v37, v41, v42
	v_add_f32_e32 v37, v40, v37
	v_pk_add_f32 v[40:41], v[34:35], v[36:37] op_sel_hi:[1,0] neg_lo:[0,1] neg_hi:[0,1]
	s_nop 0
	v_pk_mul_f32 v[40:41], v[40:41], v[40:41]
	s_nop 0
	v_add_f32_e32 v37, v41, v37
	v_add_f32_e32 v37, v40, v37
	v_mov_b32_e32 v40, v37
	s_nop 1
	v_permlane32_swap_b32_e32 v40, v37
	s_waitcnt lgkmcnt(0)
	v_add_f32_e32 v37, v37, v40
	v_mov_b32_e32 v40, v37
	s_nop 1
	v_permlane16_swap_b32_e32 v40, v37
	s_waitcnt lgkmcnt(0)
	v_add_f32_e32 v37, v37, v40
	s_nop 1
	v_mov_b32_dpp v40, v37 row_ror:8 row_mask:0xf bank_mask:0xf
	s_waitcnt lgkmcnt(0)
	v_add_f32_e32 v37, v37, v40
	s_nop 1
	v_mov_b32_dpp v40, v37 row_shr:4 row_mask:0xf bank_mask:0xa
	v_mov_b32_dpp v40, v37 row_shl:4 row_mask:0xf bank_mask:0x5
	s_waitcnt lgkmcnt(0)
	v_add_f32_e32 v37, v37, v40
	s_nop 1
	v_mov_b32_dpp v40, v37 quad_perm:[2,3,0,1] row_mask:0xf bank_mask:0xf
	s_waitcnt lgkmcnt(0)
	v_add_f32_e32 v37, v37, v40
	s_nop 1
	v_mov_b32_dpp v40, v37 quad_perm:[1,0,3,2] row_mask:0xf bank_mask:0xf
	s_waitcnt lgkmcnt(0)
	v_add_f32_e32 v37, v37, v40
	v_fmamk_f32 v37, v37, 0x3a000000, v219
	v_mul_f32_e32 v40, 0x4b800000, v37
	v_cmp_gt_f32_e32 vcc, s33, v37
	s_nop 1
	v_cndmask_b32_e32 v37, v37, v40, vcc
	v_rsq_f32_e32 v37, v37
	s_nop 0
	v_mul_f32_e32 v40, 0x45800000, v37
	v_cndmask_b32_e32 v232, v37, v40, vcc
	ds_read_b128 v[40:43], v112 offset:12288
	ds_read_b128 v[44:47], v112 offset:4096
	ds_read_b128 v[48:51], v112 offset:4112
	ds_read_b128 v[52:55], v112 offset:12304
	v_mul_f32_e64 v233, v232, -v36
	v_fma_f32 v56, v56, v232, v233
	s_waitcnt lgkmcnt(2)
	v_fma_f32 v56, v56, v44, v40
	v_fma_f32 v40, v57, v232, v233
	v_fma_f32 v44, v89, v232, v233
	s_waitcnt lgkmcnt(0)
	v_fma_f32 v57, v40, v48, v52
	v_fma_f32 v40, v88, v232, v233
	v_fma_f32 v42, v44, v46, v42
	v_fma_f32 v44, v92, v232, v233
	v_fma_f32 v40, v40, v45, v41
	v_fma_f32 v41, v91, v232, v233
	v_fma_f32 v48, v44, v50, v54
	v_fma_f32 v44, v90, v232, v233
	v_fma_f32 v41, v41, v49, v53
	v_fmac_f32_e32 v43, v44, v47
	v_fma_f32 v44, v93, v232, v233
	v_fmac_f32_e32 v55, v44, v51
	v_cvt_pk_bf16_f32 v44, v56, v40
	v_cvt_pk_bf16_f32 v45, v42, v43
	v_cvt_pk_bf16_f32 v46, v57, v41
	v_cvt_pk_fp8_f32 v56, v56, v40
	v_cvt_pk_fp8_f32 v57, v57, v41
	v_cvt_pk_bf16_f32 v47, v48, v55
	global_store_dwordx4 v[84:85], v[44:47], off
	v_cvt_pk_fp8_f32 v56, v42, v43 op_sel:[0,0,1]
	v_cvt_pk_fp8_f32 v57, v48, v55 op_sel:[0,0,1]
	ds_read_b128 v[40:43], v112 offset:14336
	ds_read_b128 v[44:47], v112 offset:6144
	ds_read_b128 v[48:51], v112 offset:6160
	ds_read_b128 v[52:55], v112 offset:14352
	v_lshlrev_b64 v[36:37], 11, v[86:87]
	v_lshl_add_u64 v[86:87], v[78:79], 0, v[36:37]
	v_fma_f32 v36, v94, v232, v233
	s_waitcnt lgkmcnt(2)
	v_fma_f32 v36, v36, v44, v40
	v_fma_f32 v44, v96, v232, v233
	v_fma_f32 v37, v98, v232, v233
	v_fma_f32 v40, v95, v232, v233
	v_fma_f32 v42, v44, v46, v42
	v_fma_f32 v44, v100, v232, v233
	s_waitcnt lgkmcnt(0)
	v_fma_f32 v37, v37, v48, v52
	v_fma_f32 v40, v40, v45, v41
	v_fma_f32 v41, v99, v232, v233
	v_fma_f32 v48, v44, v50, v54
	v_fma_f32 v44, v97, v232, v233
	v_fma_f32 v41, v41, v49, v53
	v_fmac_f32_e32 v43, v44, v47
	v_fma_f32 v44, v101, v232, v233
	global_store_dwordx2 v[86:87], v[56:57], off
	v_fmac_f32_e32 v55, v44, v51
	v_cvt_pk_bf16_f32 v44, v36, v40
	v_cvt_pk_bf16_f32 v45, v42, v43
	v_cvt_pk_bf16_f32 v46, v37, v41
	v_cvt_pk_fp8_f32 v36, v36, v40
	v_cvt_pk_fp8_f32 v37, v37, v41
	v_cvt_pk_bf16_f32 v47, v48, v55
	global_store_dwordx4 v[84:85], v[44:47], off offset:1024
	v_cvt_pk_fp8_f32 v36, v42, v43 op_sel:[0,0,1]
	v_cvt_pk_fp8_f32 v37, v48, v55 op_sel:[0,0,1]
	ds_read_b128 v[40:43], v112 offset:16384
	ds_read_b128 v[44:47], v112 offset:8192
	ds_read_b128 v[48:51], v112 offset:8208
	ds_read_b128 v[52:55], v112 offset:16400
	v_fma_f32 v35, v35, v232, v233
	global_store_dwordx2 v[86:87], v[36:37], off offset:512
	v_fma_f32 v36, v122, v232, v233
	s_waitcnt lgkmcnt(2)
	v_fma_f32 v36, v36, v44, v40
	v_fma_f32 v44, v222, v232, v233
	v_fma_f32 v37, v224, v232, v233
	v_fma_f32 v40, v123, v232, v233
	v_fma_f32 v42, v44, v46, v42
	v_fma_f32 v44, v226, v232, v233
	s_waitcnt lgkmcnt(0)
	v_fma_f32 v37, v37, v48, v52
	v_fma_f32 v40, v40, v45, v41
	v_fma_f32 v41, v225, v232, v233
	v_fma_f32 v48, v44, v50, v54
	v_fma_f32 v44, v223, v232, v233
	v_fma_f32 v41, v41, v49, v53
	v_fmac_f32_e32 v43, v44, v47
	v_fma_f32 v44, v227, v232, v233
	v_fmac_f32_e32 v55, v44, v51
	v_cvt_pk_bf16_f32 v44, v36, v40
	v_cvt_pk_bf16_f32 v45, v42, v43
	v_cvt_pk_bf16_f32 v46, v37, v41
	v_cvt_pk_fp8_f32 v36, v36, v40
	v_cvt_pk_fp8_f32 v37, v37, v41
	v_cvt_pk_bf16_f32 v47, v48, v55
	global_store_dwordx4 v[84:85], v[44:47], off offset:2048
	v_cvt_pk_fp8_f32 v36, v42, v43 op_sel:[0,0,1]
	v_cvt_pk_fp8_f32 v37, v48, v55 op_sel:[0,0,1]
	ds_read_b128 v[40:43], v112 offset:18432
	ds_read_b128 v[44:47], v112 offset:10240
	ds_read_b128 v[48:51], v112 offset:10256
	ds_read_b128 v[52:55], v112 offset:18448
	global_store_dwordx2 v[86:87], v[36:37], off offset:1024
	v_fma_f32 v36, v228, v232, v233
	s_waitcnt lgkmcnt(2)
	v_fma_f32 v56, v36, v44, v40
	v_fma_f32 v36, v39, v232, v233
	s_waitcnt lgkmcnt(0)
	v_fma_f32 v57, v36, v48, v52
	v_fma_f32 v36, v229, v232, v233
	v_fma_f32 v39, v36, v45, v41
	v_fma_f32 v36, v38, v232, v233
	v_fma_f32 v40, v36, v49, v53
	v_fma_f32 v36, v230, v232, v233
	v_fma_f32 v41, v36, v46, v42
	v_fma_f32 v36, v231, v232, v233
	v_fmac_f32_e32 v43, v36, v47
	v_cvt_pk_bf16_f32 v36, v56, v39
	v_cvt_pk_bf16_f32 v37, v41, v43
	v_cvt_pk_bf16_f32 v38, v57, v40
	v_cvt_pk_fp8_f32 v56, v56, v39
	v_cvt_pk_fp8_f32 v57, v57, v40
	v_fmac_f32_e32 v233, v34, v232
	v_fma_f32 v35, v35, v50, v54
	v_fmac_f32_e32 v55, v233, v51
	v_cvt_pk_fp8_f32 v56, v41, v43 op_sel:[0,0,1]
	v_cvt_pk_fp8_f32 v57, v35, v55 op_sel:[0,0,1]
	v_cvt_pk_bf16_f32 v39, v35, v55
	global_store_dwordx4 v[84:85], v[36:39], off offset:3072
	global_store_dwordx2 v[86:87], v[56:57], off offset:1536
	s_waitcnt vmcnt(23)
	v_lshlrev_b32_e32 v40, 16, v30
	v_and_b32_e32 v42, 0xffff0000, v30
	s_waitcnt vmcnt(20)
	v_lshlrev_b32_e32 v90, 16, v18
	v_and_b32_e32 v91, 0xffff0000, v18
	v_add_f32_e32 v18, 0, v40
	v_lshlrev_b32_e32 v43, 16, v31
	v_add_f32_e32 v18, v18, v42
	v_and_b32_e32 v44, 0xffff0000, v31
	v_add_f32_e32 v18, v18, v43
	v_lshlrev_b32_e32 v41, 16, v32
	v_add_f32_e32 v18, v18, v44
	v_and_b32_e32 v45, 0xffff0000, v32
	v_add_f32_e32 v18, v18, v41
	v_lshlrev_b32_e32 v46, 16, v33
	v_add_f32_e32 v18, v18, v45
	v_and_b32_e32 v47, 0xffff0000, v33
	v_add_f32_e32 v18, v18, v46
	v_lshlrev_b32_e32 v48, 16, v26
	v_add_f32_e32 v18, v18, v47
	v_and_b32_e32 v49, 0xffff0000, v26
	v_add_f32_e32 v18, v18, v48
	v_lshlrev_b32_e32 v50, 16, v27
	v_add_f32_e32 v18, v18, v49
	v_and_b32_e32 v51, 0xffff0000, v27
	v_add_f32_e32 v18, v18, v50
	v_lshlrev_b32_e32 v52, 16, v28
	v_add_f32_e32 v18, v18, v51
	v_and_b32_e32 v53, 0xffff0000, v28
	v_add_f32_e32 v18, v18, v52
	v_lshlrev_b32_e32 v54, 16, v29
	v_add_f32_e32 v18, v18, v53
	v_and_b32_e32 v55, 0xffff0000, v29
	v_add_f32_e32 v18, v18, v54
	v_lshlrev_b32_e32 v56, 16, v22
	v_add_f32_e32 v18, v18, v55
	v_and_b32_e32 v57, 0xffff0000, v22
	v_add_f32_e32 v18, v18, v56
	v_lshlrev_b32_e32 v84, 16, v23
	v_add_f32_e32 v18, v18, v57
	v_and_b32_e32 v85, 0xffff0000, v23
	v_add_f32_e32 v18, v18, v84
	v_lshlrev_b32_e32 v86, 16, v24
	v_add_f32_e32 v18, v18, v85
	v_and_b32_e32 v87, 0xffff0000, v24
	v_add_f32_e32 v18, v18, v86
	v_lshlrev_b32_e32 v88, 16, v25
	v_add_f32_e32 v18, v18, v87
	v_and_b32_e32 v89, 0xffff0000, v25
	v_add_f32_e32 v18, v18, v88
	v_add_f32_e32 v18, v18, v89
	v_add_f32_e32 v18, v18, v90
	v_lshlrev_b32_e32 v92, 16, v19
	v_add_f32_e32 v18, v18, v91
	v_and_b32_e32 v93, 0xffff0000, v19
	v_add_f32_e32 v18, v18, v92
	v_add_f32_e32 v24, v18, v93
	v_lshlrev_b32_e32 v23, 16, v20
	v_and_b32_e32 v22, 0xffff0000, v20
	v_add_f32_e32 v20, v24, v23
	v_lshlrev_b32_e32 v19, 16, v21
	v_add_f32_e32 v20, v20, v22
	v_and_b32_e32 v18, 0xffff0000, v21
	v_add_f32_e32 v20, v20, v19
	v_add_f32_e32 v20, v20, v18
	v_mov_b32_e32 v21, v20
	s_nop 1
	v_permlane32_swap_b32_e32 v21, v20
	s_waitcnt lgkmcnt(0)
	v_add_f32_e32 v20, v20, v21
	v_mov_b32_e32 v21, v20
	s_nop 1
	v_permlane16_swap_b32_e32 v21, v20
	s_waitcnt lgkmcnt(0)
	v_add_f32_e32 v20, v20, v21
	s_nop 1
	v_mov_b32_dpp v21, v20 row_ror:8 row_mask:0xf bank_mask:0xf
	s_waitcnt lgkmcnt(0)
	v_add_f32_e32 v20, v20, v21
	s_nop 1
	v_mov_b32_dpp v21, v20 row_shr:4 row_mask:0xf bank_mask:0xa
	v_mov_b32_dpp v21, v20 row_shl:4 row_mask:0xf bank_mask:0x5
	s_waitcnt lgkmcnt(0)
	v_add_f32_e32 v20, v20, v21
	s_nop 1
	v_mov_b32_dpp v21, v20 quad_perm:[2,3,0,1] row_mask:0xf bank_mask:0xf
	s_waitcnt lgkmcnt(0)
	v_add_f32_e32 v20, v20, v21
	s_nop 1
	v_mov_b32_dpp v21, v20 quad_perm:[1,0,3,2] row_mask:0xf bank_mask:0xf
	s_waitcnt lgkmcnt(0)
	v_add_f32_e32 v21, v20, v21
	v_fmamk_f32 v25, v21, 0xba000000, v42
	v_fmamk_f32 v24, v21, 0xba000000, v40
	v_mul_f32_e32 v26, v25, v25
	v_fmac_f32_e32 v26, v24, v24
	v_fmamk_f32 v24, v21, 0xba000000, v43
	v_fmac_f32_e32 v26, v24, v24
	v_fmamk_f32 v24, v21, 0xba000000, v44
	v_fmac_f32_e32 v26, v24, v24
	v_fmamk_f32 v24, v21, 0xba000000, v41
	v_fmac_f32_e32 v26, v24, v24
	v_fmamk_f32 v24, v21, 0xba000000, v45
	v_fmac_f32_e32 v26, v24, v24
	v_fmamk_f32 v24, v21, 0xba000000, v46
	v_fmac_f32_e32 v26, v24, v24
	v_fmamk_f32 v24, v21, 0xba000000, v47
	v_fmac_f32_e32 v26, v24, v24
	v_fmamk_f32 v24, v21, 0xba000000, v48
	v_fmac_f32_e32 v26, v24, v24
	v_fmamk_f32 v24, v21, 0xba000000, v49
	v_fmac_f32_e32 v26, v24, v24
	v_fmamk_f32 v24, v21, 0xba000000, v50
	v_fmac_f32_e32 v26, v24, v24
	v_fmamk_f32 v24, v21, 0xba000000, v51
	v_fmac_f32_e32 v26, v24, v24
	v_fmamk_f32 v24, v21, 0xba000000, v52
	v_fmac_f32_e32 v26, v24, v24
	v_fmamk_f32 v24, v21, 0xba000000, v53
	v_fmac_f32_e32 v26, v24, v24
	v_fmamk_f32 v24, v21, 0xba000000, v54
	v_fmac_f32_e32 v26, v24, v24
	v_fmamk_f32 v24, v21, 0xba000000, v55
	v_fmac_f32_e32 v26, v24, v24
	v_fmamk_f32 v24, v21, 0xba000000, v56
	v_fmac_f32_e32 v26, v24, v24
	v_fmamk_f32 v24, v21, 0xba000000, v57
	v_fmac_f32_e32 v26, v24, v24
	v_fmamk_f32 v24, v21, 0xba000000, v84
	v_fmac_f32_e32 v26, v24, v24
	v_fmamk_f32 v24, v21, 0xba000000, v85
	v_fmac_f32_e32 v26, v24, v24
	v_fmamk_f32 v24, v21, 0xba000000, v86
	v_fmac_f32_e32 v26, v24, v24
	v_fmamk_f32 v24, v21, 0xba000000, v87
	v_fmac_f32_e32 v26, v24, v24
	v_fmamk_f32 v24, v21, 0xba000000, v88
	v_fmac_f32_e32 v26, v24, v24
	v_fmamk_f32 v24, v21, 0xba000000, v89
	v_fmac_f32_e32 v26, v24, v24
	v_fmamk_f32 v24, v21, 0xba000000, v90
	v_fmac_f32_e32 v26, v24, v24
	v_fmamk_f32 v24, v21, 0xba000000, v91
	v_mul_f32_e32 v20, 0x3a000000, v21
	v_fmac_f32_e32 v26, v24, v24
	v_fmamk_f32 v24, v21, 0xba000000, v92
	v_fmamk_f32 v21, v21, 0xba000000, v93
	v_fmac_f32_e32 v26, v24, v24
	v_pk_add_f32 v[24:25], v[22:23], v[20:21] op_sel_hi:[1,0] neg_lo:[0,1] neg_hi:[0,1]
	v_fmac_f32_e32 v26, v21, v21
	v_pk_mul_f32 v[24:25], v[24:25], v[24:25]
	s_nop 0
	v_add_f32_e32 v21, v25, v26
	v_add_f32_e32 v21, v24, v21
	v_pk_add_f32 v[24:25], v[18:19], v[20:21] op_sel_hi:[1,0] neg_lo:[0,1] neg_hi:[0,1]
	s_nop 0
	v_pk_mul_f32 v[24:25], v[24:25], v[24:25]
	s_nop 0
	v_add_f32_e32 v21, v25, v21
	v_add_f32_e32 v21, v24, v21
	v_mov_b32_e32 v24, v21
	s_nop 1
	v_permlane32_swap_b32_e32 v24, v21
	s_waitcnt lgkmcnt(0)
	v_add_f32_e32 v21, v21, v24
	v_mov_b32_e32 v24, v21
	s_nop 1
	v_permlane16_swap_b32_e32 v24, v21
	s_waitcnt lgkmcnt(0)
	v_add_f32_e32 v21, v21, v24
	s_nop 1
	v_mov_b32_dpp v24, v21 row_ror:8 row_mask:0xf bank_mask:0xf
	s_waitcnt lgkmcnt(0)
	v_add_f32_e32 v21, v21, v24
	s_nop 1
	v_mov_b32_dpp v24, v21 row_shr:4 row_mask:0xf bank_mask:0xa
	v_mov_b32_dpp v24, v21 row_shl:4 row_mask:0xf bank_mask:0x5
	s_waitcnt lgkmcnt(0)
	v_add_f32_e32 v21, v21, v24
	s_nop 1
	v_mov_b32_dpp v24, v21 quad_perm:[2,3,0,1] row_mask:0xf bank_mask:0xf
	s_waitcnt lgkmcnt(0)
	v_add_f32_e32 v21, v21, v24
	s_nop 1
	v_mov_b32_dpp v24, v21 quad_perm:[1,0,3,2] row_mask:0xf bank_mask:0xf
	s_waitcnt lgkmcnt(0)
	v_add_f32_e32 v21, v21, v24
	v_fmamk_f32 v21, v21, 0x3a000000, v219
	v_mul_f32_e32 v24, 0x4b800000, v21
	v_cmp_gt_f32_e32 vcc, s33, v21
	s_nop 1
	v_cndmask_b32_e32 v21, v21, v24, vcc
	v_rsq_f32_e32 v21, v21
	s_nop 0
	v_mul_f32_e32 v24, 0x45800000, v21
	v_cndmask_b32_e32 v94, v21, v24, vcc
	ds_read_b128 v[24:27], v112 offset:12288
	ds_read_b128 v[28:31], v112 offset:4096
	ds_read_b128 v[32:35], v112 offset:4112
	ds_read_b128 v[36:39], v112 offset:12304
	v_mul_f32_e64 v95, v94, -v20
	v_fma_f32 v40, v40, v94, v95
	s_waitcnt lgkmcnt(2)
	v_fma_f32 v40, v40, v28, v24
	v_fma_f32 v24, v41, v94, v95
	v_fma_f32 v28, v43, v94, v95
	s_waitcnt lgkmcnt(0)
	v_fma_f32 v41, v24, v32, v36
	v_fma_f32 v24, v42, v94, v95
	v_fma_f32 v26, v28, v30, v26
	v_fma_f32 v28, v46, v94, v95
	v_fma_f32 v24, v24, v29, v25
	v_fma_f32 v25, v45, v94, v95
	v_fma_f32 v32, v28, v34, v38
	v_fma_f32 v28, v44, v94, v95
	v_fma_f32 v25, v25, v33, v37
	v_fmac_f32_e32 v27, v28, v31
	v_fma_f32 v28, v47, v94, v95
	v_fmac_f32_e32 v39, v28, v35
	v_cvt_pk_bf16_f32 v28, v40, v24
	v_cvt_pk_bf16_f32 v29, v26, v27
	v_cvt_pk_bf16_f32 v30, v41, v25
	v_cvt_pk_fp8_f32 v40, v40, v24
	v_cvt_pk_fp8_f32 v41, v41, v25
	v_lshl_add_u64 v[42:43], v[76:77], 0, v[62:63]
	v_cvt_pk_bf16_f32 v31, v32, v39
	global_store_dwordx4 v[42:43], v[28:31], off
	v_cvt_pk_fp8_f32 v40, v26, v27 op_sel:[0,0,1]
	v_cvt_pk_fp8_f32 v41, v32, v39 op_sel:[0,0,1]
	ds_read_b128 v[24:27], v112 offset:14336
	ds_read_b128 v[28:31], v112 offset:6144
	ds_read_b128 v[32:35], v112 offset:6160
	ds_read_b128 v[36:39], v112 offset:14352
	v_lshlrev_b64 v[20:21], 11, v[64:65]
	v_lshl_add_u64 v[44:45], v[78:79], 0, v[20:21]
	v_fma_f32 v20, v48, v94, v95
	s_waitcnt lgkmcnt(2)
	v_fma_f32 v20, v20, v28, v24
	v_fma_f32 v28, v50, v94, v95
	v_fma_f32 v21, v52, v94, v95
	v_fma_f32 v24, v49, v94, v95
	v_fma_f32 v26, v28, v30, v26
	v_fma_f32 v28, v54, v94, v95
	s_waitcnt lgkmcnt(0)
	v_fma_f32 v21, v21, v32, v36
	v_fma_f32 v24, v24, v29, v25
	v_fma_f32 v25, v53, v94, v95
	v_fma_f32 v32, v28, v34, v38
	v_fma_f32 v28, v51, v94, v95
	v_fma_f32 v25, v25, v33, v37
	v_fmac_f32_e32 v27, v28, v31
	v_fma_f32 v28, v55, v94, v95
	global_store_dwordx2 v[44:45], v[40:41], off
	v_fmac_f32_e32 v39, v28, v35
	v_cvt_pk_bf16_f32 v28, v20, v24
	v_cvt_pk_bf16_f32 v29, v26, v27
	v_cvt_pk_bf16_f32 v30, v21, v25
	v_cvt_pk_fp8_f32 v20, v20, v24
	v_cvt_pk_fp8_f32 v21, v21, v25
	v_cvt_pk_bf16_f32 v31, v32, v39
	global_store_dwordx4 v[42:43], v[28:31], off offset:1024
	v_cvt_pk_fp8_f32 v20, v26, v27 op_sel:[0,0,1]
	v_cvt_pk_fp8_f32 v21, v32, v39 op_sel:[0,0,1]
	ds_read_b128 v[24:27], v112 offset:16384
	ds_read_b128 v[28:31], v112 offset:8192
	ds_read_b128 v[32:35], v112 offset:8208
	ds_read_b128 v[36:39], v112 offset:16400
	v_fma_f32 v19, v19, v94, v95
	global_store_dwordx2 v[44:45], v[20:21], off offset:512
	v_fma_f32 v20, v56, v94, v95
	s_waitcnt lgkmcnt(2)
	v_fma_f32 v20, v20, v28, v24
	v_fma_f32 v28, v84, v94, v95
	v_fma_f32 v21, v86, v94, v95
	v_fma_f32 v24, v57, v94, v95
	v_fma_f32 v26, v28, v30, v26
	v_fma_f32 v28, v88, v94, v95
	s_waitcnt lgkmcnt(0)
	v_fma_f32 v21, v21, v32, v36
	v_fma_f32 v24, v24, v29, v25
	v_fma_f32 v25, v87, v94, v95
	v_fma_f32 v32, v28, v34, v38
	v_fma_f32 v28, v85, v94, v95
	v_fma_f32 v25, v25, v33, v37
	v_fmac_f32_e32 v27, v28, v31
	v_fma_f32 v28, v89, v94, v95
	v_fmac_f32_e32 v39, v28, v35
	v_cvt_pk_bf16_f32 v28, v20, v24
	v_cvt_pk_bf16_f32 v29, v26, v27
	v_cvt_pk_bf16_f32 v30, v21, v25
	v_cvt_pk_fp8_f32 v20, v20, v24
	v_cvt_pk_fp8_f32 v21, v21, v25
	v_cvt_pk_bf16_f32 v31, v32, v39
	global_store_dwordx4 v[42:43], v[28:31], off offset:2048
	v_cvt_pk_fp8_f32 v20, v26, v27 op_sel:[0,0,1]
	v_cvt_pk_fp8_f32 v21, v32, v39 op_sel:[0,0,1]
	ds_read_b128 v[24:27], v112 offset:18432
	ds_read_b128 v[28:31], v112 offset:10240
	ds_read_b128 v[32:35], v112 offset:10256
	ds_read_b128 v[36:39], v112 offset:18448
	global_store_dwordx2 v[44:45], v[20:21], off offset:1024
	v_fma_f32 v20, v90, v94, v95
	s_waitcnt lgkmcnt(2)
	v_fma_f32 v40, v20, v28, v24
	v_fma_f32 v20, v23, v94, v95
	s_waitcnt lgkmcnt(0)
	v_fma_f32 v41, v20, v32, v36
	v_fma_f32 v20, v91, v94, v95
	v_fma_f32 v23, v20, v29, v25
	v_fma_f32 v20, v22, v94, v95
	v_fma_f32 v24, v20, v33, v37
	v_fma_f32 v20, v92, v94, v95
	v_fma_f32 v25, v20, v30, v26
	v_fma_f32 v20, v93, v94, v95
	v_fmac_f32_e32 v27, v20, v31
	v_cvt_pk_bf16_f32 v20, v40, v23
	v_cvt_pk_bf16_f32 v21, v25, v27
	v_cvt_pk_bf16_f32 v22, v41, v24
	v_cvt_pk_fp8_f32 v40, v40, v23
	v_cvt_pk_fp8_f32 v41, v41, v24
	v_fmac_f32_e32 v95, v18, v94
	v_fma_f32 v19, v19, v34, v38
	v_fmac_f32_e32 v39, v95, v35
	v_cvt_pk_fp8_f32 v40, v25, v27 op_sel:[0,0,1]
	v_cvt_pk_fp8_f32 v41, v19, v39 op_sel:[0,0,1]
	v_cvt_pk_bf16_f32 v23, v19, v39
	global_store_dwordx4 v[42:43], v[20:23], off offset:3072
	global_store_dwordx2 v[44:45], v[40:41], off offset:1536
	s_waitcnt vmcnt(27)
	v_lshlrev_b32_e32 v24, 16, v14
	v_and_b32_e32 v26, 0xffff0000, v14
	s_waitcnt vmcnt(24)
	v_lshlrev_b32_e32 v48, 16, v2
	v_and_b32_e32 v49, 0xffff0000, v2
	v_add_f32_e32 v2, 0, v24
	v_lshlrev_b32_e32 v27, 16, v15
	v_add_f32_e32 v2, v2, v26
	v_and_b32_e32 v28, 0xffff0000, v15
	v_add_f32_e32 v2, v2, v27
	v_lshlrev_b32_e32 v25, 16, v16
	v_add_f32_e32 v2, v2, v28
	v_and_b32_e32 v29, 0xffff0000, v16
	v_add_f32_e32 v2, v2, v25
	v_lshlrev_b32_e32 v30, 16, v17
	v_add_f32_e32 v2, v2, v29
	v_and_b32_e32 v31, 0xffff0000, v17
	v_add_f32_e32 v2, v2, v30
	v_lshlrev_b32_e32 v32, 16, v10
	v_add_f32_e32 v2, v2, v31
	v_and_b32_e32 v33, 0xffff0000, v10
	v_add_f32_e32 v2, v2, v32
	v_lshlrev_b32_e32 v34, 16, v11
	v_add_f32_e32 v2, v2, v33
	v_and_b32_e32 v35, 0xffff0000, v11
	v_add_f32_e32 v2, v2, v34
	v_lshlrev_b32_e32 v36, 16, v12
	v_add_f32_e32 v2, v2, v35
	v_and_b32_e32 v37, 0xffff0000, v12
	v_add_f32_e32 v2, v2, v36
	v_lshlrev_b32_e32 v38, 16, v13
	v_add_f32_e32 v2, v2, v37
	v_and_b32_e32 v39, 0xffff0000, v13
	v_add_f32_e32 v2, v2, v38
	v_lshlrev_b32_e32 v40, 16, v6
	v_add_f32_e32 v2, v2, v39
	v_and_b32_e32 v41, 0xffff0000, v6
	v_add_f32_e32 v2, v2, v40
	v_lshlrev_b32_e32 v42, 16, v7
	v_add_f32_e32 v2, v2, v41
	v_and_b32_e32 v43, 0xffff0000, v7
	v_add_f32_e32 v2, v2, v42
	v_lshlrev_b32_e32 v44, 16, v8
	v_add_f32_e32 v2, v2, v43
	v_and_b32_e32 v45, 0xffff0000, v8
	v_add_f32_e32 v2, v2, v44
	v_lshlrev_b32_e32 v46, 16, v9
	v_add_f32_e32 v2, v2, v45
	v_and_b32_e32 v47, 0xffff0000, v9
	v_add_f32_e32 v2, v2, v46
	v_add_f32_e32 v2, v2, v47
	v_add_f32_e32 v2, v2, v48
	v_lshlrev_b32_e32 v50, 16, v3
	v_add_f32_e32 v2, v2, v49
	v_and_b32_e32 v51, 0xffff0000, v3
	v_add_f32_e32 v2, v2, v50
	v_add_f32_e32 v8, v2, v51
	v_lshlrev_b32_e32 v7, 16, v4
	v_and_b32_e32 v6, 0xffff0000, v4
	v_add_f32_e32 v4, v8, v7
	v_lshlrev_b32_e32 v3, 16, v5
	v_add_f32_e32 v4, v4, v6
	v_and_b32_e32 v2, 0xffff0000, v5
	v_add_f32_e32 v4, v4, v3
	v_add_f32_e32 v4, v4, v2
	v_mov_b32_e32 v5, v4
	s_nop 1
	v_permlane32_swap_b32_e32 v5, v4
	s_waitcnt lgkmcnt(0)
	v_add_f32_e32 v4, v4, v5
	v_mov_b32_e32 v5, v4
	s_nop 1
	v_permlane16_swap_b32_e32 v5, v4
	s_waitcnt lgkmcnt(0)
	v_add_f32_e32 v4, v4, v5
	s_nop 1
	v_mov_b32_dpp v5, v4 row_ror:8 row_mask:0xf bank_mask:0xf
	s_waitcnt lgkmcnt(0)
	v_add_f32_e32 v4, v4, v5
	s_nop 1
	v_mov_b32_dpp v5, v4 row_shr:4 row_mask:0xf bank_mask:0xa
	v_mov_b32_dpp v5, v4 row_shl:4 row_mask:0xf bank_mask:0x5
	s_waitcnt lgkmcnt(0)
	v_add_f32_e32 v4, v4, v5
	s_nop 1
	v_mov_b32_dpp v5, v4 quad_perm:[2,3,0,1] row_mask:0xf bank_mask:0xf
	s_waitcnt lgkmcnt(0)
	v_add_f32_e32 v4, v4, v5
	s_nop 1
	v_mov_b32_dpp v5, v4 quad_perm:[1,0,3,2] row_mask:0xf bank_mask:0xf
	s_waitcnt lgkmcnt(0)
	v_add_f32_e32 v5, v4, v5
	v_fmamk_f32 v9, v5, 0xba000000, v26
	v_fmamk_f32 v8, v5, 0xba000000, v24
	v_mul_f32_e32 v10, v9, v9
	v_fmac_f32_e32 v10, v8, v8
	v_fmamk_f32 v8, v5, 0xba000000, v27
	v_fmac_f32_e32 v10, v8, v8
	v_fmamk_f32 v8, v5, 0xba000000, v28
	v_fmac_f32_e32 v10, v8, v8
	v_fmamk_f32 v8, v5, 0xba000000, v25
	v_fmac_f32_e32 v10, v8, v8
	v_fmamk_f32 v8, v5, 0xba000000, v29
	v_fmac_f32_e32 v10, v8, v8
	v_fmamk_f32 v8, v5, 0xba000000, v30
	v_fmac_f32_e32 v10, v8, v8
	v_fmamk_f32 v8, v5, 0xba000000, v31
	v_fmac_f32_e32 v10, v8, v8
	v_fmamk_f32 v8, v5, 0xba000000, v32
	v_fmac_f32_e32 v10, v8, v8
	v_fmamk_f32 v8, v5, 0xba000000, v33
	v_fmac_f32_e32 v10, v8, v8
	v_fmamk_f32 v8, v5, 0xba000000, v34
	v_fmac_f32_e32 v10, v8, v8
	v_fmamk_f32 v8, v5, 0xba000000, v35
	v_fmac_f32_e32 v10, v8, v8
	v_fmamk_f32 v8, v5, 0xba000000, v36
	v_fmac_f32_e32 v10, v8, v8
	v_fmamk_f32 v8, v5, 0xba000000, v37
	v_fmac_f32_e32 v10, v8, v8
	v_fmamk_f32 v8, v5, 0xba000000, v38
	v_fmac_f32_e32 v10, v8, v8
	v_fmamk_f32 v8, v5, 0xba000000, v39
	v_fmac_f32_e32 v10, v8, v8
	v_fmamk_f32 v8, v5, 0xba000000, v40
	v_fmac_f32_e32 v10, v8, v8
	v_fmamk_f32 v8, v5, 0xba000000, v41
	v_fmac_f32_e32 v10, v8, v8
	v_fmamk_f32 v8, v5, 0xba000000, v42
	v_fmac_f32_e32 v10, v8, v8
	v_fmamk_f32 v8, v5, 0xba000000, v43
	v_fmac_f32_e32 v10, v8, v8
	v_fmamk_f32 v8, v5, 0xba000000, v44
	v_fmac_f32_e32 v10, v8, v8
	v_fmamk_f32 v8, v5, 0xba000000, v45
	v_fmac_f32_e32 v10, v8, v8
	v_fmamk_f32 v8, v5, 0xba000000, v46
	v_fmac_f32_e32 v10, v8, v8
	v_fmamk_f32 v8, v5, 0xba000000, v47
	v_fmac_f32_e32 v10, v8, v8
	v_fmamk_f32 v8, v5, 0xba000000, v48
	v_fmac_f32_e32 v10, v8, v8
	v_fmamk_f32 v8, v5, 0xba000000, v49
	v_mul_f32_e32 v4, 0x3a000000, v5
	v_fmac_f32_e32 v10, v8, v8
	v_fmamk_f32 v8, v5, 0xba000000, v50
	v_fmamk_f32 v5, v5, 0xba000000, v51
	v_fmac_f32_e32 v10, v8, v8
	v_pk_add_f32 v[8:9], v[6:7], v[4:5] op_sel_hi:[1,0] neg_lo:[0,1] neg_hi:[0,1]
	v_fmac_f32_e32 v10, v5, v5
	v_pk_mul_f32 v[8:9], v[8:9], v[8:9]
	s_nop 0
	v_add_f32_e32 v5, v9, v10
	v_add_f32_e32 v5, v8, v5
	v_pk_add_f32 v[8:9], v[2:3], v[4:5] op_sel_hi:[1,0] neg_lo:[0,1] neg_hi:[0,1]
	s_nop 0
	v_pk_mul_f32 v[8:9], v[8:9], v[8:9]
	s_nop 0
	v_add_f32_e32 v5, v9, v5
	v_add_f32_e32 v5, v8, v5
	v_mov_b32_e32 v8, v5
	s_nop 1
	v_permlane32_swap_b32_e32 v8, v5
	s_waitcnt lgkmcnt(0)
	v_add_f32_e32 v5, v5, v8
	v_mov_b32_e32 v8, v5
	s_nop 1
	v_permlane16_swap_b32_e32 v8, v5
	s_waitcnt lgkmcnt(0)
	v_add_f32_e32 v5, v5, v8
	s_nop 1
	v_mov_b32_dpp v8, v5 row_ror:8 row_mask:0xf bank_mask:0xf
	s_waitcnt lgkmcnt(0)
	v_add_f32_e32 v5, v5, v8
	s_nop 1
	v_mov_b32_dpp v8, v5 row_shr:4 row_mask:0xf bank_mask:0xa
	v_mov_b32_dpp v8, v5 row_shl:4 row_mask:0xf bank_mask:0x5
	s_waitcnt lgkmcnt(0)
	v_add_f32_e32 v5, v5, v8
	s_nop 1
	v_mov_b32_dpp v8, v5 quad_perm:[2,3,0,1] row_mask:0xf bank_mask:0xf
	s_waitcnt lgkmcnt(0)
	v_add_f32_e32 v5, v5, v8
	s_nop 1
	v_mov_b32_dpp v8, v5 quad_perm:[1,0,3,2] row_mask:0xf bank_mask:0xf
	s_waitcnt lgkmcnt(0)
	v_add_f32_e32 v5, v5, v8
	v_fmamk_f32 v5, v5, 0x3a000000, v219
	v_mul_f32_e32 v8, 0x4b800000, v5
	v_cmp_gt_f32_e32 vcc, s33, v5
	s_nop 1
	v_cndmask_b32_e32 v5, v5, v8, vcc
	v_rsq_f32_e32 v5, v5
	s_nop 0
	v_mul_f32_e32 v8, 0x45800000, v5
	v_cndmask_b32_e32 v52, v5, v8, vcc
	ds_read_b128 v[8:11], v112 offset:12288
	ds_read_b128 v[12:15], v112 offset:4096
	ds_read_b128 v[16:19], v112 offset:4112
	ds_read_b128 v[20:23], v112 offset:12304
	v_mul_f32_e64 v53, v52, -v4
	v_fma_f32 v24, v24, v52, v53
	s_waitcnt lgkmcnt(2)
	v_fma_f32 v24, v24, v12, v8
	v_fma_f32 v8, v25, v52, v53
	v_fma_f32 v12, v27, v52, v53
	s_waitcnt lgkmcnt(0)
	v_fma_f32 v25, v8, v16, v20
	v_fma_f32 v8, v26, v52, v53
	v_fma_f32 v10, v12, v14, v10
	v_fma_f32 v12, v30, v52, v53
	v_fma_f32 v8, v8, v13, v9
	v_fma_f32 v9, v29, v52, v53
	v_fma_f32 v16, v12, v18, v22
	v_fma_f32 v12, v28, v52, v53
	v_fma_f32 v9, v9, v17, v21
	v_fmac_f32_e32 v11, v12, v15
	v_fma_f32 v12, v31, v52, v53
	v_fmac_f32_e32 v23, v12, v19
	v_cvt_pk_bf16_f32 v12, v24, v8
	v_cvt_pk_bf16_f32 v13, v10, v11
	v_cvt_pk_bf16_f32 v14, v25, v9
	v_cvt_pk_fp8_f32 v24, v24, v8
	v_cvt_pk_fp8_f32 v25, v25, v9
	v_lshl_add_u64 v[26:27], v[76:77], 0, v[58:59]
	v_cvt_pk_bf16_f32 v15, v16, v23
	global_store_dwordx4 v[26:27], v[12:15], off
	v_cvt_pk_fp8_f32 v24, v10, v11 op_sel:[0,0,1]
	v_cvt_pk_fp8_f32 v25, v16, v23 op_sel:[0,0,1]
	ds_read_b128 v[8:11], v112 offset:14336
	ds_read_b128 v[12:15], v112 offset:6144
	ds_read_b128 v[16:19], v112 offset:6160
	ds_read_b128 v[20:23], v112 offset:14352
	v_lshlrev_b64 v[4:5], 11, v[60:61]
	v_lshl_add_u64 v[28:29], v[78:79], 0, v[4:5]
	v_fma_f32 v4, v32, v52, v53
	s_waitcnt lgkmcnt(2)
	v_fma_f32 v4, v4, v12, v8
	v_fma_f32 v12, v34, v52, v53
	v_fma_f32 v5, v36, v52, v53
	v_fma_f32 v8, v33, v52, v53
	v_fma_f32 v10, v12, v14, v10
	v_fma_f32 v12, v38, v52, v53
	s_waitcnt lgkmcnt(0)
	v_fma_f32 v5, v5, v16, v20
	v_fma_f32 v8, v8, v13, v9
	v_fma_f32 v9, v37, v52, v53
	v_fma_f32 v16, v12, v18, v22
	v_fma_f32 v12, v35, v52, v53
	v_fma_f32 v9, v9, v17, v21
	v_fmac_f32_e32 v11, v12, v15
	v_fma_f32 v12, v39, v52, v53
	global_store_dwordx2 v[28:29], v[24:25], off
	v_fmac_f32_e32 v23, v12, v19
	v_cvt_pk_bf16_f32 v12, v4, v8
	v_cvt_pk_bf16_f32 v13, v10, v11
	v_cvt_pk_bf16_f32 v14, v5, v9
	v_cvt_pk_fp8_f32 v4, v4, v8
	v_cvt_pk_fp8_f32 v5, v5, v9
	v_cvt_pk_bf16_f32 v15, v16, v23
	global_store_dwordx4 v[26:27], v[12:15], off offset:1024
	v_cvt_pk_fp8_f32 v4, v10, v11 op_sel:[0,0,1]
	v_cvt_pk_fp8_f32 v5, v16, v23 op_sel:[0,0,1]
	ds_read_b128 v[8:11], v112 offset:16384
	ds_read_b128 v[12:15], v112 offset:8192
	ds_read_b128 v[16:19], v112 offset:8208
	ds_read_b128 v[20:23], v112 offset:16400
	v_fma_f32 v3, v3, v52, v53
	global_store_dwordx2 v[28:29], v[4:5], off offset:512
	v_fma_f32 v4, v40, v52, v53
	s_waitcnt lgkmcnt(2)
	v_fma_f32 v4, v4, v12, v8
	v_fma_f32 v12, v42, v52, v53
	v_fma_f32 v5, v44, v52, v53
	v_fma_f32 v8, v41, v52, v53
	v_fma_f32 v10, v12, v14, v10
	v_fma_f32 v12, v46, v52, v53
	s_waitcnt lgkmcnt(0)
	v_fma_f32 v5, v5, v16, v20
	v_fma_f32 v8, v8, v13, v9
	v_fma_f32 v9, v45, v52, v53
	v_fma_f32 v16, v12, v18, v22
	v_fma_f32 v12, v43, v52, v53
	v_fma_f32 v9, v9, v17, v21
	v_fmac_f32_e32 v11, v12, v15
	v_fma_f32 v12, v47, v52, v53
	v_fmac_f32_e32 v23, v12, v19
	v_cvt_pk_bf16_f32 v12, v4, v8
	v_cvt_pk_bf16_f32 v13, v10, v11
	v_cvt_pk_bf16_f32 v14, v5, v9
	v_cvt_pk_fp8_f32 v4, v4, v8
	v_cvt_pk_fp8_f32 v5, v5, v9
	v_cvt_pk_bf16_f32 v15, v16, v23
	global_store_dwordx4 v[26:27], v[12:15], off offset:2048
	v_cvt_pk_fp8_f32 v4, v10, v11 op_sel:[0,0,1]
	v_cvt_pk_fp8_f32 v5, v16, v23 op_sel:[0,0,1]
	ds_read_b128 v[8:11], v112 offset:18432
	ds_read_b128 v[12:15], v112 offset:10240
	ds_read_b128 v[16:19], v112 offset:10256
	ds_read_b128 v[20:23], v112 offset:18448
	global_store_dwordx2 v[28:29], v[4:5], off offset:1024
	v_fma_f32 v4, v48, v52, v53
	s_waitcnt lgkmcnt(2)
	v_fma_f32 v24, v4, v12, v8
	v_fma_f32 v4, v7, v52, v53
	s_waitcnt lgkmcnt(0)
	v_fma_f32 v25, v4, v16, v20
	v_fma_f32 v4, v49, v52, v53
	v_fma_f32 v7, v4, v13, v9
	v_fma_f32 v4, v6, v52, v53
	v_fma_f32 v8, v4, v17, v21
	v_fma_f32 v4, v50, v52, v53
	v_fma_f32 v9, v4, v14, v10
	v_fma_f32 v4, v51, v52, v53
	v_fmac_f32_e32 v11, v4, v15
	v_cvt_pk_bf16_f32 v4, v24, v7
	v_cvt_pk_bf16_f32 v5, v9, v11
	v_cvt_pk_bf16_f32 v6, v25, v8
	v_cvt_pk_fp8_f32 v24, v24, v7
	v_cvt_pk_fp8_f32 v25, v25, v8
	v_fmac_f32_e32 v53, v2, v52
	v_fma_f32 v3, v3, v18, v22
	v_fmac_f32_e32 v23, v53, v19
	v_cvt_pk_fp8_f32 v24, v9, v11 op_sel:[0,0,1]
	v_cvt_pk_fp8_f32 v25, v3, v23 op_sel:[0,0,1]
	v_cvt_pk_bf16_f32 v7, v3, v23
	global_store_dwordx4 v[26:27], v[4:7], off offset:3072
	global_store_dwordx2 v[28:29], v[24:25], off offset:1536
	s_mov_b32 s0, 4
	s_andn2_b64 vcc, exec, s[26:27]
	s_mov_b64 s[26:27], 0
	s_cbranch_vccz .LBB0_1026
	v_ashrrev_i32_e32 v83, 31, v82
	s_waitcnt vmcnt(0)
	v_lshlrev_b64 v[2:3], 12, v[82:83]
	v_mov_b32_e32 v30, 0
	v_lshl_add_u64 v[84:85], v[80:81], 0, v[2:3]
	s_mov_b64 s[42:43], 0
	v_mov_b32_e32 v31, v30
	v_mov_b32_e32 v32, v30
	v_mov_b32_e32 v33, v30
	v_mov_b32_e32 v6, v30
	v_mov_b32_e32 v7, v30
	v_mov_b32_e32 v8, v30
	v_mov_b32_e32 v9, v30
	v_mov_b32_e32 v14, v30
	v_mov_b32_e32 v15, v30
	v_mov_b32_e32 v16, v30
	v_mov_b32_e32 v17, v30
	v_mov_b32_e32 v26, v30
	v_mov_b32_e32 v27, v30
	v_mov_b32_e32 v28, v30
	v_mov_b32_e32 v29, v30
	v_mov_b32_e32 v2, v30
	v_mov_b32_e32 v3, v30
	v_mov_b32_e32 v4, v30
	v_mov_b32_e32 v5, v30
	v_mov_b32_e32 v10, v30
	v_mov_b32_e32 v11, v30
	v_mov_b32_e32 v12, v30
	v_mov_b32_e32 v13, v30
	v_mov_b32_e32 v18, v30
	v_mov_b32_e32 v19, v30
	v_mov_b32_e32 v20, v30
	v_mov_b32_e32 v21, v30
	v_mov_b32_e32 v34, v30
	v_mov_b32_e32 v35, v30
	v_mov_b32_e32 v36, v30
	v_mov_b32_e32 v37, v30
	v_mov_b32_e32 v38, v30
	v_mov_b32_e32 v39, v30
	v_mov_b32_e32 v40, v30
	v_mov_b32_e32 v41, v30
	v_mov_b32_e32 v42, v30
	v_mov_b32_e32 v43, v30
	v_mov_b32_e32 v44, v30
	v_mov_b32_e32 v45, v30
	v_mov_b32_e32 v46, v30
	v_mov_b32_e32 v47, v30
	v_mov_b32_e32 v48, v30
	v_mov_b32_e32 v49, v30
	v_mov_b32_e32 v50, v30
	v_mov_b32_e32 v51, v30
	v_mov_b32_e32 v52, v30
	v_mov_b32_e32 v53, v30
	v_mov_b32_e32 v54, v30
	v_mov_b32_e32 v55, v30
	v_mov_b32_e32 v56, v30
	v_mov_b32_e32 v57, v30
	v_mov_b32_e32 v58, v30
	v_mov_b32_e32 v59, v30
	v_mov_b32_e32 v60, v30
	v_mov_b32_e32 v61, v30
	v_mov_b32_e32 v62, v30
	v_mov_b32_e32 v63, v30
	v_mov_b32_e32 v64, v30
	v_mov_b32_e32 v65, v30
	v_mov_b32_e32 v22, v30
	v_mov_b32_e32 v23, v30
	v_mov_b32_e32 v24, v30
	v_mov_b32_e32 v25, v30
	s_barrier

.LBB0_1734:
	v_ashrrev_i32_e32 v73, 31, v72
	v_ashrrev_i32_e32 v67, 31, v66
	v_lshl_add_u64 v[80:81], v[72:73], 2, s[8:9]
	v_lshlrev_b64 v[82:83], 12, v[66:67]
	global_load_dword v100, v[80:81], off sc1
	global_load_dword v102, v[80:81], off offset:4 sc1
	global_load_dword v104, v[80:81], off offset:8 sc1
	global_load_dword v106, v[80:81], off offset:12 sc1
	global_load_dword v108, v[80:81], off offset:16 sc1
	global_load_dword v110, v[80:81], off offset:20 sc1
	global_load_dword v112, v[80:81], off offset:24 sc1
	global_load_dword v114, v[80:81], off offset:28 sc1
	v_lshlrev_b64 v[84:85], 13, v[66:67]
	v_lshl_add_u64 v[80:81], v[70:71], 0, v[82:83]
	v_lshl_add_u64 v[124:125], s[10:11], 0, v[84:85]
	global_load_dwordx4 v[84:87], v[80:81], off offset:3072 nt
	global_load_dwordx4 v[88:91], v[80:81], off nt
	global_load_dwordx4 v[92:95], v[80:81], off offset:1024 nt
	global_load_dwordx4 v[96:99], v[80:81], off offset:2048 nt
	v_add_u32_e32 v78, v116, v66
	v_ashrrev_i32_e32 v79, 31, v78
	v_lshlrev_b64 v[78:79], 11, v[78:79]
	v_mov_b32_e32 v75, v65
	v_mov_b32_e32 v77, v65
	v_lshl_add_u64 v[126:127], v[68:69], 0, v[78:79]
	v_lshl_add_u64 v[82:83], v[124:125], 0, v[64:65]
	v_lshl_add_u64 v[80:81], v[124:125], 0, v[74:75]
	v_lshl_add_u64 v[78:79], v[124:125], 0, v[76:77]
	global_load_dwordx2 v[124:125], v[126:127], off nt
	global_load_dwordx2 v[128:129], v[126:127], off offset:512 nt
	global_load_dwordx2 v[130:131], v[126:127], off offset:1024 nt
	global_load_dwordx2 v[132:133], v[126:127], off offset:1536 nt
	v_add_u32_e32 v66, s5, v66
	v_cmp_lt_i32_e32 vcc, s7, v66
	s_or_b64 s[0:1], vcc, s[0:1]
	v_add_u32_e32 v72, s3, v72
	s_waitcnt vmcnt(15)
	v_ashrrev_i32_e32 v101, 31, v100
	s_waitcnt vmcnt(14)
	v_ashrrev_i32_e32 v103, 31, v102
	s_waitcnt vmcnt(13)
	v_ashrrev_i32_e32 v105, 31, v104
	s_waitcnt vmcnt(12)
	v_ashrrev_i32_e32 v107, 31, v106
	s_waitcnt vmcnt(11)
	v_ashrrev_i32_e32 v109, 31, v108
	s_waitcnt vmcnt(10)
	v_ashrrev_i32_e32 v111, 31, v110
	s_waitcnt vmcnt(9)
	v_ashrrev_i32_e32 v113, 31, v112
	s_waitcnt vmcnt(8)
	v_ashrrev_i32_e32 v115, 31, v114
	v_lshlrev_b64 v[100:101], 11, v[100:101]
	v_lshlrev_b64 v[102:103], 11, v[102:103]
	v_lshlrev_b64 v[104:105], 11, v[104:105]
	v_lshlrev_b64 v[106:107], 11, v[106:107]
	v_lshlrev_b64 v[108:109], 11, v[108:109]
	v_lshlrev_b64 v[110:111], 11, v[110:111]
	v_lshlrev_b64 v[112:113], 11, v[112:113]
	v_lshlrev_b64 v[114:115], 11, v[114:115]
	s_waitcnt vmcnt(7)
	v_and_b32_e32 v127, 0xffff0000, v86
	v_lshlrev_b32_e32 v126, 16, v86
	v_and_b32_e32 v135, 0xffff0000, v87
	v_lshlrev_b32_e32 v134, 16, v87
	s_waitcnt vmcnt(6)
	v_lshlrev_b32_e32 v136, 16, v90
	v_and_b32_e32 v137, 0xffff0000, v90
	v_lshlrev_b32_e32 v138, 16, v88
	v_and_b32_e32 v139, 0xffff0000, v88
	v_lshlrev_b32_e32 v140, 16, v89
	v_and_b32_e32 v141, 0xffff0000, v89
	s_waitcnt vmcnt(5)
	v_lshlrev_b32_e32 v142, 16, v94
	v_and_b32_e32 v143, 0xffff0000, v94
	v_lshlrev_b32_e32 v144, 16, v95
	v_and_b32_e32 v145, 0xffff0000, v95
	v_lshlrev_b32_e32 v146, 16, v92
	v_and_b32_e32 v147, 0xffff0000, v92
	v_lshlrev_b32_e32 v148, 16, v93
	v_and_b32_e32 v149, 0xffff0000, v93
	s_waitcnt vmcnt(4)
	v_lshlrev_b32_e32 v150, 16, v98
	v_and_b32_e32 v151, 0xffff0000, v98
	v_lshlrev_b32_e32 v152, 16, v99
	v_and_b32_e32 v153, 0xffff0000, v99
	v_lshlrev_b32_e32 v154, 16, v96
	v_and_b32_e32 v155, 0xffff0000, v96
	v_lshlrev_b32_e32 v156, 16, v97
	v_and_b32_e32 v157, 0xffff0000, v97
	v_lshlrev_b32_e32 v158, 16, v84
	v_and_b32_e32 v159, 0xffff0000, v84
	v_lshlrev_b32_e32 v160, 16, v85
	v_and_b32_e32 v161, 0xffff0000, v85
	v_lshl_add_u64 v[186:187], v[68:69], 0, v[100:101]
	v_lshl_add_u64 v[188:189], v[68:69], 0, v[102:103]
	v_lshl_add_u64 v[190:191], v[68:69], 0, v[104:105]
	v_lshl_add_u64 v[192:193], v[68:69], 0, v[106:107]
	v_lshl_add_u64 v[194:195], v[68:69], 0, v[108:109]
	v_lshl_add_u64 v[196:197], v[68:69], 0, v[110:111]
	v_lshl_add_u64 v[198:199], v[68:69], 0, v[112:113]
	v_lshl_add_u64 v[200:201], v[68:69], 0, v[114:115]
	v_pk_mul_f32 v[84:85], v[126:127], s[4:5] op_sel_hi:[1,0]
	v_pk_mul_f32 v[86:87], v[134:135], s[4:5] op_sel_hi:[1,0]
	v_pk_mul_f32 v[88:89], v[136:137], s[4:5] op_sel_hi:[1,0]
	v_pk_mul_f32 v[92:93], v[138:139], s[4:5] op_sel_hi:[1,0]
	v_pk_mul_f32 v[94:95], v[140:141], s[4:5] op_sel_hi:[1,0]
	v_pk_mul_f32 v[96:97], v[142:143], s[4:5] op_sel_hi:[1,0]
	v_pk_mul_f32 v[98:99], v[144:145], s[4:5] op_sel_hi:[1,0]
	v_pk_mul_f32 v[100:101], v[146:147], s[4:5] op_sel_hi:[1,0]
	v_pk_mul_f32 v[102:103], v[148:149], s[4:5] op_sel_hi:[1,0]
	v_pk_mul_f32 v[104:105], v[150:151], s[4:5] op_sel_hi:[1,0]
	v_pk_mul_f32 v[106:107], v[152:153], s[4:5] op_sel_hi:[1,0]
	v_pk_mul_f32 v[108:109], v[154:155], s[4:5] op_sel_hi:[1,0]
	v_pk_mul_f32 v[110:111], v[156:157], s[4:5] op_sel_hi:[1,0]
	v_pk_mul_f32 v[112:113], v[158:159], s[4:5] op_sel_hi:[1,0]
	v_pk_mul_f32 v[114:115], v[160:161], s[4:5] op_sel_hi:[1,0]
	global_load_dwordx2 v[126:127], v[186:187], off nt
	global_load_dwordx2 v[134:135], v[186:187], off offset:512 nt
	global_load_dwordx2 v[136:137], v[186:187], off offset:1024 nt
	global_load_dwordx2 v[138:139], v[186:187], off offset:1536 nt
	global_load_dwordx2 v[140:141], v[188:189], off nt
	global_load_dwordx2 v[142:143], v[188:189], off offset:512 nt
	global_load_dwordx2 v[144:145], v[188:189], off offset:1024 nt
	global_load_dwordx2 v[146:147], v[188:189], off offset:1536 nt
	global_load_dwordx2 v[148:149], v[190:191], off nt
	global_load_dwordx2 v[150:151], v[190:191], off offset:512 nt
	global_load_dwordx2 v[152:153], v[190:191], off offset:1024 nt
	global_load_dwordx2 v[154:155], v[190:191], off offset:1536 nt
	global_load_dwordx2 v[156:157], v[192:193], off nt
	global_load_dwordx2 v[158:159], v[192:193], off offset:512 nt
	global_load_dwordx2 v[160:161], v[192:193], off offset:1024 nt
	global_load_dwordx2 v[186:187], v[192:193], off offset:1536 nt
	global_load_dwordx2 v[188:189], v[194:195], off nt
	global_load_dwordx2 v[190:191], v[194:195], off offset:512 nt
	s_nop 0
	global_load_dwordx2 v[192:193], v[194:195], off offset:1024 nt
	s_nop 0
	global_load_dwordx2 v[194:195], v[194:195], off offset:1536 nt
	s_nop 0
	global_load_dwordx2 v[202:203], v[196:197], off nt
	global_load_dwordx2 v[204:205], v[196:197], off offset:512 nt
	global_load_dwordx2 v[206:207], v[196:197], off offset:1024 nt
	s_nop 0
	global_load_dwordx2 v[196:197], v[196:197], off offset:1536 nt
	s_nop 0
	global_load_dwordx2 v[208:209], v[198:199], off nt
	global_load_dwordx2 v[210:211], v[198:199], off offset:512 nt
	global_load_dwordx2 v[212:213], v[198:199], off offset:1024 nt
	s_nop 0
	global_load_dwordx2 v[198:199], v[198:199], off offset:1536 nt
	s_nop 0
	global_load_dwordx2 v[214:215], v[200:201], off nt
	global_load_dwordx2 v[216:217], v[200:201], off offset:512 nt
	global_load_dwordx2 v[218:219], v[200:201], off offset:1024 nt
	s_nop 0
	global_load_dwordx2 v[200:201], v[200:201], off offset:1536 nt
	s_waitcnt vmcnt(35)
	v_cvt_pk_f32_fp8_e32 v[162:163], v124
	v_cvt_pk_f32_fp8_sdwa v[164:165], v124 src0_sel:WORD_1
	v_cvt_pk_f32_fp8_e32 v[166:167], v125
	v_cvt_pk_f32_fp8_sdwa v[124:125], v125 src0_sel:WORD_1
	s_waitcnt vmcnt(34)
	v_cvt_pk_f32_fp8_e32 v[168:169], v128
	v_cvt_pk_f32_fp8_sdwa v[170:171], v128 src0_sel:WORD_1
	v_cvt_pk_f32_fp8_e32 v[172:173], v129
	v_cvt_pk_f32_fp8_sdwa v[128:129], v129 src0_sel:WORD_1
	s_waitcnt vmcnt(33)
	v_cvt_pk_f32_fp8_e32 v[174:175], v130
	v_cvt_pk_f32_fp8_sdwa v[176:177], v130 src0_sel:WORD_1
	v_cvt_pk_f32_fp8_e32 v[178:179], v131
	v_cvt_pk_f32_fp8_sdwa v[130:131], v131 src0_sel:WORD_1
	s_waitcnt vmcnt(32)
	v_cvt_pk_f32_fp8_e32 v[180:181], v132
	v_cvt_pk_f32_fp8_sdwa v[182:183], v132 src0_sel:WORD_1
	v_cvt_pk_f32_fp8_e32 v[184:185], v133
	v_cvt_pk_f32_fp8_sdwa v[132:133], v133 src0_sel:WORD_1
	v_pk_add_f32 v[162:163], v[162:163], 0 op_sel_hi:[1,0]
	v_pk_add_f32 v[164:165], v[164:165], 0 op_sel_hi:[1,0]
	v_pk_add_f32 v[166:167], v[166:167], 0 op_sel_hi:[1,0]
	v_pk_add_f32 v[124:125], v[124:125], 0 op_sel_hi:[1,0]
	v_pk_add_f32 v[168:169], v[168:169], 0 op_sel_hi:[1,0]
	v_pk_add_f32 v[170:171], v[170:171], 0 op_sel_hi:[1,0]
	v_pk_add_f32 v[172:173], v[172:173], 0 op_sel_hi:[1,0]
	v_pk_add_f32 v[128:129], v[128:129], 0 op_sel_hi:[1,0]
	v_pk_add_f32 v[174:175], v[174:175], 0 op_sel_hi:[1,0]
	v_pk_add_f32 v[176:177], v[176:177], 0 op_sel_hi:[1,0]
	v_pk_add_f32 v[130:131], v[130:131], 0 op_sel_hi:[1,0]
	v_pk_add_f32 v[180:181], v[180:181], 0 op_sel_hi:[1,0]
	v_pk_add_f32 v[182:183], v[182:183], 0 op_sel_hi:[1,0]
	v_pk_add_f32 v[184:185], v[184:185], 0 op_sel_hi:[1,0]
	v_pk_add_f32 v[132:133], v[132:133], 0 op_sel_hi:[1,0]
	v_pk_add_f32 v[178:179], v[178:179], 0 op_sel_hi:[1,0]
	v_lshlrev_b32_e32 v90, 16, v91
	v_and_b32_e32 v91, 0xffff0000, v91
	v_pk_mul_f32 v[90:91], v[90:91], s[4:5] op_sel_hi:[1,0]
	s_waitcnt vmcnt(31)
	v_cvt_pk_f32_fp8_e32 v[220:221], v126
	v_cvt_pk_f32_fp8_sdwa v[222:223], v126 src0_sel:WORD_1
	v_cvt_pk_f32_fp8_e32 v[224:225], v127
	v_cvt_pk_f32_fp8_sdwa v[126:127], v127 src0_sel:WORD_1
	s_waitcnt vmcnt(30)
	v_cvt_pk_f32_fp8_e32 v[226:227], v134
	v_cvt_pk_f32_fp8_sdwa v[228:229], v134 src0_sel:WORD_1
	v_cvt_pk_f32_fp8_e32 v[230:231], v135
	v_cvt_pk_f32_fp8_sdwa v[134:135], v135 src0_sel:WORD_1
	s_waitcnt vmcnt(29)
	v_cvt_pk_f32_fp8_e32 v[232:233], v136
	v_cvt_pk_f32_fp8_sdwa v[234:235], v136 src0_sel:WORD_1
	v_cvt_pk_f32_fp8_e32 v[236:237], v137
	v_cvt_pk_f32_fp8_sdwa v[136:137], v137 src0_sel:WORD_1
	s_waitcnt vmcnt(28)
	v_cvt_pk_f32_fp8_e32 v[238:239], v138
	v_cvt_pk_f32_fp8_sdwa v[240:241], v138 src0_sel:WORD_1
	v_cvt_pk_f32_fp8_e32 v[242:243], v139
	v_cvt_pk_f32_fp8_sdwa v[138:139], v139 src0_sel:WORD_1
	s_waitcnt vmcnt(27)
	v_cvt_pk_f32_fp8_e32 v[244:245], v140
	v_cvt_pk_f32_fp8_sdwa v[246:247], v140 src0_sel:WORD_1
	s_waitcnt vmcnt(26)
	v_cvt_pk_f32_fp8_e32 v[250:251], v142
	v_pk_add_f32 v[162:163], v[162:163], v[220:221]
	v_cvt_pk_f32_fp8_sdwa v[220:221], v142 src0_sel:WORD_1
	v_pk_add_f32 v[164:165], v[164:165], v[222:223]
	v_cvt_pk_f32_fp8_e32 v[222:223], v143
	v_cvt_pk_f32_fp8_sdwa v[142:143], v143 src0_sel:WORD_1
	v_pk_add_f32 v[166:167], v[166:167], v[224:225]
	s_waitcnt vmcnt(25)
	v_cvt_pk_f32_fp8_e32 v[224:225], v144
	v_pk_add_f32 v[124:125], v[124:125], v[126:127]
	v_cvt_pk_f32_fp8_sdwa v[126:127], v144 src0_sel:WORD_1
	v_cvt_pk_f32_fp8_e32 v[248:249], v141
	v_cvt_pk_f32_fp8_sdwa v[140:141], v141 src0_sel:WORD_1
	v_pk_add_f32 v[168:169], v[168:169], v[226:227]
	v_cvt_pk_f32_fp8_e32 v[226:227], v145
	v_cvt_pk_f32_fp8_sdwa v[144:145], v145 src0_sel:WORD_1
	v_pk_add_f32 v[170:171], v[170:171], v[228:229]
	s_waitcnt vmcnt(24)
	v_cvt_pk_f32_fp8_e32 v[228:229], v146
	v_pk_add_f32 v[172:173], v[172:173], v[230:231]
	v_cvt_pk_f32_fp8_sdwa v[230:231], v146 src0_sel:WORD_1
	v_pk_add_f32 v[128:129], v[128:129], v[134:135]
	v_cvt_pk_f32_fp8_e32 v[134:135], v147
	v_cvt_pk_f32_fp8_sdwa v[146:147], v147 src0_sel:WORD_1
	v_pk_add_f32 v[174:175], v[174:175], v[232:233]
	s_waitcnt vmcnt(23)
	v_cvt_pk_f32_fp8_e32 v[232:233], v148
	v_pk_add_f32 v[176:177], v[176:177], v[234:235]
	v_pk_add_f32 v[130:131], v[130:131], v[136:137]
	s_waitcnt vmcnt(22)
	v_cvt_pk_f32_fp8_e32 v[136:137], v150
	v_pk_add_f32 v[180:181], v[180:181], v[238:239]
	v_cvt_pk_f32_fp8_sdwa v[238:239], v150 src0_sel:WORD_1
	v_pk_add_f32 v[182:183], v[182:183], v[240:241]
	v_cvt_pk_f32_fp8_e32 v[240:241], v151
	v_cvt_pk_f32_fp8_sdwa v[150:151], v151 src0_sel:WORD_1
	v_pk_add_f32 v[184:185], v[184:185], v[242:243]
	s_waitcnt vmcnt(21)
	v_cvt_pk_f32_fp8_e32 v[242:243], v152
	v_pk_add_f32 v[132:133], v[132:133], v[138:139]
	v_cvt_pk_f32_fp8_sdwa v[138:139], v152 src0_sel:WORD_1
	v_pk_add_f32 v[162:163], v[162:163], v[244:245]
	v_cvt_pk_f32_fp8_e32 v[244:245], v153
	v_cvt_pk_f32_fp8_sdwa v[152:153], v153 src0_sel:WORD_1
	v_cvt_pk_f32_fp8_sdwa v[234:235], v148 src0_sel:WORD_1
	v_pk_add_f32 v[164:165], v[164:165], v[246:247]
	s_waitcnt vmcnt(20)
	v_cvt_pk_f32_fp8_e32 v[246:247], v154
	v_pk_add_f32 v[128:129], v[128:129], v[142:143]
	s_waitcnt vmcnt(18)
	v_cvt_pk_f32_fp8_e32 v[142:143], v158
	v_pk_add_f32 v[174:175], v[174:175], v[224:225]
	v_cvt_pk_f32_fp8_sdwa v[224:225], v158 src0_sel:WORD_1
	v_pk_add_f32 v[126:127], v[176:177], v[126:127]
	v_cvt_pk_f32_fp8_e32 v[176:177], v159
	v_cvt_pk_f32_fp8_sdwa v[158:159], v159 src0_sel:WORD_1
	v_pk_add_f32 v[124:125], v[124:125], v[140:141]
	v_cvt_pk_f32_fp8_e32 v[140:141], v155
	v_pk_add_f32 v[168:169], v[168:169], v[250:251]
	v_cvt_pk_f32_fp8_e32 v[250:251], v156
	v_pk_add_f32 v[166:167], v[166:167], v[248:249]
	v_cvt_pk_f32_fp8_sdwa v[248:249], v154 src0_sel:WORD_1
	v_pk_add_f32 v[130:131], v[130:131], v[144:145]
	v_pk_add_f32 v[132:133], v[132:133], v[146:147]
	s_waitcnt vmcnt(16)
	v_cvt_pk_f32_fp8_e32 v[146:147], v187
	v_pk_add_f32 v[162:163], v[162:163], v[232:233]
	s_waitcnt vmcnt(15)
	v_cvt_pk_f32_fp8_e32 v[232:233], v188
	v_pk_add_f32 v[178:179], v[178:179], v[236:237]
	v_cvt_pk_f32_fp8_e32 v[236:237], v149
	v_pk_add_f32 v[170:171], v[170:171], v[220:221]
	v_cvt_pk_f32_fp8_sdwa v[220:221], v156 src0_sel:WORD_1
	v_pk_add_f32 v[180:181], v[180:181], v[228:229]
	v_pk_add_f32 v[128:129], v[128:129], v[150:151]
	v_pk_add_f32 v[130:131], v[130:131], v[152:153]
	s_waitcnt vmcnt(12)
	v_cvt_pk_f32_fp8_e32 v[152:153], v195
	v_pk_add_f32 v[134:135], v[184:185], v[134:135]
	v_pk_add_f32 v[164:165], v[164:165], v[234:235]
	v_cvt_pk_f32_fp8_sdwa v[234:235], v188 src0_sel:WORD_1
	v_pk_add_f32 v[136:137], v[168:169], v[136:137]
	v_pk_add_f32 v[180:181], v[180:181], v[246:247]
	s_waitcnt vmcnt(11)
	v_cvt_pk_f32_fp8_e32 v[246:247], v202
	v_pk_add_f32 v[128:129], v[128:129], v[158:159]
	s_waitcnt vmcnt(8)
	v_cvt_pk_f32_fp8_e32 v[158:159], v197
	v_cvt_pk_f32_fp8_e32 v[228:229], v161
	v_pk_add_f32 v[182:183], v[182:183], v[230:231]
	v_pk_add_f32 v[134:135], v[134:135], v[140:141]
	v_pk_add_f32 v[162:163], v[162:163], v[250:251]
	v_pk_add_f32 v[136:137], v[136:137], v[142:143]
	s_waitcnt vmcnt(7)
	v_cvt_pk_f32_fp8_e32 v[142:143], v208
	v_cvt_pk_f32_fp8_sdwa v[148:149], v149 src0_sel:WORD_1
	v_pk_add_f32 v[172:173], v[172:173], v[222:223]
	v_cvt_pk_f32_fp8_e32 v[222:223], v157
	v_pk_add_f32 v[170:171], v[170:171], v[238:239]
	v_cvt_pk_f32_fp8_e32 v[238:239], v191
	v_pk_add_f32 v[182:183], v[182:183], v[248:249]
	v_cvt_pk_f32_fp8_sdwa v[248:249], v202 src0_sel:WORD_1
	v_pk_add_f32 v[134:135], v[134:135], v[146:147]
	v_pk_add_f32 v[162:163], v[162:163], v[232:233]
	s_waitcnt vmcnt(3)
	v_cvt_pk_f32_fp8_e32 v[232:233], v214
	v_pk_add_f32 v[178:179], v[178:179], v[226:227]
	v_pk_add_f32 v[166:167], v[166:167], v[236:237]
	v_cvt_pk_f32_fp8_e32 v[236:237], v189
	v_pk_add_f32 v[164:165], v[164:165], v[220:221]
	v_pk_add_f32 v[170:171], v[170:171], v[224:225]
	v_cvt_pk_f32_fp8_sdwa v[224:225], v208 src0_sel:WORD_1
	v_pk_add_f32 v[134:135], v[134:135], v[152:153]
	v_cvt_pk_f32_fp8_sdwa v[154:155], v155 src0_sel:WORD_1
	v_cvt_pk_f32_fp8_sdwa v[156:157], v157 src0_sel:WORD_1
	v_pk_add_f32 v[172:173], v[172:173], v[240:241]
	v_pk_add_f32 v[178:179], v[178:179], v[244:245]
	v_cvt_pk_f32_fp8_e32 v[140:141], v203
	v_pk_add_f32 v[164:165], v[164:165], v[234:235]
	v_cvt_pk_f32_fp8_sdwa v[234:235], v214 src0_sel:WORD_1
	v_pk_add_f32 v[134:135], v[134:135], v[158:159]
	v_pk_add_f32 v[158:159], v[162:163], v[246:247]
	v_cvt_pk_f32_fp8_e32 v[226:227], v160
	v_cvt_pk_f32_fp8_sdwa v[144:145], v160 src0_sel:WORD_1
	v_cvt_pk_f32_fp8_sdwa v[160:161], v161 src0_sel:WORD_1
	v_cvt_pk_f32_fp8_sdwa v[188:189], v189 src0_sel:WORD_1
	v_pk_add_f32 v[172:173], v[172:173], v[176:177]
	v_pk_add_f32 v[178:179], v[178:179], v[228:229]
	v_cvt_pk_f32_fp8_e32 v[228:229], v209
	v_pk_add_f32 v[142:143], v[158:159], v[142:143]
	v_pk_add_f32 v[124:125], v[124:125], v[148:149]
	v_cvt_pk_f32_fp8_e32 v[148:149], v190
	v_cvt_pk_f32_fp8_sdwa v[168:169], v190 src0_sel:WORD_1
	v_cvt_pk_f32_fp8_sdwa v[190:191], v191 src0_sel:WORD_1
	v_cvt_pk_f32_fp8_sdwa v[202:203], v203 src0_sel:WORD_1
	v_pk_add_f32 v[166:167], v[166:167], v[222:223]
	v_pk_add_f32 v[172:173], v[172:173], v[238:239]
	v_cvt_pk_f32_fp8_e32 v[238:239], v215
	v_pk_add_f32 v[162:163], v[164:165], v[248:249]
	v_pk_add_f32 v[142:143], v[142:143], v[232:233]
	v_cvt_pk_f32_fp8_sdwa v[208:209], v209 src0_sel:WORD_1
	v_pk_add_f32 v[166:167], v[166:167], v[236:237]
	v_pk_add_f32 v[158:159], v[162:163], v[224:225]
	v_pk_fma_f32 v[92:93], v[142:143], s[2:3], v[92:93] op_sel_hi:[1,0,1]
	v_cvt_pk_f32_fp8_e32 v[230:231], v186
	v_cvt_pk_f32_fp8_sdwa v[184:185], v186 src0_sel:WORD_1
	v_cvt_pk_f32_fp8_sdwa v[186:187], v187 src0_sel:WORD_1
	v_pk_add_f32 v[132:133], v[132:133], v[154:155]
	v_cvt_pk_f32_fp8_e32 v[154:155], v204
	v_pk_add_f32 v[124:125], v[124:125], v[156:157]
	v_cvt_pk_f32_fp8_sdwa v[214:215], v215 src0_sel:WORD_1
	v_pk_add_f32 v[140:141], v[166:167], v[140:141]
	v_pk_add_f32 v[158:159], v[158:159], v[234:235]
	v_add_f32_e32 v67, 0, v92
	v_pk_add_f32 v[130:131], v[130:131], v[160:161]
	v_cvt_pk_f32_fp8_e32 v[160:161], v210
	v_pk_add_f32 v[124:125], v[124:125], v[188:189]
	v_pk_add_f32 v[140:141], v[140:141], v[228:229]
	v_pk_fma_f32 v[94:95], v[158:159], s[2:3], v[94:95] op_sel_hi:[1,0,1]
	v_add_f32_e32 v67, v93, v67
	v_pk_add_f32 v[174:175], v[174:175], v[242:243]
	v_cvt_pk_f32_fp8_sdwa v[146:147], v204 src0_sel:WORD_1
	v_pk_add_f32 v[128:129], v[128:129], v[190:191]
	s_waitcnt vmcnt(2)
	v_cvt_pk_f32_fp8_e32 v[190:191], v216
	v_pk_add_f32 v[124:125], v[124:125], v[202:203]
	v_pk_add_f32 v[140:141], v[140:141], v[238:239]
	v_add_f32_e32 v67, v94, v67
	v_pk_add_f32 v[174:175], v[174:175], v[226:227]
	v_cvt_pk_f32_fp8_sdwa v[226:227], v210 src0_sel:WORD_1
	v_pk_add_f32 v[136:137], v[136:137], v[148:149]
	v_pk_add_f32 v[124:125], v[124:125], v[208:209]
	v_pk_fma_f32 v[88:89], v[140:141], s[2:3], v[88:89] op_sel_hi:[1,0,1]
	v_add_f32_e32 v67, v95, v67
	v_pk_add_f32 v[126:127], v[126:127], v[138:139]
	v_pk_add_f32 v[132:133], v[132:133], v[186:187]
	v_cvt_pk_f32_fp8_e32 v[186:187], v205
	v_cvt_pk_f32_fp8_sdwa v[148:149], v216 src0_sel:WORD_1
	v_pk_add_f32 v[136:137], v[136:137], v[154:155]
	v_pk_add_f32 v[124:125], v[124:125], v[214:215]
	v_add_f32_e32 v67, v88, v67
	v_pk_add_f32 v[126:127], v[126:127], v[144:145]
	v_cvt_pk_f32_fp8_e32 v[144:145], v211
	v_pk_add_f32 v[168:169], v[170:171], v[168:169]
	v_pk_add_f32 v[136:137], v[136:137], v[160:161]
	v_pk_fma_f32 v[90:91], v[124:125], s[2:3], v[90:91] op_sel_hi:[1,0,1]
	v_add_f32_e32 v67, v89, v67
	v_cvt_pk_f32_fp8_e32 v[240:241], v192
	v_cvt_pk_f32_fp8_e32 v[242:243], v193
	v_cvt_pk_f32_fp8_sdwa v[204:205], v205 src0_sel:WORD_1
	v_cvt_pk_f32_fp8_e32 v[170:171], v217
	v_pk_add_f32 v[146:147], v[168:169], v[146:147]
	v_pk_add_f32 v[136:137], v[136:137], v[190:191]
	v_add_f32_e32 v67, v90, v67
	v_cvt_pk_f32_fp8_sdwa v[210:211], v211 src0_sel:WORD_1
	v_pk_add_f32 v[146:147], v[146:147], v[226:227]
	v_pk_fma_f32 v[100:101], v[136:137], s[2:3], v[100:101] op_sel_hi:[1,0,1]
	v_add_f32_e32 v67, v91, v67
	v_cvt_pk_f32_fp8_sdwa v[150:151], v192 src0_sel:WORD_1
	v_cvt_pk_f32_fp8_sdwa v[192:193], v193 src0_sel:WORD_1
	v_cvt_pk_f32_fp8_e32 v[222:223], v206
	v_cvt_pk_f32_fp8_e32 v[250:251], v207
	v_cvt_pk_f32_fp8_sdwa v[216:217], v217 src0_sel:WORD_1
	v_pk_add_f32 v[164:165], v[172:173], v[186:187]
	v_pk_add_f32 v[146:147], v[146:147], v[148:149]
	v_add_f32_e32 v67, v100, v67
	v_pk_add_f32 v[180:181], v[180:181], v[230:231]
	v_cvt_pk_f32_fp8_e32 v[230:231], v212
	v_cvt_pk_f32_fp8_e32 v[152:153], v213
	v_pk_add_f32 v[144:145], v[164:165], v[144:145]
	v_pk_fma_f32 v[102:103], v[146:147], s[2:3], v[102:103] op_sel_hi:[1,0,1]
	v_add_f32_e32 v67, v101, v67
	v_cvt_pk_f32_fp8_sdwa v[156:157], v206 src0_sel:WORD_1
	v_pk_add_f32 v[178:179], v[178:179], v[242:243]
	s_waitcnt vmcnt(1)
	v_cvt_pk_f32_fp8_e32 v[242:243], v218
	v_pk_add_f32 v[174:175], v[174:175], v[240:241]
	v_cvt_pk_f32_fp8_e32 v[240:241], v219
	v_pk_add_f32 v[128:129], v[128:129], v[204:205]
	v_pk_add_f32 v[144:145], v[144:145], v[170:171]
	v_add_f32_e32 v67, v102, v67
	v_pk_add_f32 v[182:183], v[182:183], v[184:185]
	v_cvt_pk_f32_fp8_sdwa v[184:185], v212 src0_sel:WORD_1
	v_pk_add_f32 v[128:129], v[128:129], v[210:211]
	v_pk_fma_f32 v[96:97], v[144:145], s[2:3], v[96:97] op_sel_hi:[1,0,1]
	v_add_f32_e32 v67, v103, v67
	v_pk_add_f32 v[130:131], v[130:131], v[192:193]
	v_cvt_pk_f32_fp8_sdwa v[192:193], v218 src0_sel:WORD_1
	v_pk_add_f32 v[154:155], v[178:179], v[250:251]
	v_pk_add_f32 v[166:167], v[174:175], v[222:223]
	v_pk_add_f32 v[128:129], v[128:129], v[216:217]
	v_add_f32_e32 v67, v96, v67
	v_cvt_pk_f32_fp8_e32 v[138:139], v194
	v_cvt_pk_f32_fp8_sdwa v[244:245], v194 src0_sel:WORD_1
	v_cvt_pk_f32_fp8_sdwa v[194:195], v195 src0_sel:WORD_1
	v_pk_add_f32 v[126:127], v[126:127], v[150:151]
	v_pk_add_f32 v[152:153], v[154:155], v[152:153]
	v_pk_add_f32 v[154:155], v[166:167], v[230:231]
	v_pk_fma_f32 v[98:99], v[128:129], s[2:3], v[98:99] op_sel_hi:[1,0,1]
	v_add_f32_e32 v67, v97, v67
	v_cvt_pk_f32_fp8_sdwa v[206:207], v207 src0_sel:WORD_1
	v_pk_add_f32 v[126:127], v[126:127], v[156:157]
	v_pk_add_f32 v[148:149], v[152:153], v[240:241]
	v_pk_add_f32 v[152:153], v[154:155], v[242:243]
	v_add_f32_e32 v67, v98, v67
	v_cvt_pk_f32_fp8_sdwa v[212:213], v213 src0_sel:WORD_1
	v_pk_add_f32 v[126:127], v[126:127], v[184:185]
	v_pk_fma_f32 v[108:109], v[152:153], s[2:3], v[108:109] op_sel_hi:[1,0,1]
	v_add_f32_e32 v67, v99, v67
	v_cvt_pk_f32_fp8_e32 v[220:221], v196
	v_cvt_pk_f32_fp8_sdwa v[218:219], v219 src0_sel:WORD_1
	v_pk_add_f32 v[126:127], v[126:127], v[192:193]
	v_add_f32_e32 v67, v108, v67
	v_pk_add_f32 v[132:133], v[132:133], v[194:195]
	v_cvt_pk_f32_fp8_e32 v[194:195], v198
	v_pk_fma_f32 v[110:111], v[126:127], s[2:3], v[110:111] op_sel_hi:[1,0,1]
	v_add_f32_e32 v67, v109, v67
	v_cvt_pk_f32_fp8_sdwa v[176:177], v196 src0_sel:WORD_1
	s_waitcnt vmcnt(0)
	v_cvt_pk_f32_fp8_e32 v[150:151], v200
	v_pk_add_f32 v[130:131], v[130:131], v[206:207]
	v_add_f32_e32 v67, v110, v67
	v_cvt_pk_f32_fp8_sdwa v[236:237], v198 src0_sel:WORD_1
	v_pk_add_f32 v[138:139], v[180:181], v[138:139]
	v_pk_add_f32 v[130:131], v[130:131], v[212:213]
	v_pk_fma_f32 v[104:105], v[148:149], s[2:3], v[104:105] op_sel_hi:[1,0,1]
	v_add_f32_e32 v67, v111, v67
	v_cvt_pk_f32_fp8_sdwa v[180:181], v200 src0_sel:WORD_1
	v_pk_add_f32 v[138:139], v[138:139], v[220:221]
	v_pk_add_f32 v[130:131], v[130:131], v[218:219]
	v_add_f32_e32 v67, v104, v67
	v_cvt_pk_f32_fp8_e32 v[188:189], v199
	v_pk_add_f32 v[182:183], v[182:183], v[244:245]
	v_pk_add_f32 v[138:139], v[138:139], v[194:195]
	v_pk_fma_f32 v[106:107], v[130:131], s[2:3], v[106:107] op_sel_hi:[1,0,1]
	v_add_f32_e32 v67, v105, v67
	v_cvt_pk_f32_fp8_sdwa v[196:197], v197 src0_sel:WORD_1
	v_cvt_pk_f32_fp8_e32 v[244:245], v201
	v_pk_add_f32 v[156:157], v[182:183], v[176:177]
	v_pk_add_f32 v[138:139], v[138:139], v[150:151]
	v_add_f32_e32 v67, v106, v67
	v_cvt_pk_f32_fp8_sdwa v[198:199], v199 src0_sel:WORD_1
	v_pk_add_f32 v[156:157], v[156:157], v[236:237]
	v_pk_fma_f32 v[112:113], v[138:139], s[2:3], v[112:113] op_sel_hi:[1,0,1]
	v_add_f32_e32 v67, v107, v67
	v_cvt_pk_f32_fp8_sdwa v[200:201], v201 src0_sel:WORD_1
	v_pk_add_f32 v[150:151], v[156:157], v[180:181]
	v_add_f32_e32 v67, v112, v67
	v_pk_add_f32 v[134:135], v[134:135], v[188:189]
	v_pk_fma_f32 v[114:115], v[150:151], s[2:3], v[114:115] op_sel_hi:[1,0,1]
	v_add_f32_e32 v67, v113, v67
	v_pk_add_f32 v[132:133], v[132:133], v[196:197]
	v_pk_add_f32 v[134:135], v[134:135], v[244:245]
	v_add_f32_e32 v67, v114, v67
	v_pk_add_f32 v[132:133], v[132:133], v[198:199]
	v_pk_fma_f32 v[84:85], v[134:135], s[2:3], v[84:85] op_sel_hi:[1,0,1]
	v_add_f32_e32 v67, v115, v67
	v_pk_add_f32 v[132:133], v[132:133], v[200:201]
	v_add_f32_e32 v67, v84, v67
	v_pk_fma_f32 v[86:87], v[132:133], s[2:3], v[86:87] op_sel_hi:[1,0,1]
	v_add_f32_e32 v67, v85, v67
	v_add_f32_e32 v67, v86, v67
	v_add_f32_e32 v67, v87, v67
	v_mov_b32_e32 v73, v67
	s_nop 1
	v_permlane32_swap_b32_e32 v73, v67
	s_waitcnt lgkmcnt(0)
	v_add_f32_e32 v67, v67, v73
	v_mov_b32_e32 v73, v67
	s_nop 1
	v_permlane16_swap_b32_e32 v73, v67
	s_waitcnt lgkmcnt(0)
	v_add_f32_e32 v67, v67, v73
	s_nop 1
	v_mov_b32_dpp v73, v67 row_ror:8 row_mask:0xf bank_mask:0xf
	s_waitcnt lgkmcnt(0)
	v_add_f32_e32 v67, v67, v73
	s_nop 1
	v_mov_b32_dpp v73, v67 row_shr:4 row_mask:0xf bank_mask:0xa
	v_mov_b32_dpp v73, v67 row_shl:4 row_mask:0xf bank_mask:0x5
	s_waitcnt lgkmcnt(0)
	v_add_f32_e32 v67, v67, v73
	s_nop 1
	v_mov_b32_dpp v73, v67 quad_perm:[2,3,0,1] row_mask:0xf bank_mask:0xf
	s_waitcnt lgkmcnt(0)
	v_add_f32_e32 v67, v67, v73
	s_nop 1
	v_mov_b32_dpp v73, v67 quad_perm:[1,0,3,2] row_mask:0xf bank_mask:0xf
	s_waitcnt lgkmcnt(0)
	v_add_f32_e32 v67, v67, v73
	v_mul_f32_e32 v124, 0x3a000000, v67
	v_pk_add_f32 v[92:93], v[92:93], v[124:125] op_sel_hi:[1,0] neg_lo:[0,1] neg_hi:[0,1]
	v_pk_add_f32 v[94:95], v[94:95], v[124:125] op_sel_hi:[1,0] neg_lo:[0,1] neg_hi:[0,1]
	v_pk_add_f32 v[88:89], v[88:89], v[124:125] op_sel_hi:[1,0] neg_lo:[0,1] neg_hi:[0,1]
	v_pk_add_f32 v[90:91], v[90:91], v[124:125] op_sel_hi:[1,0] neg_lo:[0,1] neg_hi:[0,1]
	v_pk_add_f32 v[100:101], v[100:101], v[124:125] op_sel_hi:[1,0] neg_lo:[0,1] neg_hi:[0,1]
	v_pk_add_f32 v[102:103], v[102:103], v[124:125] op_sel_hi:[1,0] neg_lo:[0,1] neg_hi:[0,1]
	v_pk_add_f32 v[96:97], v[96:97], v[124:125] op_sel_hi:[1,0] neg_lo:[0,1] neg_hi:[0,1]
	v_pk_add_f32 v[98:99], v[98:99], v[124:125] op_sel_hi:[1,0] neg_lo:[0,1] neg_hi:[0,1]
	v_pk_add_f32 v[108:109], v[108:109], v[124:125] op_sel_hi:[1,0] neg_lo:[0,1] neg_hi:[0,1]
	v_pk_add_f32 v[110:111], v[110:111], v[124:125] op_sel_hi:[1,0] neg_lo:[0,1] neg_hi:[0,1]
	v_pk_add_f32 v[104:105], v[104:105], v[124:125] op_sel_hi:[1,0] neg_lo:[0,1] neg_hi:[0,1]
	v_pk_add_f32 v[106:107], v[106:107], v[124:125] op_sel_hi:[1,0] neg_lo:[0,1] neg_hi:[0,1]
	v_pk_add_f32 v[112:113], v[112:113], v[124:125] op_sel_hi:[1,0] neg_lo:[0,1] neg_hi:[0,1]
	v_pk_add_f32 v[114:115], v[114:115], v[124:125] op_sel_hi:[1,0] neg_lo:[0,1] neg_hi:[0,1]
	v_pk_add_f32 v[84:85], v[84:85], v[124:125] op_sel_hi:[1,0] neg_lo:[0,1] neg_hi:[0,1]
	v_pk_add_f32 v[86:87], v[86:87], v[124:125] op_sel_hi:[1,0] neg_lo:[0,1] neg_hi:[0,1]
	v_pk_mul_f32 v[124:125], v[92:93], v[92:93]
	v_pk_mul_f32 v[126:127], v[94:95], v[94:95]
	v_add_f32_e32 v67, v124, v125
	v_add_f32_e32 v67, v126, v67
	v_pk_mul_f32 v[128:129], v[88:89], v[88:89]
	v_add_f32_e32 v67, v127, v67
	v_add_f32_e32 v67, v128, v67
	v_pk_mul_f32 v[130:131], v[90:91], v[90:91]
	v_add_f32_e32 v67, v129, v67
	v_add_f32_e32 v67, v130, v67
	v_pk_mul_f32 v[132:133], v[100:101], v[100:101]
	v_add_f32_e32 v67, v131, v67
	v_add_f32_e32 v67, v132, v67
	v_pk_mul_f32 v[134:135], v[102:103], v[102:103]
	v_add_f32_e32 v67, v133, v67
	v_add_f32_e32 v67, v134, v67
	v_pk_mul_f32 v[136:137], v[96:97], v[96:97]
	v_add_f32_e32 v67, v135, v67
	v_add_f32_e32 v67, v136, v67
	v_pk_mul_f32 v[138:139], v[98:99], v[98:99]
	v_add_f32_e32 v67, v137, v67
	v_add_f32_e32 v67, v138, v67
	v_pk_mul_f32 v[140:141], v[108:109], v[108:109]
	v_add_f32_e32 v67, v139, v67
	v_add_f32_e32 v67, v140, v67
	v_pk_mul_f32 v[142:143], v[110:111], v[110:111]
	v_add_f32_e32 v67, v141, v67
	v_add_f32_e32 v67, v142, v67
	v_pk_mul_f32 v[144:145], v[104:105], v[104:105]
	v_add_f32_e32 v67, v143, v67
	v_add_f32_e32 v67, v144, v67
	v_pk_mul_f32 v[146:147], v[106:107], v[106:107]
	v_add_f32_e32 v67, v145, v67
	v_add_f32_e32 v67, v146, v67
	v_pk_mul_f32 v[148:149], v[112:113], v[112:113]
	v_add_f32_e32 v67, v147, v67
	v_add_f32_e32 v67, v148, v67
	v_pk_mul_f32 v[150:151], v[114:115], v[114:115]
	v_add_f32_e32 v67, v149, v67
	v_add_f32_e32 v67, v150, v67
	v_pk_mul_f32 v[152:153], v[84:85], v[84:85]
	v_add_f32_e32 v67, v151, v67
	v_add_f32_e32 v67, v152, v67
	v_pk_mul_f32 v[154:155], v[86:87], v[86:87]
	v_add_f32_e32 v67, v153, v67
	v_add_f32_e32 v67, v154, v67
	v_add_f32_e32 v67, v155, v67
	v_mov_b32_e32 v73, v67
	s_nop 1
	v_permlane32_swap_b32_e32 v73, v67
	s_waitcnt lgkmcnt(0)
	v_add_f32_e32 v67, v67, v73
	v_mov_b32_e32 v73, v67
	s_nop 1
	v_permlane16_swap_b32_e32 v73, v67
	s_waitcnt lgkmcnt(0)
	v_add_f32_e32 v67, v67, v73
	s_nop 1
	v_mov_b32_dpp v73, v67 row_ror:8 row_mask:0xf bank_mask:0xf
	s_waitcnt lgkmcnt(0)
	v_add_f32_e32 v67, v67, v73
	s_nop 1
	v_mov_b32_dpp v73, v67 row_shr:4 row_mask:0xf bank_mask:0xa
	v_mov_b32_dpp v73, v67 row_shl:4 row_mask:0xf bank_mask:0x5
	s_waitcnt lgkmcnt(0)
	v_add_f32_e32 v67, v67, v73
	s_nop 1
	v_mov_b32_dpp v73, v67 quad_perm:[2,3,0,1] row_mask:0xf bank_mask:0xf
	s_waitcnt lgkmcnt(0)
	v_add_f32_e32 v67, v67, v73
	s_nop 1
	v_mov_b32_dpp v73, v67 quad_perm:[1,0,3,2] row_mask:0xf bank_mask:0xf
	s_waitcnt lgkmcnt(0)
	v_add_f32_e32 v67, v67, v73
	v_fmamk_f32 v67, v67, 0x3a000000, v123
	v_mul_f32_e32 v73, 0x4b800000, v67
	v_cmp_gt_f32_e32 vcc, s6, v67
	s_nop 1
	v_cndmask_b32_e32 v67, v67, v73, vcc
	v_rsq_f32_e32 v67, v67
	s_nop 0
	v_mul_f32_e32 v73, 0x45800000, v67
	v_cndmask_b32_e32 v124, v67, v73, vcc
	v_pk_mul_f32 v[92:93], v[92:93], v[124:125] op_sel_hi:[1,0]
	v_pk_mul_f32 v[94:95], v[94:95], v[124:125] op_sel_hi:[1,0]
	v_pk_mul_f32 v[88:89], v[88:89], v[124:125] op_sel_hi:[1,0]
	v_pk_mul_f32 v[90:91], v[90:91], v[124:125] op_sel_hi:[1,0]
	v_pk_mul_f32 v[100:101], v[100:101], v[124:125] op_sel_hi:[1,0]
	v_pk_mul_f32 v[102:103], v[102:103], v[124:125] op_sel_hi:[1,0]
	v_pk_mul_f32 v[96:97], v[96:97], v[124:125] op_sel_hi:[1,0]
	v_pk_mul_f32 v[98:99], v[98:99], v[124:125] op_sel_hi:[1,0]
	v_pk_mul_f32 v[108:109], v[108:109], v[124:125] op_sel_hi:[1,0]
	v_pk_mul_f32 v[110:111], v[110:111], v[124:125] op_sel_hi:[1,0]
	v_pk_mul_f32 v[104:105], v[104:105], v[124:125] op_sel_hi:[1,0]
	v_pk_mul_f32 v[106:107], v[106:107], v[124:125] op_sel_hi:[1,0]
	v_pk_mul_f32 v[112:113], v[112:113], v[124:125] op_sel_hi:[1,0]
	v_pk_mul_f32 v[114:115], v[114:115], v[124:125] op_sel_hi:[1,0]
	v_pk_mul_f32 v[126:127], v[84:85], v[124:125] op_sel_hi:[1,0]
	v_pk_mul_f32 v[124:125], v[86:87], v[124:125] op_sel_hi:[1,0]
	v_pk_fma_f32 v[86:87], v[62:63], v[94:95], v[58:59]
	v_pk_fma_f32 v[84:85], v[60:61], v[92:93], v[56:57]
	v_pk_fma_f32 v[90:91], v[54:55], v[90:91], v[50:51]
	v_pk_fma_f32 v[88:89], v[52:53], v[88:89], v[48:49]
	v_pk_fma_f32 v[94:95], v[46:47], v[102:103], v[42:43]
	v_pk_fma_f32 v[92:93], v[44:45], v[100:101], v[40:41]
	v_pk_fma_f32 v[98:99], v[38:39], v[98:99], v[34:35]
	v_pk_fma_f32 v[96:97], v[36:37], v[96:97], v[32:33]
	v_pk_fma_f32 v[102:103], v[30:31], v[110:111], v[26:27]
	v_pk_fma_f32 v[100:101], v[28:29], v[108:109], v[24:25]
	v_pk_fma_f32 v[106:107], v[22:23], v[106:107], v[18:19]
	v_pk_fma_f32 v[104:105], v[20:21], v[104:105], v[16:17]
	v_pk_fma_f32 v[110:111], v[14:15], v[114:115], v[10:11]
	v_pk_fma_f32 v[108:109], v[12:13], v[112:113], v[8:9]
	v_pk_fma_f32 v[114:115], v[6:7], v[124:125], v[2:3]
	v_pk_fma_f32 v[112:113], v[4:5], v[126:127], v[0:1]
	global_store_dwordx4 v[82:83], v[84:87], off nt
	global_store_dwordx4 v[82:83], v[88:91], off offset:16 nt
	global_store_dwordx4 v[82:83], v[92:95], off offset:2048 nt
	global_store_dwordx4 v[82:83], v[96:99], off offset:2064 nt
	global_store_dwordx4 v[80:81], v[100:103], off nt
	global_store_dwordx4 v[80:81], v[104:107], off offset:16 nt
	global_store_dwordx4 v[78:79], v[108:111], off nt
	global_store_dwordx4 v[78:79], v[112:115], off offset:16 nt
	s_andn2_b64 exec, exec, s[0:1]
	s_cbranch_execnz .LBB0_1734
